# B3 first row-pair block batches window loads up to 9 deep using 3 more dead VGPR pairs; otherwise as previous version
# speedup vs baseline: 1.0041x; 1.0041x over previous
.LBB0_1336:
	s_add_i32 s18, s2, s65
	s_max_i32 s13, s18, 4
	s_add_i32 s14, s13, -4
	s_mov_b32 s15, s60
	s_max_i32 s13, s18, 3
	s_lshl_b64 s[36:37], s[14:15], 12
	s_add_i32 s14, s13, -3
	s_max_i32 s13, s18, 2
	s_lshl_b64 s[52:53], s[14:15], 12
	s_add_i32 s14, s13, -2
	s_max_i32 s13, s18, 1
	s_lshl_b64 s[50:51], s[14:15], 12
	s_add_i32 s14, s13, -1
	s_and_b32 s12, s18, 0x7fc
	s_lshl_b64 s[26:27], s[14:15], 12
	s_max_i32 s14, s18, 0
	s_max_i32 s13, s18, -1
	s_lshl_b64 s[24:25], s[14:15], 12
	s_add_i32 s14, s13, 1
	s_min_u32 s13, s12, 15
	s_add_i32 s13, s13, 1
	s_lshl_b64 s[78:79], s[14:15], 12
	s_min_u32 s14, s12, 14
	v_cvt_f32_ubyte0_e32 v0, s13
	s_add_i32 s16, s14, 2
	v_div_scale_f32 v1, s[14:15], v0, v0, 1.0
	v_rcp_f32_e32 v2, v1
	s_min_u32 s13, s12, 7
	s_add_i32 s13, s13, 1
	s_waitcnt lgkmcnt(0)
	v_fma_f32 v3, -v1, v2, 1.0
	v_fmac_f32_e32 v2, v3, v2
	v_div_scale_f32 v3, vcc, 1.0, v0, 1.0
	v_mul_f32_e32 v4, v3, v2
	v_fma_f32 v5, -v1, v4, v3
	v_fmac_f32_e32 v4, v5, v2
	v_fma_f32 v1, -v1, v4, v3
	v_div_fmas_f32 v1, v1, v2, v4
	v_div_fixup_f32 v92, v1, v0, 1.0
	v_cvt_f32_ubyte0_e32 v0, s16
	v_div_scale_f32 v1, s[14:15], v0, v0, 1.0
	v_rcp_f32_e32 v2, v1
	s_min_u32 s14, s12, 6
	s_add_i32 s16, s14, 2
	s_waitcnt lgkmcnt(0)
	v_fma_f32 v3, -v1, v2, 1.0
	v_fmac_f32_e32 v2, v3, v2
	v_div_scale_f32 v3, vcc, 1.0, v0, 1.0
	v_mul_f32_e32 v4, v3, v2
	v_fma_f32 v5, -v1, v4, v3
	v_fmac_f32_e32 v4, v5, v2
	v_fma_f32 v1, -v1, v4, v3
	v_div_fmas_f32 v1, v1, v2, v4
	v_div_fixup_f32 v94, v1, v0, 1.0
	v_cvt_f32_ubyte0_e32 v0, s13
	v_div_scale_f32 v1, s[14:15], v0, v0, 1.0
	v_rcp_f32_e32 v2, v1
	s_min_u32 s13, s12, 3
	s_add_i32 s13, s13, 1
	s_barrier
	v_fma_f32 v3, -v1, v2, 1.0
	v_fmac_f32_e32 v2, v3, v2
	v_div_scale_f32 v3, vcc, 1.0, v0, 1.0
	v_mul_f32_e32 v4, v3, v2
	v_fma_f32 v5, -v1, v4, v3
	v_fmac_f32_e32 v4, v5, v2
	v_fma_f32 v1, -v1, v4, v3
	v_div_fmas_f32 v1, v1, v2, v4
	v_div_fixup_f32 v8, v1, v0, 1.0
	v_cvt_f32_ubyte0_e32 v0, s16
	v_div_scale_f32 v1, s[14:15], v0, v0, 1.0
	v_rcp_f32_e32 v2, v1
	s_min_u32 s14, s12, 2
	s_add_i32 s16, s14, 2
	v_fma_f32 v3, -v1, v2, 1.0
	v_fmac_f32_e32 v2, v3, v2
	v_div_scale_f32 v3, vcc, 1.0, v0, 1.0
	v_mul_f32_e32 v4, v3, v2
	v_fma_f32 v5, -v1, v4, v3
	v_fmac_f32_e32 v4, v5, v2
	v_fma_f32 v1, -v1, v4, v3
	v_div_fmas_f32 v1, v1, v2, v4
	v_div_fixup_f32 v10, v1, v0, 1.0
	v_cvt_f32_ubyte0_e32 v0, s13
	v_div_scale_f32 v1, s[14:15], v0, v0, 1.0
	v_rcp_f32_e32 v2, v1
	v_mov_b32_e32 v27, s7
	s_max_i32 s0, s18, 15
	s_add_i32 s0, s0, -15
	v_fma_f32 v3, -v1, v2, 1.0
	v_fmac_f32_e32 v2, v3, v2
	v_div_scale_f32 v3, vcc, 1.0, v0, 1.0
	v_mul_f32_e32 v4, v3, v2
	v_fma_f32 v5, -v1, v4, v3
	v_fmac_f32_e32 v4, v5, v2
	v_fma_f32 v1, -v1, v4, v3
	v_div_fmas_f32 v1, v1, v2, v4
	v_div_fixup_f32 v4, v1, v0, 1.0
	v_cvt_f32_ubyte0_e32 v0, s16
	v_div_scale_f32 v1, s[14:15], v0, v0, 1.0
	v_rcp_f32_e32 v2, v1
	s_mov_b32 s1, s60
	s_lshl_b64 s[76:77], s[0:1], 12
	s_max_i32 s0, s18, 14
	v_fma_f32 v3, -v1, v2, 1.0
	v_fmac_f32_e32 v2, v3, v2
	v_div_scale_f32 v3, vcc, 1.0, v0, 1.0
	v_mul_f32_e32 v5, v3, v2
	v_fma_f32 v6, -v1, v5, v3
	v_fmac_f32_e32 v5, v6, v2
	v_fma_f32 v1, -v1, v5, v3
	v_div_fmas_f32 v1, v1, v2, v5
	v_mov_b32_e32 v5, v21
	v_div_fixup_f32 v6, v1, v0, 1.0
	ds_read_b64 v[2:3], v27 offset:56
	ds_read_b32 v12, v27 offset:64
	v_lshlrev_b32_e32 v0, 2, v5
	v_ashrrev_i32_e32 v1, 31, v0
	v_lshlrev_b64 v[84:85], 1, v[0:1]
	v_lshl_add_u64 v[0:1], s[92:93], 0, v[84:85]
	v_lshl_add_u64 v[236:237], v[0:1], 0, s[78:79]
	global_load_dwordx2 v[236:237], v[236:237], off
	v_lshl_add_u64 v[238:239], v[0:1], 0, s[26:27]
	global_load_dwordx2 v[238:239], v[238:239], off
	v_lshl_add_u64 v[240:241], v[0:1], 0, s[24:25]
	global_load_dwordx2 v[240:241], v[240:241], off
	s_nop 0
	s_nop 0
	s_nop 0
	s_nop 0
	s_nop 0
	s_add_i32 s0, s0, -14
	s_nop 0
	s_lshl_b64 s[10:11], s[0:1], 12
	s_max_i32 s0, s18, 13
	s_add_i32 s0, s0, -13
	s_lshl_b64 s[8:9], s[0:1], 12
	s_max_i32 s0, s18, 12
	s_add_i32 s0, s0, -12
	s_lshl_b64 s[44:45], s[0:1], 12
	s_max_i32 s0, s18, 11
	s_add_i32 s0, s0, -11
	s_lshl_b64 s[48:49], s[0:1], 12
	s_max_i32 s0, s18, 10
	s_add_i32 s0, s0, -10
	s_lshl_b64 s[46:47], s[0:1], 12
	s_max_i32 s0, s18, 9
	s_add_i32 s0, s0, -9
	s_lshl_b64 s[30:31], s[0:1], 12
	s_max_i32 s0, s18, 8
	s_max_i32 s2, s18, 6
	s_add_i32 s0, s0, -8
	s_add_i32 s2, s2, -6
	s_mov_b32 s3, s60
	s_lshl_b64 s[28:29], s[0:1], 12
	s_max_i32 s0, s18, 7
	s_lshl_b64 s[42:43], s[2:3], 12
	s_max_i32 s2, s18, 5
	s_add_i32 s0, s0, -7
	s_add_i32 s2, s2, -5
	s_lshl_b64 s[0:1], s[0:1], 12
	s_lshl_b64 s[2:3], s[2:3], 12
	s_cmp_eq_u32 s12, 0
	s_cselect_b32 s54, 1.0, 0.5
	s_ashr_i32 s19, s18, 31
	s_lshl_b64 s[12:13], s[18:19], 12
	s_add_u32 s22, s4, s12
	s_addc_u32 s23, s5, s13
	s_or_b32 s16, s18, 1
	s_ashr_i32 s17, s16, 31
	s_lshl_b64 s[12:13], s[16:17], 12
	s_add_u32 s20, s4, s12
	s_addc_u32 s21, s5, s13
	s_add_i32 s17, 0, 0x12000
	s_add_u32 vcc_lo, s92, s78
	s_addc_u32 vcc_hi, s93, s79
	s_add_u32 s26, s92, s26
	s_addc_u32 s27, s93, s27
	s_add_u32 s24, s92, s24
	s_addc_u32 s25, s93, s25
	s_add_u32 s52, s92, s52
	s_addc_u32 s53, s93, s53
	s_add_u32 s50, s92, s50
	s_addc_u32 s51, s93, s51
	s_nop 0
	s_waitcnt vmcnt(2)
	v_lshlrev_b32_e32 v80, 16, v236
	v_and_b32_e32 v81, 0xffff0000, v236
	s_nop 0
	s_waitcnt vmcnt(1)
	v_lshlrev_b32_e32 v90, 16, v238
	v_and_b32_e32 v91, 0xffff0000, v238
	v_lshlrev_b32_e32 v88, 16, v239
	v_and_b32_e32 v89, 0xffff0000, v239
	s_waitcnt lgkmcnt(1)
	v_pk_fma_f32 v[96:97], v[2:3], v[90:91], 0 op_sel_hi:[0,1,0]
	v_pk_fma_f32 v[98:99], v[2:3], v[88:89], 0 op_sel_hi:[0,1,0]
	s_nop 0
	s_waitcnt vmcnt(0)
	v_lshlrev_b32_e32 v100, 16, v240
	v_and_b32_e32 v101, 0xffff0000, v240
	v_lshlrev_b32_e32 v0, 16, v241
	v_and_b32_e32 v1, 0xffff0000, v241
	v_pk_mul_f32 v[102:103], v[2:3], v[0:1] op_sel:[1,0]
	v_pk_fma_f32 v[0:1], v[2:3], v[0:1], v[98:99] op_sel:[1,0,0]
	v_pk_fma_f32 v[96:97], v[2:3], v[100:101], v[96:97] op_sel:[1,0,0]
	v_lshlrev_b32_e32 v14, 16, v237
	v_and_b32_e32 v15, 0xffff0000, v237
	v_pk_mul_f32 v[104:105], v[2:3], v[100:101] op_sel:[1,0]
	v_pk_fma_f32 v[90:91], v[2:3], v[90:91], v[96:97] op_sel_hi:[0,1,1] neg_lo:[1,0,0] neg_hi:[1,0,0]
	v_pk_fma_f32 v[2:3], v[2:3], v[88:89], v[0:1] op_sel_hi:[0,1,1] neg_lo:[1,0,0] neg_hi:[1,0,0]
	s_waitcnt lgkmcnt(0)
	v_pk_mul_f32 v[82:83], v[12:13], v[14:15] op_sel_hi:[0,1]
	v_pk_mul_f32 v[86:87], v[12:13], v[80:81] op_sel_hi:[0,1]
	v_pk_fma_f32 v[2:3], v[12:13], v[14:15], v[2:3] op_sel_hi:[0,1,1]
	v_pk_fma_f32 v[12:13], v[12:13], v[80:81], v[90:91] op_sel_hi:[0,1,1]
	v_lshl_add_u64 v[236:237], s[22:23], 0, v[84:85]
	global_load_dwordx2 v[236:237], v[236:237], off
	v_lshl_add_u64 v[238:239], s[20:21], 0, v[84:85]
	global_load_dwordx2 v[238:239], v[238:239], off
	v_lshl_add_u64 v[88:89], s[22:23], 0, v[84:85]
	v_pk_fma_f32 v[12:13], v[12:13], 0.5, v[86:87] op_sel_hi:[1,0,1] neg_lo:[0,0,1] neg_hi:[0,0,1]
	s_nop 0
	v_pk_fma_f32 v[80:81], s[54:55], v[0:1], v[102:103] op_sel_hi:[0,1,1] neg_lo:[0,0,1] neg_hi:[0,0,1]
	v_lshl_add_u32 v0, v5, 4, s17
	v_pk_fma_f32 v[14:15], v[2:3], 0.5, v[82:83] op_sel_hi:[1,0,1] neg_lo:[0,0,1] neg_hi:[0,0,1]
	ds_read_b128 v[0:3], v0
	v_pk_fma_f32 v[82:83], s[54:55], v[96:97], v[104:105] op_sel_hi:[0,1,1] neg_lo:[0,0,1] neg_hi:[0,0,1]
	s_nop 0
	s_waitcnt vmcnt(1)
	v_lshlrev_b32_e32 v90, 16, v236
	v_and_b32_e32 v91, 0xffff0000, v236
	s_waitcnt lgkmcnt(0)
	v_pk_fma_f32 v[82:83], v[0:1], v[82:83], v[90:91]
	v_lshl_add_u64 v[90:91], s[20:21], 0, v[84:85]
	s_nop 0
	v_lshlrev_b32_e32 v86, 16, v237
	v_and_b32_e32 v87, 0xffff0000, v237
	v_pk_fma_f32 v[80:81], v[2:3], v[80:81], v[86:87]
	s_nop 0
	s_waitcnt vmcnt(0)
	v_lshlrev_b32_e32 v86, 16, v238
	v_and_b32_e32 v87, 0xffff0000, v238
	v_lshlrev_b32_e32 v84, 16, v239
	v_and_b32_e32 v85, 0xffff0000, v239
	v_pk_fma_f32 v[86:87], v[0:1], v[12:13], v[86:87]
	v_cvt_pk_bf16_f32 v0, v82, v83
	v_cvt_pk_bf16_f32 v1, v80, v81
	v_pk_fma_f32 v[84:85], v[2:3], v[14:15], v[84:85]
	v_cvt_pk_bf16_f32 v2, v86, v87
	s_nop 0
	v_cvt_pk_bf16_f32 v3, v84, v85
	global_store_dwordx2 v[88:89], v[0:1], off
	global_store_dwordx2 v[90:91], v[2:3], off
	v_mov_b32_e32 v0, v21
	ds_read_b64 v[2:3], v27 offset:56
	ds_read_b32 v12, v27 offset:64
	v_lshlrev_b32_e32 v88, 2, v0
	v_add_u32_e32 v0, 0x100, v88
	v_ashrrev_i32_e32 v1, 31, v0
	v_lshlrev_b64 v[14:15], 1, v[0:1]
	v_lshl_add_u64 v[236:237], vcc, 0, v[14:15]
	global_load_dwordx2 v[236:237], v[236:237], off
	v_lshl_add_u64 v[238:239], s[26:27], 0, v[14:15]
	global_load_dwordx2 v[238:239], v[238:239], off
	v_lshl_add_u64 v[240:241], s[24:25], 0, v[14:15]
	global_load_dwordx2 v[240:241], v[240:241], off
	s_nop 0
	s_nop 0
	s_nop 0
	s_nop 0
	s_nop 0
	v_ashrrev_i32_e32 v89, 31, v88
	s_nop 0
	v_lshl_add_u32 v0, v0, 2, s17
	s_nop 0
	s_waitcnt vmcnt(2)
	v_lshlrev_b32_e32 v96, 16, v236
	v_and_b32_e32 v97, 0xffff0000, v236
	s_nop 0
	s_waitcnt vmcnt(1)
	v_lshlrev_b32_e32 v104, 16, v238
	v_and_b32_e32 v105, 0xffff0000, v238
	v_lshlrev_b32_e32 v102, 16, v239
	v_and_b32_e32 v103, 0xffff0000, v239
	s_waitcnt lgkmcnt(1)
	v_pk_fma_f32 v[106:107], v[2:3], v[104:105], 0 op_sel_hi:[0,1,0]
	v_pk_fma_f32 v[108:109], v[2:3], v[102:103], 0 op_sel_hi:[0,1,0]
	s_nop 0
	s_waitcnt vmcnt(0)
	v_lshlrev_b32_e32 v110, 16, v240
	v_and_b32_e32 v111, 0xffff0000, v240
	v_lshlrev_b32_e32 v14, 16, v241
	v_and_b32_e32 v15, 0xffff0000, v241
	v_pk_fma_f32 v[108:109], v[2:3], v[14:15], v[108:109] op_sel:[1,0,0]
	v_pk_fma_f32 v[106:107], v[2:3], v[110:111], v[106:107] op_sel:[1,0,0]
	v_lshlrev_b32_e32 v90, 16, v237
	v_and_b32_e32 v91, 0xffff0000, v237
	v_pk_mul_f32 v[112:113], v[2:3], v[14:15] op_sel:[1,0]
	v_pk_mul_f32 v[114:115], v[2:3], v[110:111] op_sel:[1,0]
	v_pk_fma_f32 v[14:15], v[2:3], v[104:105], v[106:107] op_sel_hi:[0,1,1] neg_lo:[1,0,0] neg_hi:[1,0,0]
	v_pk_fma_f32 v[2:3], v[2:3], v[102:103], v[108:109] op_sel_hi:[0,1,1] neg_lo:[1,0,0] neg_hi:[1,0,0]
	s_waitcnt lgkmcnt(0)
	v_pk_mul_f32 v[98:99], v[12:13], v[90:91] op_sel_hi:[0,1]
	v_pk_fma_f32 v[2:3], v[12:13], v[90:91], v[2:3] op_sel_hi:[0,1,1]
	v_pk_mul_f32 v[100:101], v[12:13], v[96:97] op_sel_hi:[0,1]
	v_pk_fma_f32 v[12:13], v[12:13], v[96:97], v[14:15] op_sel_hi:[0,1,1]
	v_pk_fma_f32 v[14:15], v[2:3], 0.5, v[98:99] op_sel_hi:[1,0,1] neg_lo:[0,0,1] neg_hi:[0,0,1]
	v_lshlrev_b64 v[98:99], 1, v[88:89]
	v_pk_fma_f32 v[12:13], v[12:13], 0.5, v[100:101] op_sel_hi:[1,0,1] neg_lo:[0,0,1] neg_hi:[0,0,1]
	v_lshl_add_u64 v[236:237], s[22:23], 0, v[98:99]
	global_load_dwordx2 v[236:237], v[236:237], off offset:512
	v_lshl_add_u64 v[238:239], s[20:21], 0, v[98:99]
	global_load_dwordx2 v[238:239], v[238:239], off offset:512
	v_lshl_add_u64 v[100:101], s[22:23], 0, v[98:99]
	s_nop 0
	ds_read_b128 v[0:3], v0
	v_pk_fma_f32 v[90:91], s[54:55], v[106:107], v[114:115] op_sel_hi:[0,1,1] neg_lo:[0,0,1] neg_hi:[0,0,1]
	v_pk_fma_f32 v[96:97], s[54:55], v[108:109], v[112:113] op_sel_hi:[0,1,1] neg_lo:[0,0,1] neg_hi:[0,0,1]
	s_nop 0
	s_waitcnt vmcnt(1)
	v_lshlrev_b32_e32 v102, 16, v236
	v_and_b32_e32 v103, 0xffff0000, v236
	v_lshlrev_b32_e32 v88, 16, v237
	v_and_b32_e32 v89, 0xffff0000, v237
	s_waitcnt lgkmcnt(0)
	v_pk_fma_f32 v[90:91], v[0:1], v[90:91], v[102:103]
	v_lshl_add_u64 v[102:103], s[20:21], 0, v[98:99]
	v_pk_fma_f32 v[88:89], v[2:3], v[96:97], v[88:89]
	s_nop 0
	s_nop 0
	s_waitcnt vmcnt(0)
	v_lshlrev_b32_e32 v98, 16, v238
	v_and_b32_e32 v99, 0xffff0000, v238
	v_lshlrev_b32_e32 v96, 16, v239
	v_and_b32_e32 v97, 0xffff0000, v239
	v_pk_fma_f32 v[98:99], v[0:1], v[12:13], v[98:99]
	v_cvt_pk_bf16_f32 v0, v90, v91
	v_cvt_pk_bf16_f32 v1, v88, v89
	v_pk_fma_f32 v[96:97], v[2:3], v[14:15], v[96:97]
	v_cvt_pk_bf16_f32 v2, v98, v99
	s_nop 0
	v_cvt_pk_bf16_f32 v3, v96, v97
	global_store_dwordx2 v[100:101], v[0:1], off offset:512
	global_store_dwordx2 v[102:103], v[2:3], off offset:512
	v_mov_b32_e32 v0, v21
	s_nop 0
	v_lshlrev_b32_e32 v100, 2, v0
	v_add_u32_e32 v102, 0x200, v100
	v_ashrrev_i32_e32 v103, 31, v102
	v_lshlrev_b64 v[14:15], 1, v[102:103]
	v_lshl_add_u64 v[236:237], vcc, 0, v[14:15]
	global_load_dwordx2 v[236:237], v[236:237], off
	v_lshl_add_u64 v[238:239], s[52:53], 0, v[14:15]
	global_load_dwordx2 v[238:239], v[238:239], off
	v_lshl_add_u64 v[240:241], s[50:51], 0, v[14:15]
	global_load_dwordx2 v[240:241], v[240:241], off
	v_lshl_add_u64 v[242:243], s[26:27], 0, v[14:15]
	global_load_dwordx2 v[242:243], v[242:243], off
	v_lshl_add_u64 v[244:245], s[24:25], 0, v[14:15]
	global_load_dwordx2 v[244:245], v[244:245], off
	s_nop 0
	s_nop 0
	ds_read_b128 v[0:3], v27 offset:48
	ds_read_b32 v12, v27 offset:64
	s_nop 0
	s_nop 0
	s_nop 0
	v_ashrrev_i32_e32 v101, 31, v100
	s_nop 0
	s_nop 0
	s_waitcnt vmcnt(3)
	v_lshlrev_b32_e32 v114, 16, v238
	v_and_b32_e32 v115, 0xffff0000, v238
	v_lshlrev_b32_e32 v112, 16, v239
	v_and_b32_e32 v113, 0xffff0000, v239
	s_waitcnt lgkmcnt(1)
	v_pk_fma_f32 v[118:119], v[0:1], v[112:113], 0 op_sel_hi:[0,1,0]
	s_nop 0
	s_waitcnt vmcnt(2)
	v_lshlrev_b32_e32 v122, 16, v240
	v_and_b32_e32 v123, 0xffff0000, v240
	v_lshlrev_b32_e32 v120, 16, v241
	v_and_b32_e32 v121, 0xffff0000, v241
	v_pk_fma_f32 v[118:119], v[0:1], v[120:121], v[118:119] op_sel:[1,0,0]
	s_nop 0
	s_nop 0
	s_nop 0
	s_nop 0
	v_pk_fma_f32 v[116:117], v[0:1], v[114:115], 0 op_sel_hi:[0,1,0]
	v_pk_fma_f32 v[116:117], v[0:1], v[122:123], v[116:117] op_sel:[1,0,0]
	v_lshlrev_b32_e32 v106, 16, v236
	v_and_b32_e32 v107, 0xffff0000, v236
	v_lshlrev_b32_e32 v104, 16, v237
	v_and_b32_e32 v105, 0xffff0000, v237
	s_waitcnt lgkmcnt(0)
	v_pk_mul_f32 v[108:109], v[12:13], v[104:105] op_sel_hi:[0,1]
	v_pk_mul_f32 v[110:111], v[12:13], v[106:107] op_sel_hi:[0,1]
	s_nop 0
	s_waitcnt vmcnt(1)
	v_lshlrev_b32_e32 v122, 16, v242
	v_and_b32_e32 v123, 0xffff0000, v242
	v_lshlrev_b32_e32 v120, 16, v243
	v_and_b32_e32 v121, 0xffff0000, v243
	v_pk_fma_f32 v[116:117], v[2:3], v[122:123], v[116:117] op_sel_hi:[0,1,1]
	v_pk_fma_f32 v[118:119], v[2:3], v[120:121], v[118:119] op_sel_hi:[0,1,1]
	s_nop 0
	s_waitcnt vmcnt(0)
	v_lshlrev_b32_e32 v120, 16, v244
	v_and_b32_e32 v121, 0xffff0000, v244
	v_lshlrev_b32_e32 v14, 16, v245
	v_and_b32_e32 v15, 0xffff0000, v245
	v_mov_b32_e32 v2, v3
	v_pk_mul_f32 v[122:123], v[2:3], v[14:15] op_sel_hi:[0,1]
	v_pk_mul_f32 v[124:125], v[2:3], v[120:121] op_sel_hi:[0,1]
	v_pk_fma_f32 v[118:119], v[2:3], v[14:15], v[118:119] op_sel_hi:[0,1,1]
	v_pk_fma_f32 v[2:3], v[2:3], v[120:121], v[116:117] op_sel_hi:[0,1,1]
	v_pk_fma_f32 v[14:15], v[0:1], v[114:115], v[2:3] op_sel_hi:[0,1,1] neg_lo:[1,0,0] neg_hi:[1,0,0]
	v_pk_fma_f32 v[0:1], v[0:1], v[112:113], v[118:119] op_sel_hi:[0,1,1] neg_lo:[1,0,0] neg_hi:[1,0,0]
	v_pk_fma_f32 v[0:1], v[12:13], v[104:105], v[0:1] op_sel_hi:[0,1,1]
	v_pk_fma_f32 v[12:13], v[12:13], v[106:107], v[14:15] op_sel_hi:[0,1,1]
	v_pk_fma_f32 v[12:13], v[6:7], v[12:13], v[110:111] op_sel_hi:[0,1,1] neg_lo:[0,0,1] neg_hi:[0,0,1]
	v_lshlrev_b64 v[110:111], 1, v[100:101]
	v_pk_fma_f32 v[14:15], v[6:7], v[0:1], v[108:109] op_sel_hi:[0,1,1] neg_lo:[0,0,1] neg_hi:[0,0,1]
	v_lshl_add_u64 v[108:109], s[22:23], 0, v[110:111]
	global_load_dwordx2 v[100:101], v[108:109], off offset:1024
	v_lshl_add_u32 v0, v102, 2, s17
	v_pk_fma_f32 v[104:105], v[4:5], v[2:3], v[124:125] op_sel_hi:[0,1,1] neg_lo:[0,0,1] neg_hi:[0,0,1]
	ds_read_b128 v[0:3], v0
	v_lshl_add_u64 v[110:111], s[20:21], 0, v[110:111]
	v_pk_fma_f32 v[106:107], v[4:5], v[118:119], v[122:123] op_sel_hi:[0,1,1] neg_lo:[0,0,1] neg_hi:[0,0,1]
	s_nop 0
	s_waitcnt vmcnt(0)
	v_lshlrev_b32_e32 v102, 16, v100
	v_and_b32_e32 v103, 0xffff0000, v100
	s_waitcnt lgkmcnt(0)
	v_pk_fma_f32 v[102:103], v[0:1], v[104:105], v[102:103]
	global_load_dwordx2 v[104:105], v[110:111], off offset:1024
	v_lshlrev_b32_e32 v100, 16, v101
	v_and_b32_e32 v101, 0xffff0000, v101
	v_pk_fma_f32 v[100:101], v[2:3], v[106:107], v[100:101]
	s_nop 0
	s_waitcnt vmcnt(0)
	v_lshlrev_b32_e32 v106, 16, v104
	v_and_b32_e32 v107, 0xffff0000, v104
	v_lshlrev_b32_e32 v104, 16, v105
	v_and_b32_e32 v105, 0xffff0000, v105
	v_pk_fma_f32 v[106:107], v[0:1], v[12:13], v[106:107]
	v_cvt_pk_bf16_f32 v0, v102, v103
	v_cvt_pk_bf16_f32 v1, v100, v101
	v_pk_fma_f32 v[104:105], v[2:3], v[14:15], v[104:105]
	v_cvt_pk_bf16_f32 v2, v106, v107
	s_nop 0
	v_cvt_pk_bf16_f32 v3, v104, v105
	global_store_dwordx2 v[108:109], v[0:1], off offset:1024
	global_store_dwordx2 v[110:111], v[2:3], off offset:1024
	v_mov_b32_e32 v0, v21
	s_nop 0
	v_lshlrev_b32_e32 v14, 2, v0
	v_add_u32_e32 v108, 0x300, v14
	v_ashrrev_i32_e32 v109, 31, v108
	v_lshlrev_b64 v[110:111], 1, v[108:109]
	v_lshl_add_u64 v[236:237], vcc, 0, v[110:111]
	global_load_dwordx2 v[236:237], v[236:237], off
	v_lshl_add_u64 v[238:239], s[52:53], 0, v[110:111]
	global_load_dwordx2 v[238:239], v[238:239], off
	v_lshl_add_u64 v[240:241], s[50:51], 0, v[110:111]
	global_load_dwordx2 v[240:241], v[240:241], off
	v_lshl_add_u64 v[242:243], s[26:27], 0, v[110:111]
	global_load_dwordx2 v[242:243], v[242:243], off
	v_lshl_add_u64 v[244:245], s[24:25], 0, v[110:111]
	global_load_dwordx2 v[244:245], v[244:245], off
	s_nop 0
	s_nop 0
	ds_read_b128 v[0:3], v27 offset:48
	ds_read_b32 v12, v27 offset:64
	s_nop 0
	s_nop 0
	s_nop 0
	v_ashrrev_i32_e32 v15, 31, v14
	s_nop 0
	v_lshlrev_b64 v[14:15], 1, v[14:15]
	s_nop 0
	s_waitcnt vmcnt(3)
	v_lshlrev_b32_e32 v122, 16, v238
	v_and_b32_e32 v123, 0xffff0000, v238
	v_lshlrev_b32_e32 v120, 16, v239
	v_and_b32_e32 v121, 0xffff0000, v239
	s_waitcnt lgkmcnt(1)
	v_pk_fma_f32 v[126:127], v[0:1], v[120:121], 0 op_sel_hi:[0,1,0]
	s_nop 0
	s_waitcnt vmcnt(2)
	v_lshlrev_b32_e32 v130, 16, v240
	v_and_b32_e32 v131, 0xffff0000, v240
	v_lshlrev_b32_e32 v128, 16, v241
	v_and_b32_e32 v129, 0xffff0000, v241
	v_pk_fma_f32 v[126:127], v[0:1], v[128:129], v[126:127] op_sel:[1,0,0]
	s_nop 0
	s_nop 0
	s_nop 0
	s_nop 0
	v_pk_fma_f32 v[124:125], v[0:1], v[122:123], 0 op_sel_hi:[0,1,0]
	v_pk_fma_f32 v[124:125], v[0:1], v[130:131], v[124:125] op_sel:[1,0,0]
	v_lshlrev_b32_e32 v114, 16, v236
	v_and_b32_e32 v115, 0xffff0000, v236
	v_lshlrev_b32_e32 v112, 16, v237
	v_and_b32_e32 v113, 0xffff0000, v237
	s_waitcnt lgkmcnt(0)
	v_pk_mul_f32 v[116:117], v[12:13], v[112:113] op_sel_hi:[0,1]
	v_pk_mul_f32 v[118:119], v[12:13], v[114:115] op_sel_hi:[0,1]
	s_nop 0
	s_waitcnt vmcnt(1)
	v_lshlrev_b32_e32 v130, 16, v242
	v_and_b32_e32 v131, 0xffff0000, v242
	v_lshlrev_b32_e32 v128, 16, v243
	v_and_b32_e32 v129, 0xffff0000, v243
	v_pk_fma_f32 v[124:125], v[2:3], v[130:131], v[124:125] op_sel_hi:[0,1,1]
	v_pk_fma_f32 v[126:127], v[2:3], v[128:129], v[126:127] op_sel_hi:[0,1,1]
	s_nop 0
	s_waitcnt vmcnt(0)
	v_lshlrev_b32_e32 v128, 16, v244
	v_and_b32_e32 v129, 0xffff0000, v244
	v_lshlrev_b32_e32 v110, 16, v245
	v_and_b32_e32 v111, 0xffff0000, v245
	v_mov_b32_e32 v2, v3
	v_pk_mul_f32 v[130:131], v[2:3], v[110:111] op_sel_hi:[0,1]
	v_pk_mul_f32 v[132:133], v[2:3], v[128:129] op_sel_hi:[0,1]
	v_pk_fma_f32 v[110:111], v[2:3], v[110:111], v[126:127] op_sel_hi:[0,1,1]
	v_pk_fma_f32 v[2:3], v[2:3], v[128:129], v[124:125] op_sel_hi:[0,1,1]
	v_pk_fma_f32 v[122:123], v[0:1], v[122:123], v[2:3] op_sel_hi:[0,1,1] neg_lo:[1,0,0] neg_hi:[1,0,0]
	v_pk_fma_f32 v[0:1], v[0:1], v[120:121], v[110:111] op_sel_hi:[0,1,1] neg_lo:[1,0,0] neg_hi:[1,0,0]
	v_pk_fma_f32 v[0:1], v[12:13], v[112:113], v[0:1] op_sel_hi:[0,1,1]
	v_pk_fma_f32 v[12:13], v[12:13], v[114:115], v[122:123] op_sel_hi:[0,1,1]
	v_pk_fma_f32 v[112:113], v[4:5], v[2:3], v[132:133] op_sel_hi:[0,1,1] neg_lo:[0,0,1] neg_hi:[0,0,1]
	v_pk_fma_f32 v[110:111], v[4:5], v[110:111], v[130:131] op_sel_hi:[0,1,1] neg_lo:[0,0,1] neg_hi:[0,0,1]
	v_lshl_add_u64 v[4:5], s[22:23], 0, v[14:15]
	v_pk_fma_f32 v[12:13], v[6:7], v[12:13], v[118:119] op_sel_hi:[0,1,1] neg_lo:[0,0,1] neg_hi:[0,0,1]
	v_pk_fma_f32 v[6:7], v[6:7], v[0:1], v[116:117] op_sel_hi:[0,1,1] neg_lo:[0,0,1] neg_hi:[0,0,1]
	v_lshl_add_u32 v0, v108, 2, s17
	global_load_dwordx2 v[108:109], v[4:5], off offset:1536
	ds_read_b128 v[0:3], v0
	v_lshl_add_u64 v[14:15], s[20:21], 0, v[14:15]
	s_nop 0
	s_waitcnt vmcnt(0)
	v_lshlrev_b32_e32 v114, 16, v108
	v_and_b32_e32 v115, 0xffff0000, v108
	v_lshlrev_b32_e32 v108, 16, v109
	v_and_b32_e32 v109, 0xffff0000, v109
	s_waitcnt lgkmcnt(0)
	v_pk_fma_f32 v[108:109], v[2:3], v[110:111], v[108:109]
	v_pk_fma_f32 v[110:111], v[0:1], v[112:113], v[114:115]
	global_load_dwordx2 v[112:113], v[14:15], off offset:1536
	s_nop 0
	s_waitcnt vmcnt(0)
	v_lshlrev_b32_e32 v114, 16, v112
	v_and_b32_e32 v115, 0xffff0000, v112
	v_lshlrev_b32_e32 v112, 16, v113
	v_and_b32_e32 v113, 0xffff0000, v113
	v_pk_fma_f32 v[114:115], v[0:1], v[12:13], v[114:115]
	v_cvt_pk_bf16_f32 v0, v110, v111
	v_cvt_pk_bf16_f32 v1, v108, v109
	v_pk_fma_f32 v[112:113], v[2:3], v[6:7], v[112:113]
	v_cvt_pk_bf16_f32 v2, v114, v115
	s_nop 0
	v_cvt_pk_bf16_f32 v3, v112, v113
	global_store_dwordx2 v[4:5], v[0:1], off offset:1536
	global_store_dwordx2 v[14:15], v[2:3], off offset:1536
	v_mov_b32_e32 v0, v21
	s_add_u32 s0, s92, s0
	v_lshlrev_b32_e32 v12, 2, v0
	v_add_u32_e32 v14, 0x400, v12
	v_ashrrev_i32_e32 v15, 31, v14
	s_addc_u32 s1, s93, s1
	v_lshlrev_b64 v[126:127], 1, v[14:15]
	s_add_u32 s42, s92, s42
	v_lshl_add_u64 v[128:129], s[0:1], 0, v[126:127]
	s_addc_u32 s43, s93, s43
	ds_read_b128 v[0:3], v27 offset:32
	ds_read_b128 v[4:7], v27 offset:48
	ds_read_b32 v116, v27 offset:64
	global_load_dwordx2 v[130:131], v[128:129], off
	v_lshl_add_u64 v[238:239], s[42:43], 0, v[126:127]
	global_load_dwordx2 v[238:239], v[238:239], off
	v_lshl_add_u64 v[240:241], vcc, 0, v[126:127]
	global_load_dwordx2 v[240:241], v[240:241], off
	s_nop 0
	s_nop 0
	s_add_u32 s2, s92, s2
	s_addc_u32 s3, s93, s3
	s_add_u32 s36, s92, s36
	s_addc_u32 s37, s93, s37
	v_lshl_add_u64 v[118:119], vcc, 0, v[126:127]
	s_nop 0
	v_ashrrev_i32_e32 v13, 31, v12
	s_add_u32 s76, s92, s76
	s_addc_u32 s77, s93, s77
	s_add_u32 s10, s92, s10
	s_addc_u32 s11, s93, s11
	s_add_u32 s8, s92, s8
	s_addc_u32 s9, s93, s9
	s_add_u32 s44, s92, s44
	s_addc_u32 s45, s93, s45
	s_add_u32 s48, s92, s48
	s_addc_u32 s49, s93, s49
	s_add_u32 s46, s92, s46
	s_addc_u32 s47, s93, s47
	s_add_u32 s30, s92, s30
	s_addc_u32 s31, s93, s31
	s_add_u32 s28, s92, s28
	s_addc_u32 s29, s93, s29
	s_nop 0
	s_waitcnt vmcnt(2)
	v_lshlrev_b32_e32 v128, 16, v130
	v_and_b32_e32 v129, 0xffff0000, v130
	v_lshlrev_b32_e32 v130, 16, v131
	v_and_b32_e32 v131, 0xffff0000, v131
	s_waitcnt lgkmcnt(2)
	v_pk_fma_f32 v[134:135], v[0:1], v[130:131], 0 op_sel_hi:[0,1,0]
	s_nop 0
	s_waitcnt vmcnt(1)
	v_lshlrev_b32_e32 v138, 16, v238
	v_and_b32_e32 v139, 0xffff0000, v238
	v_lshlrev_b32_e32 v136, 16, v239
	v_and_b32_e32 v137, 0xffff0000, v239
	v_pk_fma_f32 v[134:135], v[0:1], v[136:137], v[134:135] op_sel:[1,0,0]
	v_lshl_add_u64 v[236:237], s[2:3], 0, v[126:127]
	global_load_dwordx2 v[236:237], v[236:237], off
	v_lshl_add_u64 v[238:239], s[36:37], 0, v[126:127]
	global_load_dwordx2 v[238:239], v[238:239], off
	v_lshl_add_u64 v[242:243], s[52:53], 0, v[126:127]
	global_load_dwordx2 v[242:243], v[242:243], off
	v_lshl_add_u64 v[244:245], s[50:51], 0, v[126:127]
	global_load_dwordx2 v[244:245], v[244:245], off
	v_lshl_add_u64 v[246:247], s[24:25], 0, v[126:127]
	global_load_dwordx2 v[246:247], v[246:247], off
	v_lshl_add_u64 v[230:231], s[26:27], 0, v[126:127]
	global_load_dwordx2 v[230:231], v[230:231], off
	s_nop 0
	s_nop 0
	v_pk_fma_f32 v[132:133], v[0:1], v[128:129], 0 op_sel_hi:[0,1,0]
	v_pk_fma_f32 v[132:133], v[0:1], v[138:139], v[132:133] op_sel:[1,0,0]
	s_nop 0
	s_waitcnt vmcnt(5)
	v_lshlrev_b32_e32 v138, 16, v236
	v_and_b32_e32 v139, 0xffff0000, v236
	v_lshlrev_b32_e32 v136, 16, v237
	v_and_b32_e32 v137, 0xffff0000, v237
	v_pk_fma_f32 v[134:135], v[2:3], v[136:137], v[134:135] op_sel_hi:[0,1,1]
	s_nop 0
	s_nop 0
	v_pk_fma_f32 v[132:133], v[2:3], v[138:139], v[132:133] op_sel_hi:[0,1,1]
	v_mov_b32_e32 v2, v3
	s_nop 0
	s_waitcnt vmcnt(4)
	v_lshlrev_b32_e32 v138, 16, v238
	v_and_b32_e32 v139, 0xffff0000, v238
	v_lshlrev_b32_e32 v136, 16, v239
	v_and_b32_e32 v137, 0xffff0000, v239
	v_pk_fma_f32 v[134:135], v[2:3], v[136:137], v[134:135] op_sel_hi:[0,1,1]
	v_pk_fma_f32 v[2:3], v[2:3], v[138:139], v[132:133] op_sel_hi:[0,1,1]
	s_nop 0
	s_nop 0
	s_nop 0
	s_waitcnt vmcnt(3)
	v_lshlrev_b32_e32 v136, 16, v242
	v_and_b32_e32 v137, 0xffff0000, v242
	v_lshlrev_b32_e32 v132, 16, v243
	v_and_b32_e32 v133, 0xffff0000, v243
	s_waitcnt lgkmcnt(1)
	v_pk_fma_f32 v[132:133], v[4:5], v[132:133], v[134:135] op_sel_hi:[0,1,1]
	s_nop 0
	s_nop 0
	v_pk_fma_f32 v[2:3], v[4:5], v[136:137], v[2:3] op_sel_hi:[0,1,1]
	s_nop 0
	s_waitcnt vmcnt(2)
	v_lshlrev_b32_e32 v136, 16, v244
	v_and_b32_e32 v137, 0xffff0000, v244
	v_lshlrev_b32_e32 v134, 16, v245
	v_and_b32_e32 v135, 0xffff0000, v245
	v_pk_fma_f32 v[132:133], v[4:5], v[134:135], v[132:133] op_sel:[1,0,0]
	v_pk_fma_f32 v[2:3], v[4:5], v[136:137], v[2:3] op_sel:[1,0,0]
	s_nop 0
	s_nop 0
	s_nop 0
	s_nop 0
	s_nop 0
	v_lshlrev_b32_e32 v122, 16, v241
	v_and_b32_e32 v123, 0xffff0000, v241
	v_lshlrev_b32_e32 v118, 16, v240
	v_and_b32_e32 v119, 0xffff0000, v240
	s_waitcnt lgkmcnt(0)
	v_pk_mul_f32 v[120:121], v[116:117], v[122:123] op_sel_hi:[0,1]
	v_pk_mul_f32 v[124:125], v[116:117], v[118:119] op_sel_hi:[0,1]
	s_nop 0
	s_waitcnt vmcnt(0)
	v_lshlrev_b32_e32 v134, 16, v230
	v_and_b32_e32 v135, 0xffff0000, v230
	v_lshlrev_b32_e32 v4, 16, v231
	v_and_b32_e32 v5, 0xffff0000, v231
	v_pk_fma_f32 v[2:3], v[6:7], v[134:135], v[2:3] op_sel_hi:[0,1,1]
	v_pk_fma_f32 v[4:5], v[6:7], v[4:5], v[132:133] op_sel_hi:[0,1,1]
	v_lshlrev_b32_e32 v132, 16, v246
	v_and_b32_e32 v133, 0xffff0000, v246
	v_lshlrev_b32_e32 v126, 16, v247
	v_and_b32_e32 v127, 0xffff0000, v247
	v_mov_b32_e32 v6, v7
	v_pk_mul_f32 v[134:135], v[6:7], v[126:127] op_sel_hi:[0,1]
	v_pk_fma_f32 v[126:127], v[6:7], v[126:127], v[4:5] op_sel_hi:[0,1,1]
	v_pk_fma_f32 v[2:3], v[6:7], v[132:133], v[2:3] op_sel_hi:[0,1,1]
	v_pk_fma_f32 v[4:5], v[0:1], v[128:129], v[2:3] op_sel_hi:[0,1,1] neg_lo:[1,0,0] neg_hi:[1,0,0]
	v_pk_fma_f32 v[0:1], v[0:1], v[130:131], v[126:127] op_sel_hi:[0,1,1] neg_lo:[1,0,0] neg_hi:[1,0,0]
	v_pk_fma_f32 v[0:1], v[116:117], v[122:123], v[0:1] op_sel_hi:[0,1,1]
	v_pk_mul_f32 v[136:137], v[6:7], v[132:133] op_sel_hi:[0,1]
	v_pk_fma_f32 v[6:7], v[10:11], v[0:1], v[120:121] op_sel_hi:[0,1,1] neg_lo:[0,0,1] neg_hi:[0,0,1]
	v_lshl_add_u32 v0, v14, 2, s17
	v_lshlrev_b64 v[14:15], 1, v[12:13]
	v_lshl_add_u64 v[12:13], s[22:23], 0, v[14:15]
	global_load_dwordx2 v[120:121], v[12:13], off offset:2048
	v_pk_fma_f32 v[4:5], v[116:117], v[118:119], v[4:5] op_sel_hi:[0,1,1]
	v_pk_fma_f32 v[118:119], v[8:9], v[2:3], v[136:137] op_sel_hi:[0,1,1] neg_lo:[0,0,1] neg_hi:[0,0,1]
	ds_read_b128 v[0:3], v0
	v_pk_fma_f32 v[116:117], v[8:9], v[126:127], v[134:135] op_sel_hi:[0,1,1] neg_lo:[0,0,1] neg_hi:[0,0,1]
	v_lshl_add_u64 v[14:15], s[20:21], 0, v[14:15]
	v_pk_fma_f32 v[4:5], v[10:11], v[4:5], v[124:125] op_sel_hi:[0,1,1] neg_lo:[0,0,1] neg_hi:[0,0,1]
	s_nop 0
	s_waitcnt vmcnt(0)
	v_lshlrev_b32_e32 v122, 16, v120
	v_and_b32_e32 v123, 0xffff0000, v120
	v_lshlrev_b32_e32 v120, 16, v121
	v_and_b32_e32 v121, 0xffff0000, v121
	s_waitcnt lgkmcnt(0)
	v_pk_fma_f32 v[116:117], v[2:3], v[116:117], v[120:121]
	global_load_dwordx2 v[120:121], v[14:15], off offset:2048
	v_pk_fma_f32 v[118:119], v[0:1], v[118:119], v[122:123]
	s_nop 0
	s_waitcnt vmcnt(0)
	v_lshlrev_b32_e32 v122, 16, v120
	v_and_b32_e32 v123, 0xffff0000, v120
	v_lshlrev_b32_e32 v120, 16, v121
	v_and_b32_e32 v121, 0xffff0000, v121
	v_pk_fma_f32 v[122:123], v[0:1], v[4:5], v[122:123]
	v_cvt_pk_bf16_f32 v0, v118, v119
	v_cvt_pk_bf16_f32 v1, v116, v117
	v_pk_fma_f32 v[120:121], v[2:3], v[6:7], v[120:121]
	v_cvt_pk_bf16_f32 v2, v122, v123
	s_nop 0
	v_cvt_pk_bf16_f32 v3, v120, v121
	global_store_dwordx2 v[12:13], v[0:1], off offset:2048
	global_store_dwordx2 v[14:15], v[2:3], off offset:2048
	v_mov_b32_e32 v0, v21
	s_nop 0
	v_lshlrev_b32_e32 v12, 2, v0
	v_add_u32_e32 v14, 0x500, v12
	v_ashrrev_i32_e32 v15, 31, v14
	v_lshlrev_b64 v[134:135], 1, v[14:15]
	v_lshl_add_u64 v[236:237], s[0:1], 0, v[134:135]
	global_load_dwordx2 v[236:237], v[236:237], off
	v_lshl_add_u64 v[238:239], s[42:43], 0, v[134:135]
	global_load_dwordx2 v[238:239], v[238:239], off
	v_lshl_add_u64 v[240:241], vcc, 0, v[134:135]
	global_load_dwordx2 v[240:241], v[240:241], off
	v_lshl_add_u64 v[242:243], s[2:3], 0, v[134:135]
	global_load_dwordx2 v[242:243], v[242:243], off
	v_lshl_add_u64 v[244:245], s[36:37], 0, v[134:135]
	global_load_dwordx2 v[244:245], v[244:245], off
	v_lshl_add_u64 v[246:247], s[52:53], 0, v[134:135]
	global_load_dwordx2 v[246:247], v[246:247], off
	v_lshl_add_u64 v[230:231], s[50:51], 0, v[134:135]
	global_load_dwordx2 v[230:231], v[230:231], off
	v_lshl_add_u64 v[232:233], s[24:25], 0, v[134:135]
	global_load_dwordx2 v[232:233], v[232:233], off
	v_lshl_add_u64 v[234:235], s[26:27], 0, v[134:135]
	global_load_dwordx2 v[234:235], v[234:235], off
	v_lshl_add_u64 v[136:137], s[0:1], 0, v[134:135]
	ds_read_b128 v[0:3], v27 offset:32
	ds_read_b128 v[4:7], v27 offset:48
	ds_read_b32 v124, v27 offset:64
	s_nop 0
	s_nop 0
	s_nop 0
	v_lshl_add_u64 v[126:127], vcc, 0, v[134:135]
	s_nop 0
	v_ashrrev_i32_e32 v13, 31, v12
	v_lshlrev_b64 v[12:13], 1, v[12:13]
	s_nop 0
	s_waitcnt vmcnt(8)
	v_lshlrev_b32_e32 v136, 16, v236
	v_and_b32_e32 v137, 0xffff0000, v236
	v_lshlrev_b32_e32 v138, 16, v237
	v_and_b32_e32 v139, 0xffff0000, v237
	s_waitcnt lgkmcnt(2)
	v_pk_fma_f32 v[142:143], v[0:1], v[138:139], 0 op_sel_hi:[0,1,0]
	s_nop 0
	s_waitcnt vmcnt(7)
	v_lshlrev_b32_e32 v146, 16, v238
	v_and_b32_e32 v147, 0xffff0000, v238
	v_lshlrev_b32_e32 v144, 16, v239
	v_and_b32_e32 v145, 0xffff0000, v239
	v_pk_fma_f32 v[142:143], v[0:1], v[144:145], v[142:143] op_sel:[1,0,0]
	s_nop 0
	s_nop 0
	v_pk_fma_f32 v[140:141], v[0:1], v[136:137], 0 op_sel_hi:[0,1,0]
	v_pk_fma_f32 v[140:141], v[0:1], v[146:147], v[140:141] op_sel:[1,0,0]
	s_nop 0
	s_waitcnt vmcnt(5)
	v_lshlrev_b32_e32 v146, 16, v242
	v_and_b32_e32 v147, 0xffff0000, v242
	v_lshlrev_b32_e32 v144, 16, v243
	v_and_b32_e32 v145, 0xffff0000, v243
	v_pk_fma_f32 v[142:143], v[2:3], v[144:145], v[142:143] op_sel_hi:[0,1,1]
	s_nop 0
	s_nop 0
	v_pk_fma_f32 v[140:141], v[2:3], v[146:147], v[140:141] op_sel_hi:[0,1,1]
	v_mov_b32_e32 v2, v3
	s_nop 0
	s_waitcnt vmcnt(4)
	v_lshlrev_b32_e32 v146, 16, v244
	v_and_b32_e32 v147, 0xffff0000, v244
	v_lshlrev_b32_e32 v144, 16, v245
	v_and_b32_e32 v145, 0xffff0000, v245
	v_pk_fma_f32 v[142:143], v[2:3], v[144:145], v[142:143] op_sel_hi:[0,1,1]
	v_pk_fma_f32 v[2:3], v[2:3], v[146:147], v[140:141] op_sel_hi:[0,1,1]
	s_nop 0
	s_nop 0
	s_nop 0
	s_waitcnt vmcnt(3)
	v_lshlrev_b32_e32 v144, 16, v246
	v_and_b32_e32 v145, 0xffff0000, v246
	v_lshlrev_b32_e32 v140, 16, v247
	v_and_b32_e32 v141, 0xffff0000, v247
	s_waitcnt lgkmcnt(1)
	v_pk_fma_f32 v[140:141], v[4:5], v[140:141], v[142:143] op_sel_hi:[0,1,1]
	s_nop 0
	s_nop 0
	v_pk_fma_f32 v[2:3], v[4:5], v[144:145], v[2:3] op_sel_hi:[0,1,1]
	s_nop 0
	s_waitcnt vmcnt(2)
	v_lshlrev_b32_e32 v144, 16, v230
	v_and_b32_e32 v145, 0xffff0000, v230
	v_lshlrev_b32_e32 v142, 16, v231
	v_and_b32_e32 v143, 0xffff0000, v231
	v_pk_fma_f32 v[140:141], v[4:5], v[142:143], v[140:141] op_sel:[1,0,0]
	v_pk_fma_f32 v[2:3], v[4:5], v[144:145], v[2:3] op_sel:[1,0,0]
	s_nop 0
	s_nop 0
	s_nop 0
	s_nop 0
	s_nop 0
	v_lshlrev_b32_e32 v126, 16, v240
	v_and_b32_e32 v127, 0xffff0000, v240
	v_lshlrev_b32_e32 v130, 16, v241
	v_and_b32_e32 v131, 0xffff0000, v241
	s_waitcnt lgkmcnt(0)
	v_pk_mul_f32 v[128:129], v[124:125], v[130:131] op_sel_hi:[0,1]
	v_pk_mul_f32 v[132:133], v[124:125], v[126:127] op_sel_hi:[0,1]
	s_nop 0
	s_waitcnt vmcnt(0)
	v_lshlrev_b32_e32 v142, 16, v234
	v_and_b32_e32 v143, 0xffff0000, v234
	v_lshlrev_b32_e32 v4, 16, v235
	v_and_b32_e32 v5, 0xffff0000, v235
	v_pk_fma_f32 v[2:3], v[6:7], v[142:143], v[2:3] op_sel_hi:[0,1,1]
	v_pk_fma_f32 v[4:5], v[6:7], v[4:5], v[140:141] op_sel_hi:[0,1,1]
	v_lshlrev_b32_e32 v140, 16, v232
	v_and_b32_e32 v141, 0xffff0000, v232
	v_lshlrev_b32_e32 v134, 16, v233
	v_and_b32_e32 v135, 0xffff0000, v233
	v_mov_b32_e32 v6, v7
	v_pk_mul_f32 v[142:143], v[6:7], v[134:135] op_sel_hi:[0,1]
	v_pk_fma_f32 v[134:135], v[6:7], v[134:135], v[4:5] op_sel_hi:[0,1,1]
	v_pk_fma_f32 v[2:3], v[6:7], v[140:141], v[2:3] op_sel_hi:[0,1,1]
	v_pk_fma_f32 v[4:5], v[0:1], v[136:137], v[2:3] op_sel_hi:[0,1,1] neg_lo:[1,0,0] neg_hi:[1,0,0]
	v_pk_fma_f32 v[0:1], v[0:1], v[138:139], v[134:135] op_sel_hi:[0,1,1] neg_lo:[1,0,0] neg_hi:[1,0,0]
	v_pk_mul_f32 v[144:145], v[6:7], v[140:141] op_sel_hi:[0,1]
	v_pk_fma_f32 v[0:1], v[124:125], v[130:131], v[0:1] op_sel_hi:[0,1,1]
	v_pk_fma_f32 v[4:5], v[124:125], v[126:127], v[4:5] op_sel_hi:[0,1,1]
	v_pk_fma_f32 v[4:5], v[10:11], v[4:5], v[132:133] op_sel_hi:[0,1,1] neg_lo:[0,0,1] neg_hi:[0,0,1]
	v_pk_fma_f32 v[6:7], v[10:11], v[0:1], v[128:129] op_sel_hi:[0,1,1] neg_lo:[0,0,1] neg_hi:[0,0,1]
	v_pk_fma_f32 v[10:11], v[8:9], v[2:3], v[144:145] op_sel_hi:[0,1,1] neg_lo:[0,0,1] neg_hi:[0,0,1]
	v_pk_fma_f32 v[124:125], v[8:9], v[134:135], v[142:143] op_sel_hi:[0,1,1] neg_lo:[0,0,1] neg_hi:[0,0,1]
	v_lshl_add_u64 v[236:237], s[22:23], 0, v[12:13]
	global_load_dwordx2 v[236:237], v[236:237], off offset:2560
	v_lshl_add_u64 v[238:239], s[20:21], 0, v[12:13]
	global_load_dwordx2 v[238:239], v[238:239], off offset:2560
	v_lshl_add_u64 v[8:9], s[22:23], 0, v[12:13]
	v_lshl_add_u32 v0, v14, 2, s17
	s_nop 0
	ds_read_b128 v[0:3], v0
	s_nop 0
	s_waitcnt vmcnt(1)
	v_lshlrev_b32_e32 v126, 16, v236
	v_and_b32_e32 v127, 0xffff0000, v236
	s_waitcnt lgkmcnt(0)
	v_pk_fma_f32 v[126:127], v[0:1], v[10:11], v[126:127]
	v_lshl_add_u64 v[10:11], s[20:21], 0, v[12:13]
	s_nop 0
	v_lshlrev_b32_e32 v14, 16, v237
	v_and_b32_e32 v15, 0xffff0000, v237
	v_pk_fma_f32 v[124:125], v[2:3], v[124:125], v[14:15]
	s_nop 0
	s_waitcnt vmcnt(0)
	v_lshlrev_b32_e32 v14, 16, v238
	v_and_b32_e32 v15, 0xffff0000, v238
	v_lshlrev_b32_e32 v12, 16, v239
	v_and_b32_e32 v13, 0xffff0000, v239
	v_pk_fma_f32 v[130:131], v[0:1], v[4:5], v[14:15]
	v_cvt_pk_bf16_f32 v0, v126, v127
	v_cvt_pk_bf16_f32 v1, v124, v125
	v_pk_fma_f32 v[128:129], v[2:3], v[6:7], v[12:13]
	v_cvt_pk_bf16_f32 v2, v130, v131
	s_nop 0
	v_cvt_pk_bf16_f32 v3, v128, v129
	global_store_dwordx2 v[8:9], v[0:1], off offset:2560
	global_store_dwordx2 v[10:11], v[2:3], off offset:2560
	v_mov_b32_e32 v0, v21
	ds_read_b32 v136, v27 offset:64
	v_lshlrev_b32_e32 v132, 2, v0
	v_add_u32_e32 v134, 0x600, v132
	v_ashrrev_i32_e32 v135, 31, v134
	v_lshlrev_b64 v[146:147], 1, v[134:135]
	v_lshl_add_u64 v[0:1], vcc, 0, v[146:147]
	global_load_dwordx2 v[0:1], v[0:1], off
	v_lshl_add_u64 v[148:149], s[76:77], 0, v[146:147]
	v_lshl_add_u64 v[156:157], s[10:11], 0, v[146:147]
	v_ashrrev_i32_e32 v133, 31, v132
	s_nop 0
	s_waitcnt vmcnt(0)
	v_lshlrev_b32_e32 v138, 16, v0
	v_and_b32_e32 v139, 0xffff0000, v0
	v_lshlrev_b32_e32 v142, 16, v1
	v_and_b32_e32 v143, 0xffff0000, v1
	ds_read_b128 v[0:3], v27
	ds_read_b128 v[12:15], v27 offset:16
	ds_read_b128 v[8:11], v27 offset:32
	ds_read_b128 v[4:7], v27 offset:48
	global_load_dwordx2 v[150:151], v[148:149], off
	s_waitcnt lgkmcnt(4)
	v_pk_mul_f32 v[140:141], v[136:137], v[142:143] op_sel_hi:[0,1]
	global_load_dwordx2 v[156:157], v[156:157], off
	v_pk_mul_f32 v[144:145], v[136:137], v[138:139] op_sel_hi:[0,1]
	s_nop 0
	s_waitcnt vmcnt(1)
	v_lshlrev_b32_e32 v148, 16, v150
	v_and_b32_e32 v149, 0xffff0000, v150
	v_lshlrev_b32_e32 v150, 16, v151
	v_and_b32_e32 v151, 0xffff0000, v151
	s_waitcnt lgkmcnt(3)
	v_pk_fma_f32 v[154:155], v[0:1], v[150:151], 0 op_sel_hi:[0,1,0]
	s_nop 0
	s_waitcnt vmcnt(0)
	v_lshlrev_b32_e32 v158, 16, v156
	v_and_b32_e32 v159, 0xffff0000, v156
	v_lshlrev_b32_e32 v156, 16, v157
	v_and_b32_e32 v157, 0xffff0000, v157
	v_pk_fma_f32 v[154:155], v[0:1], v[156:157], v[154:155] op_sel:[1,0,0]
	v_lshl_add_u64 v[236:237], s[8:9], 0, v[146:147]
	global_load_dwordx2 v[236:237], v[236:237], off
	v_lshl_add_u64 v[238:239], s[44:45], 0, v[146:147]
	global_load_dwordx2 v[238:239], v[238:239], off
	v_lshl_add_u64 v[240:241], s[48:49], 0, v[146:147]
	global_load_dwordx2 v[240:241], v[240:241], off
	v_lshl_add_u64 v[242:243], s[46:47], 0, v[146:147]
	global_load_dwordx2 v[242:243], v[242:243], off
	v_lshl_add_u64 v[244:245], s[30:31], 0, v[146:147]
	global_load_dwordx2 v[244:245], v[244:245], off
	v_lshl_add_u64 v[246:247], s[28:29], 0, v[146:147]
	global_load_dwordx2 v[246:247], v[246:247], off
	v_lshl_add_u64 v[230:231], s[0:1], 0, v[146:147]
	global_load_dwordx2 v[230:231], v[230:231], off
	v_lshl_add_u64 v[232:233], s[42:43], 0, v[146:147]
	global_load_dwordx2 v[232:233], v[232:233], off
	v_lshl_add_u64 v[234:235], s[2:3], 0, v[146:147]
	global_load_dwordx2 v[234:235], v[234:235], off
	s_nop 0
	s_nop 0
	v_pk_fma_f32 v[152:153], v[0:1], v[148:149], 0 op_sel_hi:[0,1,0]
	v_pk_fma_f32 v[152:153], v[0:1], v[158:159], v[152:153] op_sel:[1,0,0]
	s_nop 0
	s_waitcnt vmcnt(8)
	v_lshlrev_b32_e32 v158, 16, v236
	v_and_b32_e32 v159, 0xffff0000, v236
	v_lshlrev_b32_e32 v156, 16, v237
	v_and_b32_e32 v157, 0xffff0000, v237
	v_pk_fma_f32 v[154:155], v[2:3], v[156:157], v[154:155] op_sel_hi:[0,1,1]
	s_nop 0
	s_nop 0
	v_pk_fma_f32 v[152:153], v[2:3], v[158:159], v[152:153] op_sel_hi:[0,1,1]
	v_mov_b32_e32 v2, v3
	s_nop 0
	s_waitcnt vmcnt(7)
	v_lshlrev_b32_e32 v158, 16, v238
	v_and_b32_e32 v159, 0xffff0000, v238
	v_lshlrev_b32_e32 v156, 16, v239
	v_and_b32_e32 v157, 0xffff0000, v239
	v_pk_fma_f32 v[154:155], v[2:3], v[156:157], v[154:155] op_sel_hi:[0,1,1]
	v_pk_fma_f32 v[2:3], v[2:3], v[158:159], v[152:153] op_sel_hi:[0,1,1]
	s_nop 0
	s_nop 0
	s_nop 0
	s_waitcnt vmcnt(6)
	v_lshlrev_b32_e32 v156, 16, v240
	v_and_b32_e32 v157, 0xffff0000, v240
	v_lshlrev_b32_e32 v152, 16, v241
	v_and_b32_e32 v153, 0xffff0000, v241
	s_waitcnt lgkmcnt(2)
	v_pk_fma_f32 v[152:153], v[12:13], v[152:153], v[154:155] op_sel_hi:[0,1,1]
	s_nop 0
	s_nop 0
	v_pk_fma_f32 v[2:3], v[12:13], v[156:157], v[2:3] op_sel_hi:[0,1,1]
	s_nop 0
	s_waitcnt vmcnt(5)
	v_lshlrev_b32_e32 v156, 16, v242
	v_and_b32_e32 v157, 0xffff0000, v242
	v_lshlrev_b32_e32 v154, 16, v243
	v_and_b32_e32 v155, 0xffff0000, v243
	v_pk_fma_f32 v[152:153], v[12:13], v[154:155], v[152:153] op_sel:[1,0,0]
	v_pk_fma_f32 v[2:3], v[12:13], v[156:157], v[2:3] op_sel:[1,0,0]
	s_nop 0
	s_nop 0
	s_nop 0
	s_waitcnt vmcnt(4)
	v_lshlrev_b32_e32 v154, 16, v244
	v_and_b32_e32 v155, 0xffff0000, v244
	v_lshlrev_b32_e32 v12, 16, v245
	v_and_b32_e32 v13, 0xffff0000, v245
	v_pk_fma_f32 v[12:13], v[14:15], v[12:13], v[152:153] op_sel_hi:[0,1,1]
	s_nop 0
	s_nop 0
	v_pk_fma_f32 v[2:3], v[14:15], v[154:155], v[2:3] op_sel_hi:[0,1,1]
	v_mov_b32_e32 v14, v15
	s_nop 0
	s_waitcnt vmcnt(3)
	v_lshlrev_b32_e32 v154, 16, v246
	v_and_b32_e32 v155, 0xffff0000, v246
	v_lshlrev_b32_e32 v152, 16, v247
	v_and_b32_e32 v153, 0xffff0000, v247
	v_pk_fma_f32 v[12:13], v[14:15], v[152:153], v[12:13] op_sel_hi:[0,1,1]
	v_pk_fma_f32 v[2:3], v[14:15], v[154:155], v[2:3] op_sel_hi:[0,1,1]
	s_nop 0
	s_nop 0
	s_nop 0
	s_waitcnt vmcnt(2)
	v_lshlrev_b32_e32 v152, 16, v230
	v_and_b32_e32 v153, 0xffff0000, v230
	v_lshlrev_b32_e32 v14, 16, v231
	v_and_b32_e32 v15, 0xffff0000, v231
	s_waitcnt lgkmcnt(1)
	v_pk_fma_f32 v[12:13], v[8:9], v[14:15], v[12:13] op_sel_hi:[0,1,1]
	s_nop 0
	s_nop 0
	v_pk_fma_f32 v[2:3], v[8:9], v[152:153], v[2:3] op_sel_hi:[0,1,1]
	s_nop 0
	s_waitcnt vmcnt(1)
	v_lshlrev_b32_e32 v152, 16, v232
	v_and_b32_e32 v153, 0xffff0000, v232
	v_lshlrev_b32_e32 v14, 16, v233
	v_and_b32_e32 v15, 0xffff0000, v233
	v_pk_fma_f32 v[12:13], v[8:9], v[14:15], v[12:13] op_sel:[1,0,0]
	v_pk_fma_f32 v[2:3], v[8:9], v[152:153], v[2:3] op_sel:[1,0,0]
	s_nop 0
	s_nop 0
	s_nop 0
	s_waitcnt vmcnt(0)
	v_lshlrev_b32_e32 v14, 16, v234
	v_and_b32_e32 v15, 0xffff0000, v234
	v_lshlrev_b32_e32 v8, 16, v235
	v_and_b32_e32 v9, 0xffff0000, v235
	v_pk_fma_f32 v[8:9], v[10:11], v[8:9], v[12:13] op_sel_hi:[0,1,1]
	v_lshl_add_u64 v[236:237], s[36:37], 0, v[146:147]
	global_load_dwordx2 v[236:237], v[236:237], off
	v_lshl_add_u64 v[238:239], s[52:53], 0, v[146:147]
	global_load_dwordx2 v[238:239], v[238:239], off
	v_lshl_add_u64 v[240:241], s[50:51], 0, v[146:147]
	global_load_dwordx2 v[240:241], v[240:241], off
	v_lshl_add_u64 v[242:243], s[26:27], 0, v[146:147]
	global_load_dwordx2 v[242:243], v[242:243], off
	v_lshl_add_u64 v[244:245], s[24:25], 0, v[146:147]
	global_load_dwordx2 v[244:245], v[244:245], off
	s_nop 0
	s_nop 0
	v_pk_fma_f32 v[2:3], v[10:11], v[14:15], v[2:3] op_sel_hi:[0,1,1]
	v_mov_b32_e32 v10, v11
	s_nop 0
	s_waitcnt vmcnt(4)
	v_lshlrev_b32_e32 v14, 16, v236
	v_and_b32_e32 v15, 0xffff0000, v236
	v_lshlrev_b32_e32 v12, 16, v237
	v_and_b32_e32 v13, 0xffff0000, v237
	v_pk_fma_f32 v[8:9], v[10:11], v[12:13], v[8:9] op_sel_hi:[0,1,1]
	v_pk_fma_f32 v[2:3], v[10:11], v[14:15], v[2:3] op_sel_hi:[0,1,1]
	s_nop 0
	s_nop 0
	s_nop 0
	s_waitcnt vmcnt(3)
	v_lshlrev_b32_e32 v12, 16, v238
	v_and_b32_e32 v13, 0xffff0000, v238
	v_lshlrev_b32_e32 v10, 16, v239
	v_and_b32_e32 v11, 0xffff0000, v239
	s_waitcnt lgkmcnt(0)
	v_pk_fma_f32 v[8:9], v[4:5], v[10:11], v[8:9] op_sel_hi:[0,1,1]
	s_nop 0
	s_nop 0
	v_pk_fma_f32 v[2:3], v[4:5], v[12:13], v[2:3] op_sel_hi:[0,1,1]
	s_nop 0
	s_waitcnt vmcnt(2)
	v_lshlrev_b32_e32 v12, 16, v240
	v_and_b32_e32 v13, 0xffff0000, v240
	v_lshlrev_b32_e32 v10, 16, v241
	v_and_b32_e32 v11, 0xffff0000, v241
	v_pk_fma_f32 v[8:9], v[4:5], v[10:11], v[8:9] op_sel:[1,0,0]
	v_pk_fma_f32 v[2:3], v[4:5], v[12:13], v[2:3] op_sel:[1,0,0]
	s_nop 0
	s_nop 0
	s_nop 0
	s_waitcnt vmcnt(1)
	v_lshlrev_b32_e32 v10, 16, v242
	v_and_b32_e32 v11, 0xffff0000, v242
	v_lshlrev_b32_e32 v4, 16, v243
	v_and_b32_e32 v5, 0xffff0000, v243
	v_pk_fma_f32 v[4:5], v[6:7], v[4:5], v[8:9] op_sel_hi:[0,1,1]
	s_nop 0
	s_nop 0
	v_pk_fma_f32 v[2:3], v[6:7], v[10:11], v[2:3] op_sel_hi:[0,1,1]
	v_mov_b32_e32 v6, v7
	s_nop 0
	s_waitcnt vmcnt(0)
	v_lshlrev_b32_e32 v10, 16, v244
	v_and_b32_e32 v11, 0xffff0000, v244
	v_lshlrev_b32_e32 v8, 16, v245
	v_and_b32_e32 v9, 0xffff0000, v245
	v_pk_mul_f32 v[14:15], v[6:7], v[10:11] op_sel_hi:[0,1]
	v_pk_fma_f32 v[2:3], v[6:7], v[10:11], v[2:3] op_sel_hi:[0,1,1]
	v_pk_mul_f32 v[12:13], v[6:7], v[8:9] op_sel_hi:[0,1]
	v_pk_fma_f32 v[8:9], v[6:7], v[8:9], v[4:5] op_sel_hi:[0,1,1]
	v_pk_fma_f32 v[10:11], v[92:93], v[2:3], v[14:15] op_sel_hi:[0,1,1] neg_lo:[0,0,1] neg_hi:[0,0,1]
	v_lshlrev_b64 v[14:15], 1, v[132:133]
	v_pk_fma_f32 v[4:5], v[0:1], v[148:149], v[2:3] op_sel_hi:[0,1,1] neg_lo:[1,0,0] neg_hi:[1,0,0]
	v_pk_fma_f32 v[0:1], v[0:1], v[150:151], v[8:9] op_sel_hi:[0,1,1] neg_lo:[1,0,0] neg_hi:[1,0,0]
	v_pk_fma_f32 v[12:13], v[92:93], v[8:9], v[12:13] op_sel_hi:[0,1,1] neg_lo:[0,0,1] neg_hi:[0,0,1]
	v_lshl_add_u64 v[236:237], s[22:23], 0, v[14:15]
	global_load_dwordx2 v[236:237], v[236:237], off offset:3072
	v_lshl_add_u64 v[238:239], s[20:21], 0, v[14:15]
	global_load_dwordx2 v[238:239], v[238:239], off offset:3072
	v_lshl_add_u64 v[8:9], s[22:23], 0, v[14:15]
	s_nop 0
	v_pk_fma_f32 v[0:1], v[136:137], v[142:143], v[0:1] op_sel_hi:[0,1,1]
	v_pk_fma_f32 v[6:7], v[94:95], v[0:1], v[140:141] op_sel_hi:[0,1,1] neg_lo:[0,0,1] neg_hi:[0,0,1]
	v_lshl_add_u32 v0, v134, 2, s17
	ds_read_b128 v[0:3], v0
	v_pk_fma_f32 v[4:5], v[136:137], v[138:139], v[4:5] op_sel_hi:[0,1,1]
	v_pk_fma_f32 v[4:5], v[94:95], v[4:5], v[144:145] op_sel_hi:[0,1,1] neg_lo:[0,0,1] neg_hi:[0,0,1]
	s_nop 0
	s_waitcnt vmcnt(1)
	v_lshlrev_b32_e32 v134, 16, v236
	v_and_b32_e32 v135, 0xffff0000, v236
	v_lshlrev_b32_e32 v132, 16, v237
	v_and_b32_e32 v133, 0xffff0000, v237
	s_waitcnt lgkmcnt(0)
	v_pk_fma_f32 v[134:135], v[0:1], v[10:11], v[134:135]
	v_lshl_add_u64 v[10:11], s[20:21], 0, v[14:15]
	v_pk_fma_f32 v[132:133], v[2:3], v[12:13], v[132:133]
	s_nop 0
	s_nop 0
	s_waitcnt vmcnt(0)
	v_lshlrev_b32_e32 v14, 16, v238
	v_and_b32_e32 v15, 0xffff0000, v238
	v_lshlrev_b32_e32 v12, 16, v239
	v_and_b32_e32 v13, 0xffff0000, v239
	v_pk_fma_f32 v[138:139], v[0:1], v[4:5], v[14:15]
	v_cvt_pk_bf16_f32 v0, v134, v135
	v_cvt_pk_bf16_f32 v1, v132, v133
	v_pk_fma_f32 v[136:137], v[2:3], v[6:7], v[12:13]
	v_cvt_pk_bf16_f32 v2, v138, v139
	s_nop 0
	v_cvt_pk_bf16_f32 v3, v136, v137
	global_store_dwordx2 v[8:9], v[0:1], off offset:3072
	global_store_dwordx2 v[10:11], v[2:3], off offset:3072
	v_mov_b32_e32 v0, v21
	ds_read_b32 v144, v27 offset:64
	v_lshlrev_b32_e32 v140, 2, v0
	v_add_u32_e32 v142, 0x700, v140
	v_ashrrev_i32_e32 v143, 31, v142
	v_lshlrev_b64 v[154:155], 1, v[142:143]
	v_lshl_add_u64 v[0:1], vcc, 0, v[154:155]
	global_load_dwordx2 v[0:1], v[0:1], off
	v_lshl_add_u64 v[156:157], s[76:77], 0, v[154:155]
	v_lshl_add_u64 v[164:165], s[10:11], 0, v[154:155]
	v_ashrrev_i32_e32 v141, 31, v140
	s_nop 0
	s_waitcnt vmcnt(0)
	v_lshlrev_b32_e32 v146, 16, v0
	v_and_b32_e32 v147, 0xffff0000, v0
	v_lshlrev_b32_e32 v150, 16, v1
	v_and_b32_e32 v151, 0xffff0000, v1
	ds_read_b128 v[0:3], v27
	ds_read_b128 v[12:15], v27 offset:16
	ds_read_b128 v[8:11], v27 offset:32
	ds_read_b128 v[4:7], v27 offset:48
	global_load_dwordx2 v[158:159], v[156:157], off
	s_waitcnt lgkmcnt(4)
	v_pk_mul_f32 v[152:153], v[144:145], v[146:147] op_sel_hi:[0,1]
	global_load_dwordx2 v[164:165], v[164:165], off
	v_pk_mul_f32 v[148:149], v[144:145], v[150:151] op_sel_hi:[0,1]
	s_nop 0
	s_waitcnt vmcnt(1)
	v_lshlrev_b32_e32 v156, 16, v158
	v_and_b32_e32 v157, 0xffff0000, v158
	v_lshlrev_b32_e32 v158, 16, v159
	v_and_b32_e32 v159, 0xffff0000, v159
	s_waitcnt lgkmcnt(3)
	v_pk_fma_f32 v[162:163], v[0:1], v[158:159], 0 op_sel_hi:[0,1,0]
	s_nop 0
	s_waitcnt vmcnt(0)
	v_lshlrev_b32_e32 v166, 16, v164
	v_and_b32_e32 v167, 0xffff0000, v164
	v_lshlrev_b32_e32 v164, 16, v165
	v_and_b32_e32 v165, 0xffff0000, v165
	v_pk_fma_f32 v[162:163], v[0:1], v[164:165], v[162:163] op_sel:[1,0,0]
	v_lshl_add_u64 v[236:237], s[8:9], 0, v[154:155]
	global_load_dwordx2 v[236:237], v[236:237], off
	v_lshl_add_u64 v[238:239], s[44:45], 0, v[154:155]
	global_load_dwordx2 v[238:239], v[238:239], off
	v_lshl_add_u64 v[240:241], s[48:49], 0, v[154:155]
	global_load_dwordx2 v[240:241], v[240:241], off
	v_lshl_add_u64 v[242:243], s[46:47], 0, v[154:155]
	global_load_dwordx2 v[242:243], v[242:243], off
	v_lshl_add_u64 v[244:245], s[30:31], 0, v[154:155]
	global_load_dwordx2 v[244:245], v[244:245], off
	v_lshl_add_u64 v[246:247], s[28:29], 0, v[154:155]
	global_load_dwordx2 v[246:247], v[246:247], off
	v_lshl_add_u64 v[230:231], s[0:1], 0, v[154:155]
	global_load_dwordx2 v[230:231], v[230:231], off
	v_lshl_add_u64 v[232:233], s[42:43], 0, v[154:155]
	global_load_dwordx2 v[232:233], v[232:233], off
	v_lshl_add_u64 v[234:235], s[2:3], 0, v[154:155]
	global_load_dwordx2 v[234:235], v[234:235], off
	s_nop 0
	s_nop 0
	v_pk_fma_f32 v[160:161], v[0:1], v[156:157], 0 op_sel_hi:[0,1,0]
	v_pk_fma_f32 v[160:161], v[0:1], v[166:167], v[160:161] op_sel:[1,0,0]
	s_nop 0
	s_waitcnt vmcnt(8)
	v_lshlrev_b32_e32 v166, 16, v236
	v_and_b32_e32 v167, 0xffff0000, v236
	v_lshlrev_b32_e32 v164, 16, v237
	v_and_b32_e32 v165, 0xffff0000, v237
	v_pk_fma_f32 v[162:163], v[2:3], v[164:165], v[162:163] op_sel_hi:[0,1,1]
	s_nop 0
	s_nop 0
	v_pk_fma_f32 v[160:161], v[2:3], v[166:167], v[160:161] op_sel_hi:[0,1,1]
	v_mov_b32_e32 v2, v3
	s_nop 0
	s_waitcnt vmcnt(7)
	v_lshlrev_b32_e32 v166, 16, v238
	v_and_b32_e32 v167, 0xffff0000, v238
	v_lshlrev_b32_e32 v164, 16, v239
	v_and_b32_e32 v165, 0xffff0000, v239
	v_pk_fma_f32 v[162:163], v[2:3], v[164:165], v[162:163] op_sel_hi:[0,1,1]
	v_pk_fma_f32 v[2:3], v[2:3], v[166:167], v[160:161] op_sel_hi:[0,1,1]
	s_nop 0
	s_nop 0
	s_nop 0
	s_waitcnt vmcnt(6)
	v_lshlrev_b32_e32 v164, 16, v240
	v_and_b32_e32 v165, 0xffff0000, v240
	v_lshlrev_b32_e32 v160, 16, v241
	v_and_b32_e32 v161, 0xffff0000, v241
	s_waitcnt lgkmcnt(2)
	v_pk_fma_f32 v[160:161], v[12:13], v[160:161], v[162:163] op_sel_hi:[0,1,1]
	s_nop 0
	s_nop 0
	v_pk_fma_f32 v[2:3], v[12:13], v[164:165], v[2:3] op_sel_hi:[0,1,1]
	s_nop 0
	s_waitcnt vmcnt(5)
	v_lshlrev_b32_e32 v164, 16, v242
	v_and_b32_e32 v165, 0xffff0000, v242
	v_lshlrev_b32_e32 v162, 16, v243
	v_and_b32_e32 v163, 0xffff0000, v243
	v_pk_fma_f32 v[160:161], v[12:13], v[162:163], v[160:161] op_sel:[1,0,0]
	v_pk_fma_f32 v[2:3], v[12:13], v[164:165], v[2:3] op_sel:[1,0,0]
	s_nop 0
	s_nop 0
	s_nop 0
	s_waitcnt vmcnt(4)
	v_lshlrev_b32_e32 v162, 16, v244
	v_and_b32_e32 v163, 0xffff0000, v244
	v_lshlrev_b32_e32 v12, 16, v245
	v_and_b32_e32 v13, 0xffff0000, v245
	v_pk_fma_f32 v[12:13], v[14:15], v[12:13], v[160:161] op_sel_hi:[0,1,1]
	s_nop 0
	s_nop 0
	v_pk_fma_f32 v[2:3], v[14:15], v[162:163], v[2:3] op_sel_hi:[0,1,1]
	v_mov_b32_e32 v14, v15
	s_nop 0
	s_waitcnt vmcnt(3)
	v_lshlrev_b32_e32 v162, 16, v246
	v_and_b32_e32 v163, 0xffff0000, v246
	v_lshlrev_b32_e32 v160, 16, v247
	v_and_b32_e32 v161, 0xffff0000, v247
	v_pk_fma_f32 v[12:13], v[14:15], v[160:161], v[12:13] op_sel_hi:[0,1,1]
	v_pk_fma_f32 v[2:3], v[14:15], v[162:163], v[2:3] op_sel_hi:[0,1,1]
	s_nop 0
	s_nop 0
	s_nop 0
	s_waitcnt vmcnt(2)
	v_lshlrev_b32_e32 v160, 16, v230
	v_and_b32_e32 v161, 0xffff0000, v230
	v_lshlrev_b32_e32 v14, 16, v231
	v_and_b32_e32 v15, 0xffff0000, v231
	s_waitcnt lgkmcnt(1)
	v_pk_fma_f32 v[12:13], v[8:9], v[14:15], v[12:13] op_sel_hi:[0,1,1]
	s_nop 0
	s_nop 0
	v_pk_fma_f32 v[2:3], v[8:9], v[160:161], v[2:3] op_sel_hi:[0,1,1]
	s_nop 0
	s_waitcnt vmcnt(1)
	v_lshlrev_b32_e32 v160, 16, v232
	v_and_b32_e32 v161, 0xffff0000, v232
	v_lshlrev_b32_e32 v14, 16, v233
	v_and_b32_e32 v15, 0xffff0000, v233
	v_pk_fma_f32 v[12:13], v[8:9], v[14:15], v[12:13] op_sel:[1,0,0]
	v_pk_fma_f32 v[2:3], v[8:9], v[160:161], v[2:3] op_sel:[1,0,0]
	s_nop 0
	s_nop 0
	s_nop 0
	s_waitcnt vmcnt(0)
	v_lshlrev_b32_e32 v14, 16, v234
	v_and_b32_e32 v15, 0xffff0000, v234
	v_lshlrev_b32_e32 v8, 16, v235
	v_and_b32_e32 v9, 0xffff0000, v235
	v_pk_fma_f32 v[8:9], v[10:11], v[8:9], v[12:13] op_sel_hi:[0,1,1]
	v_lshl_add_u64 v[236:237], s[36:37], 0, v[154:155]
	global_load_dwordx2 v[236:237], v[236:237], off
	v_lshl_add_u64 v[238:239], s[52:53], 0, v[154:155]
	global_load_dwordx2 v[238:239], v[238:239], off
	v_lshl_add_u64 v[240:241], s[50:51], 0, v[154:155]
	global_load_dwordx2 v[240:241], v[240:241], off
	v_lshl_add_u64 v[242:243], s[26:27], 0, v[154:155]
	global_load_dwordx2 v[242:243], v[242:243], off
	v_lshl_add_u64 v[244:245], s[24:25], 0, v[154:155]
	global_load_dwordx2 v[244:245], v[244:245], off
	s_nop 0
	s_nop 0
	v_pk_fma_f32 v[2:3], v[10:11], v[14:15], v[2:3] op_sel_hi:[0,1,1]
	v_mov_b32_e32 v10, v11
	s_nop 0
	s_waitcnt vmcnt(4)
	v_lshlrev_b32_e32 v14, 16, v236
	v_and_b32_e32 v15, 0xffff0000, v236
	v_lshlrev_b32_e32 v12, 16, v237
	v_and_b32_e32 v13, 0xffff0000, v237
	v_pk_fma_f32 v[8:9], v[10:11], v[12:13], v[8:9] op_sel_hi:[0,1,1]
	v_pk_fma_f32 v[2:3], v[10:11], v[14:15], v[2:3] op_sel_hi:[0,1,1]
	s_nop 0
	s_nop 0
	s_nop 0
	s_waitcnt vmcnt(3)
	v_lshlrev_b32_e32 v12, 16, v238
	v_and_b32_e32 v13, 0xffff0000, v238
	v_lshlrev_b32_e32 v10, 16, v239
	v_and_b32_e32 v11, 0xffff0000, v239
	s_waitcnt lgkmcnt(0)
	v_pk_fma_f32 v[8:9], v[4:5], v[10:11], v[8:9] op_sel_hi:[0,1,1]
	s_nop 0
	s_nop 0
	v_pk_fma_f32 v[2:3], v[4:5], v[12:13], v[2:3] op_sel_hi:[0,1,1]
	s_nop 0
	s_waitcnt vmcnt(2)
	v_lshlrev_b32_e32 v12, 16, v240
	v_and_b32_e32 v13, 0xffff0000, v240
	v_lshlrev_b32_e32 v10, 16, v241
	v_and_b32_e32 v11, 0xffff0000, v241
	v_pk_fma_f32 v[8:9], v[4:5], v[10:11], v[8:9] op_sel:[1,0,0]
	v_pk_fma_f32 v[2:3], v[4:5], v[12:13], v[2:3] op_sel:[1,0,0]
	s_nop 0
	s_nop 0
	s_nop 0
	s_waitcnt vmcnt(1)
	v_lshlrev_b32_e32 v10, 16, v242
	v_and_b32_e32 v11, 0xffff0000, v242
	v_lshlrev_b32_e32 v4, 16, v243
	v_and_b32_e32 v5, 0xffff0000, v243
	v_pk_fma_f32 v[4:5], v[6:7], v[4:5], v[8:9] op_sel_hi:[0,1,1]
	s_nop 0
	s_nop 0
	v_pk_fma_f32 v[2:3], v[6:7], v[10:11], v[2:3] op_sel_hi:[0,1,1]
	v_mov_b32_e32 v6, v7
	s_nop 0
	s_waitcnt vmcnt(0)
	v_lshlrev_b32_e32 v10, 16, v244
	v_and_b32_e32 v11, 0xffff0000, v244
	v_lshlrev_b32_e32 v8, 16, v245
	v_and_b32_e32 v9, 0xffff0000, v245
	v_pk_fma_f32 v[2:3], v[6:7], v[10:11], v[2:3] op_sel_hi:[0,1,1]
	v_pk_mul_f32 v[12:13], v[6:7], v[8:9] op_sel_hi:[0,1]
	v_pk_mul_f32 v[14:15], v[6:7], v[10:11] op_sel_hi:[0,1]
	v_pk_fma_f32 v[4:5], v[6:7], v[8:9], v[4:5] op_sel_hi:[0,1,1]
	v_pk_fma_f32 v[6:7], v[0:1], v[156:157], v[2:3] op_sel_hi:[0,1,1] neg_lo:[1,0,0] neg_hi:[1,0,0]
	v_pk_fma_f32 v[0:1], v[0:1], v[158:159], v[4:5] op_sel_hi:[0,1,1] neg_lo:[1,0,0] neg_hi:[1,0,0]
	v_pk_fma_f32 v[6:7], v[144:145], v[146:147], v[6:7] op_sel_hi:[0,1,1]
	v_pk_fma_f32 v[4:5], v[92:93], v[4:5], v[12:13] op_sel_hi:[0,1,1] neg_lo:[0,0,1] neg_hi:[0,0,1]
	v_lshlrev_b64 v[12:13], 1, v[140:141]
	v_pk_fma_f32 v[8:9], v[94:95], v[6:7], v[152:153] op_sel_hi:[0,1,1] neg_lo:[0,0,1] neg_hi:[0,0,1]
	v_pk_fma_f32 v[6:7], v[92:93], v[2:3], v[14:15] op_sel_hi:[0,1,1] neg_lo:[0,0,1] neg_hi:[0,0,1]
	v_lshl_add_u64 v[236:237], s[22:23], 0, v[12:13]
	global_load_dwordx2 v[236:237], v[236:237], off offset:3584
	v_lshl_add_u64 v[238:239], s[20:21], 0, v[12:13]
	global_load_dwordx2 v[238:239], v[238:239], off offset:3584
	v_lshl_add_u64 v[14:15], s[22:23], 0, v[12:13]
	s_nop 0
	v_pk_fma_f32 v[0:1], v[144:145], v[150:151], v[0:1] op_sel_hi:[0,1,1]
	v_pk_fma_f32 v[10:11], v[94:95], v[0:1], v[148:149] op_sel_hi:[0,1,1] neg_lo:[0,0,1] neg_hi:[0,0,1]
	v_lshl_add_u32 v0, v142, 2, s17
	ds_read_b128 v[0:3], v0
	s_nop 0
	s_waitcnt vmcnt(1)
	v_lshlrev_b32_e32 v94, 16, v236
	v_and_b32_e32 v95, 0xffff0000, v236
	v_lshlrev_b32_e32 v92, 16, v237
	v_and_b32_e32 v93, 0xffff0000, v237
	s_waitcnt lgkmcnt(0)
	v_pk_fma_f32 v[4:5], v[2:3], v[4:5], v[92:93]
	v_lshl_add_u64 v[92:93], s[20:21], 0, v[12:13]
	s_nop 0
	v_pk_fma_f32 v[6:7], v[0:1], v[6:7], v[94:95]
	s_nop 0
	s_waitcnt vmcnt(0)
	v_lshlrev_b32_e32 v94, 16, v238
	v_and_b32_e32 v95, 0xffff0000, v238
	v_lshlrev_b32_e32 v12, 16, v239
	v_and_b32_e32 v13, 0xffff0000, v239
	v_pk_fma_f32 v[10:11], v[2:3], v[10:11], v[12:13]
	v_pk_fma_f32 v[12:13], v[0:1], v[8:9], v[94:95]
	v_cvt_pk_bf16_f32 v0, v6, v7
	v_cvt_pk_bf16_f32 v1, v4, v5
	s_nop 0
	v_cvt_pk_bf16_f32 v2, v12, v13
	v_cvt_pk_bf16_f32 v3, v10, v11
	global_store_dwordx2 v[14:15], v[0:1], off offset:3584
	global_store_dwordx2 v[92:93], v[2:3], off offset:3584
	v_mul_f32_e32 v0, v87, v87
	v_mul_f32_e32 v1, v85, v85
	v_fmac_f32_e32 v0, v86, v86
	v_fmac_f32_e32 v1, v84, v84
	v_mov_b32_e32 v2, v83
	v_mov_b32_e32 v3, v91
	v_add_f32_e32 v14, v0, v1
	v_mov_b32_e32 v0, v82
	v_mov_b32_e32 v1, v90
	v_pk_mul_f32 v[2:3], v[2:3], v[2:3]
	v_mov_b32_e32 v8, v81
	v_mov_b32_e32 v9, v89
	v_pk_fma_f32 v[0:1], v[0:1], v[0:1], v[2:3]
	v_mov_b32_e32 v2, v80
	v_mov_b32_e32 v3, v88
	v_pk_mul_f32 v[8:9], v[8:9], v[8:9]
	v_mul_f32_e32 v29, v115, v115
	v_pk_fma_f32 v[2:3], v[2:3], v[2:3], v[8:9]
	v_pk_mul_f32 v[8:9], v[102:103], v[102:103]
	v_pk_add_f32 v[0:1], v[0:1], v[2:3]
	v_mul_f32_e32 v2, v99, v99
	v_mul_f32_e32 v3, v97, v97
	v_fmac_f32_e32 v2, v98, v98
	v_fmac_f32_e32 v3, v96, v96
	v_add_f32_e32 v2, v2, v3
	v_add_f32_e32 v27, v14, v2
	v_pk_mul_f32 v[2:3], v[100:101], v[100:101]
	v_pk_add_f32 v[0:1], v[0:1], v[0:1] op_sel:[0,1] op_sel_hi:[1,0]
	v_pk_mov_b32 v[14:15], v[8:9], v[2:3] op_sel:[1,0]
	v_mov_b32_e32 v9, v3
	v_pk_add_f32 v[2:3], v[14:15], v[8:9]
	v_mul_f32_e32 v8, v107, v107
	v_mul_f32_e32 v9, v105, v105
	v_fmac_f32_e32 v8, v106, v106
	v_fmac_f32_e32 v9, v104, v104
	v_add_f32_e32 v8, v8, v9
	v_add_f32_e32 v27, v27, v8
	v_mul_f32_e32 v8, v118, v118
	v_mul_f32_e32 v9, v119, v119
	v_pk_add_f32 v[2:3], v[2:3], v[2:3] op_sel:[0,1] op_sel_hi:[1,0]
	v_mov_b32_e32 v1, v8
	v_mov_b32_e32 v3, v9
	v_pk_add_f32 v[0:1], v[0:1], v[2:3]
	v_mul_f32_e32 v2, v111, v111
	v_mul_f32_e32 v8, v109, v109
	v_mul_f32_e32 v14, v116, v116
	v_mul_f32_e32 v15, v117, v117
	v_pk_fma_f32 v[2:3], v[110:111], v[110:111], v[2:3] op_sel_hi:[1,1,0]
	v_pk_fma_f32 v[8:9], v[108:109], v[108:109], v[8:9] op_sel_hi:[1,1,0]
	v_mov_b32_e32 v3, v14
	v_mov_b32_e32 v9, v15
	v_pk_add_f32 v[2:3], v[2:3], v[8:9]
	v_pk_mul_f32 v[8:9], v[126:127], v[126:127]
	v_pk_add_f32 v[0:1], v[0:1], v[2:3]
	v_pk_mul_f32 v[2:3], v[124:125], v[124:125]
	v_pk_add_f32 v[0:1], v[0:1], v[0:1] op_sel:[0,1] op_sel_hi:[1,0]
	v_pk_mov_b32 v[14:15], v[8:9], v[2:3] op_sel:[1,0]
	v_mov_b32_e32 v9, v3
	v_pk_add_f32 v[2:3], v[14:15], v[8:9]
	v_mul_f32_e32 v8, v6, v6
	v_mul_f32_e32 v9, v7, v7
	v_pk_add_f32 v[2:3], v[2:3], v[2:3] op_sel:[0,1] op_sel_hi:[1,0]
	v_mov_b32_e32 v1, v8
	v_mov_b32_e32 v3, v9
	v_pk_add_f32 v[0:1], v[0:1], v[2:3]
	v_mul_f32_e32 v2, v135, v135
	v_mul_f32_e32 v8, v133, v133
	v_mul_f32_e32 v14, v4, v4
	v_mul_f32_e32 v15, v5, v5
	v_pk_fma_f32 v[2:3], v[134:135], v[134:135], v[2:3] op_sel_hi:[1,1,0]
	v_pk_fma_f32 v[8:9], v[132:133], v[132:133], v[8:9] op_sel_hi:[1,1,0]
	v_mov_b32_e32 v3, v14
	v_mov_b32_e32 v9, v15
	v_pk_add_f32 v[2:3], v[2:3], v[8:9]
	v_mul_f32_e32 v33, v113, v113
	v_pk_add_f32 v[0:1], v[0:1], v[2:3]
	v_xor_b32_e32 v2, 1, v188
	v_add_f32_e32 v0, v0, v1
	v_and_b32_e32 v1, 64, v188
	v_add_u32_e32 v1, 64, v1
	v_cmp_lt_i32_e32 vcc, v2, v1
	v_fmac_f32_e32 v29, v114, v114
	v_fmac_f32_e32 v33, v112, v112
	v_cndmask_b32_e32 v2, v188, v2, vcc
	v_lshlrev_b32_e32 v31, 2, v2
	ds_bpermute_b32 v2, v31, v0
	v_add_f32_e32 v3, v29, v33
	v_mul_f32_e32 v8, v123, v123
	v_mul_f32_e32 v9, v121, v121
	v_fmac_f32_e32 v8, v122, v122
	s_waitcnt lgkmcnt(0)
	v_add_f32_e32 v0, v0, v2
	v_xor_b32_e32 v2, 2, v188
	v_cmp_lt_i32_e32 vcc, v2, v1
	v_fmac_f32_e32 v9, v120, v120
	v_add_f32_e32 v3, v27, v3
	v_cndmask_b32_e32 v2, v188, v2, vcc
	v_lshlrev_b32_e32 v33, 2, v2
	ds_bpermute_b32 v2, v33, v0
	v_add_f32_e32 v8, v8, v9
	v_add_f32_e32 v3, v3, v8
	v_mul_f32_e32 v8, v131, v131
	v_mul_f32_e32 v9, v129, v129
	s_waitcnt lgkmcnt(0)
	v_add_f32_e32 v0, v0, v2
	v_xor_b32_e32 v2, 4, v188
	v_cmp_lt_i32_e32 vcc, v2, v1
	v_fmac_f32_e32 v8, v130, v130
	v_fmac_f32_e32 v9, v128, v128
	v_cndmask_b32_e32 v2, v188, v2, vcc
	v_lshlrev_b32_e32 v35, 2, v2
	ds_bpermute_b32 v2, v35, v0
	v_add_f32_e32 v8, v8, v9
	v_add_f32_e32 v3, v3, v8
	v_mul_f32_e32 v8, v139, v139
	v_mul_f32_e32 v9, v137, v137
	s_waitcnt lgkmcnt(0)
	v_add_f32_e32 v0, v0, v2
	v_xor_b32_e32 v2, 8, v188
	v_cmp_lt_i32_e32 vcc, v2, v1
	v_fmac_f32_e32 v8, v138, v138
	v_fmac_f32_e32 v9, v136, v136
	v_cndmask_b32_e32 v2, v188, v2, vcc
	v_lshlrev_b32_e32 v41, 2, v2
	ds_bpermute_b32 v2, v41, v0
	v_add_f32_e32 v8, v8, v9
	s_waitcnt lgkmcnt(0)
	v_add_f32_e32 v0, v0, v2
	v_xor_b32_e32 v2, 16, v188
	v_cmp_lt_i32_e32 vcc, v2, v1
	s_nop 1
	v_cndmask_b32_e32 v2, v188, v2, vcc
	v_lshlrev_b32_e32 v37, 2, v2
	ds_bpermute_b32 v2, v37, v0
	s_waitcnt lgkmcnt(0)
	v_add_f32_e32 v0, v0, v2
	v_xor_b32_e32 v2, 32, v188
	v_cmp_lt_i32_e32 vcc, v2, v1
	s_nop 1
	v_cndmask_b32_e32 v1, v188, v2, vcc
	v_lshlrev_b32_e32 v39, 2, v1
	ds_bpermute_b32 v1, v39, v0
	v_add_f32_e32 v2, v3, v8
	v_mul_f32_e32 v3, v13, v13
	v_mul_f32_e32 v8, v11, v11
	v_fmac_f32_e32 v3, v12, v12
	s_waitcnt lgkmcnt(0)
	v_add_f32_e32 v0, v0, v1
	v_fmamk_f32 v0, v0, 0x3a000000, v189
	v_mul_f32_e32 v1, 0x4f800000, v0
	v_cmp_gt_f32_e32 vcc, s84, v0
	v_fmac_f32_e32 v8, v10, v10
	v_add_f32_e32 v3, v3, v8
	v_cndmask_b32_e32 v0, v0, v1, vcc
	v_sqrt_f32_e32 v1, v0
	v_add_f32_e32 v2, v2, v3
	v_add_u32_e32 v3, -1, v1
	v_fma_f32 v8, -v3, v1, v0
	v_cmp_ge_f32_e64 s[46:47], 0, v8
	v_add_u32_e32 v8, 1, v1
	s_nop 0
	v_cndmask_b32_e64 v3, v1, v3, s[46:47]
	v_fma_f32 v1, -v8, v1, v0
	v_cmp_lt_f32_e64 s[46:47], 0, v1
	s_nop 1
	v_cndmask_b32_e64 v1, v3, v8, s[46:47]
	v_mul_f32_e32 v3, 0x37800000, v1
	v_cndmask_b32_e32 v1, v1, v3, vcc
	ds_bpermute_b32 v3, v31, v2
	v_cmp_class_f32_e32 vcc, v0, v190
	v_cmp_eq_u32_e64 s[46:47], 1, v20
	s_nop 0
	v_cndmask_b32_e32 v27, v1, v0, vcc
	s_waitcnt lgkmcnt(0)
	v_add_f32_e32 v0, v2, v3
	ds_bpermute_b32 v1, v33, v0
	v_div_scale_f32 v43, s[0:1], v27, v27, 1.0
	v_rcp_f32_e32 v29, v43
	v_div_scale_f32 v47, vcc, 1.0, v27, 1.0
	s_waitcnt lgkmcnt(0)
	v_add_f32_e32 v0, v0, v1
	ds_bpermute_b32 v1, v35, v0
	v_fma_f32 v2, -v43, v29, 1.0
	v_fmac_f32_e32 v29, v2, v29
	v_mul_f32_e32 v45, v47, v29
	v_fma_f32 v51, -v43, v45, v47
	s_waitcnt lgkmcnt(0)
	v_add_f32_e32 v49, v0, v1
	ds_read_b128 v[0:3], v25
	ds_read_b128 v[92:95], v25 offset:1024
	ds_read_b128 v[140:143], v25 offset:2048
	ds_read_b128 v[144:147], v25 offset:3072
	ds_read_b128 v[148:151], v25 offset:4096
	ds_read_b128 v[152:155], v25 offset:5120
	ds_read_b128 v[156:159], v25 offset:6144
	ds_read_b128 v[160:163], v25 offset:7168
	ds_read_b128 v[164:167], v25 offset:8192
	ds_read_b128 v[174:177], v25 offset:9216
	ds_read_b128 v[178:181], v25 offset:10240
	ds_read_b128 v[182:185], v25 offset:11264
	ds_read_b128 v[198:201], v25 offset:12288
	ds_read_b128 v[202:205], v25 offset:13312
	ds_read_b128 v[206:209], v25 offset:14336
	ds_read_b128 v[210:213], v25 offset:15360
	s_waitcnt lgkmcnt(7)
	v_mov_b32_e32 v8, v164
	v_mov_b32_e32 v9, v1
	v_mov_b32_e32 v1, v165
	v_mov_b32_e32 v164, v166
	v_mov_b32_e32 v165, v3
	v_pk_mul_f32 v[14:15], v[82:83], v[8:9]
	v_pk_mul_f32 v[214:215], v[80:81], v[164:165]
	v_mov_b32_e32 v3, v167
	v_pk_fma_f32 v[14:15], v[82:83], v[0:1], v[14:15] op_sel:[0,0,1] op_sel_hi:[1,1,0]
	v_pk_fma_f32 v[166:167], v[80:81], v[2:3], v[214:215] op_sel:[0,0,1] op_sel_hi:[1,1,0]
	v_pk_mul_f32 v[8:9], v[86:87], v[8:9]
	v_pk_add_f32 v[14:15], v[14:15], v[166:167]
	s_waitcnt lgkmcnt(6)
	v_mov_b32_e32 v166, v174
	v_mov_b32_e32 v167, v93
	v_pk_mul_f32 v[214:215], v[90:91], v[166:167]
	v_mov_b32_e32 v93, v175
	v_pk_fma_f32 v[174:175], v[90:91], v[92:93], v[214:215] op_sel:[0,0,1] op_sel_hi:[1,1,0]
	v_mov_b32_e32 v214, v176
	v_mov_b32_e32 v215, v95
	v_pk_mul_f32 v[216:217], v[88:89], v[214:215]
	v_mov_b32_e32 v95, v177
	v_pk_fma_f32 v[176:177], v[88:89], v[94:95], v[216:217] op_sel:[0,0,1] op_sel_hi:[1,1,0]
	v_pk_add_f32 v[14:15], v[14:15], 0 op_sel_hi:[1,0]
	v_pk_add_f32 v[174:175], v[174:175], v[176:177]
	v_pk_fma_f32 v[0:1], v[86:87], v[0:1], v[8:9] op_sel:[0,0,1] op_sel_hi:[1,1,0]
	v_pk_add_f32 v[14:15], v[14:15], v[174:175]
	s_waitcnt lgkmcnt(5)
	v_mov_b32_e32 v174, v178
	v_mov_b32_e32 v175, v141
	v_mov_b32_e32 v141, v179
	v_mov_b32_e32 v178, v180
	v_mov_b32_e32 v179, v143
	v_pk_mul_f32 v[176:177], v[102:103], v[174:175]
	v_pk_mul_f32 v[216:217], v[100:101], v[178:179]
	v_mov_b32_e32 v143, v181
	v_pk_mul_f32 v[8:9], v[84:85], v[164:165]
	v_pk_fma_f32 v[176:177], v[102:103], v[140:141], v[176:177] op_sel:[0,0,1] op_sel_hi:[1,1,0]
	v_pk_fma_f32 v[180:181], v[100:101], v[142:143], v[216:217] op_sel:[0,0,1] op_sel_hi:[1,1,0]
	v_pk_fma_f32 v[2:3], v[84:85], v[2:3], v[8:9] op_sel:[0,0,1] op_sel_hi:[1,1,0]
	v_pk_add_f32 v[176:177], v[176:177], v[180:181]
	v_pk_add_f32 v[0:1], v[0:1], v[2:3]
	v_pk_mul_f32 v[2:3], v[98:99], v[166:167]
	v_pk_mul_f32 v[8:9], v[96:97], v[214:215]
	v_pk_add_f32 v[14:15], v[14:15], v[176:177]
	s_waitcnt lgkmcnt(4)
	v_mov_b32_e32 v176, v182
	v_mov_b32_e32 v177, v145
	v_mov_b32_e32 v145, v183
	v_mov_b32_e32 v182, v184
	v_mov_b32_e32 v183, v147
	v_pk_fma_f32 v[2:3], v[98:99], v[92:93], v[2:3] op_sel:[0,0,1] op_sel_hi:[1,1,0]
	v_pk_fma_f32 v[8:9], v[96:97], v[94:95], v[8:9] op_sel:[0,0,1] op_sel_hi:[1,1,0]
	v_pk_mul_f32 v[180:181], v[110:111], v[176:177]
	v_pk_mul_f32 v[216:217], v[108:109], v[182:183]
	v_mov_b32_e32 v147, v185
	v_pk_add_f32 v[0:1], v[0:1], 0 op_sel_hi:[1,0]
	v_pk_add_f32 v[2:3], v[2:3], v[8:9]
	v_pk_fma_f32 v[180:181], v[110:111], v[144:145], v[180:181] op_sel:[0,0,1] op_sel_hi:[1,1,0]
	v_pk_fma_f32 v[184:185], v[108:109], v[146:147], v[216:217] op_sel:[0,0,1] op_sel_hi:[1,1,0]
	v_pk_add_f32 v[0:1], v[0:1], v[2:3]
	v_pk_mul_f32 v[2:3], v[106:107], v[174:175]
	v_pk_mul_f32 v[8:9], v[104:105], v[178:179]
	v_pk_add_f32 v[180:181], v[180:181], v[184:185]
	v_pk_fma_f32 v[2:3], v[106:107], v[140:141], v[2:3] op_sel:[0,0,1] op_sel_hi:[1,1,0]
	v_pk_fma_f32 v[8:9], v[104:105], v[142:143], v[8:9] op_sel:[0,0,1] op_sel_hi:[1,1,0]
	v_pk_add_f32 v[14:15], v[14:15], v[180:181]
	s_waitcnt lgkmcnt(3)
	v_mov_b32_e32 v180, v198
	v_mov_b32_e32 v181, v149
	v_mov_b32_e32 v149, v199
	v_mov_b32_e32 v198, v200
	v_mov_b32_e32 v199, v151
	v_pk_add_f32 v[2:3], v[2:3], v[8:9]
	v_pk_mul_f32 v[184:185], v[118:119], v[180:181]
	v_pk_mul_f32 v[216:217], v[116:117], v[198:199]
	v_mov_b32_e32 v151, v201
	v_pk_add_f32 v[0:1], v[0:1], v[2:3]
	v_pk_mul_f32 v[2:3], v[114:115], v[176:177]
	v_pk_mul_f32 v[8:9], v[112:113], v[182:183]
	v_pk_fma_f32 v[184:185], v[118:119], v[148:149], v[184:185] op_sel:[0,0,1] op_sel_hi:[1,1,0]
	v_pk_fma_f32 v[200:201], v[116:117], v[150:151], v[216:217] op_sel:[0,0,1] op_sel_hi:[1,1,0]
	v_pk_fma_f32 v[2:3], v[114:115], v[144:145], v[2:3] op_sel:[0,0,1] op_sel_hi:[1,1,0]
	v_pk_fma_f32 v[8:9], v[112:113], v[146:147], v[8:9] op_sel:[0,0,1] op_sel_hi:[1,1,0]
	v_pk_add_f32 v[184:185], v[184:185], v[200:201]
	v_pk_add_f32 v[2:3], v[2:3], v[8:9]
	v_pk_add_f32 v[14:15], v[14:15], v[184:185]
	s_waitcnt lgkmcnt(2)
	v_mov_b32_e32 v184, v202
	v_mov_b32_e32 v185, v153
	v_mov_b32_e32 v153, v203
	v_mov_b32_e32 v202, v204
	v_mov_b32_e32 v203, v155
	v_pk_add_f32 v[0:1], v[0:1], v[2:3]
	v_pk_mul_f32 v[2:3], v[122:123], v[180:181]
	v_pk_mul_f32 v[8:9], v[120:121], v[198:199]
	v_pk_mul_f32 v[200:201], v[126:127], v[184:185]
	v_pk_mul_f32 v[216:217], v[124:125], v[202:203]
	v_mov_b32_e32 v155, v205
	v_pk_fma_f32 v[2:3], v[122:123], v[148:149], v[2:3] op_sel:[0,0,1] op_sel_hi:[1,1,0]
	v_pk_fma_f32 v[8:9], v[120:121], v[150:151], v[8:9] op_sel:[0,0,1] op_sel_hi:[1,1,0]
	v_pk_fma_f32 v[200:201], v[126:127], v[152:153], v[200:201] op_sel:[0,0,1] op_sel_hi:[1,1,0]
	v_pk_fma_f32 v[204:205], v[124:125], v[154:155], v[216:217] op_sel:[0,0,1] op_sel_hi:[1,1,0]
	v_pk_add_f32 v[2:3], v[2:3], v[8:9]
	v_pk_add_f32 v[200:201], v[200:201], v[204:205]
	v_pk_add_f32 v[0:1], v[0:1], v[2:3]
	v_pk_mul_f32 v[2:3], v[130:131], v[184:185]
	v_pk_mul_f32 v[8:9], v[128:129], v[202:203]
	v_pk_add_f32 v[14:15], v[14:15], v[200:201]
	s_waitcnt lgkmcnt(1)
	v_mov_b32_e32 v200, v206
	v_mov_b32_e32 v201, v157
	v_mov_b32_e32 v157, v207
	v_mov_b32_e32 v206, v208
	v_mov_b32_e32 v207, v159
	v_pk_fma_f32 v[2:3], v[130:131], v[152:153], v[2:3] op_sel:[0,0,1] op_sel_hi:[1,1,0]
	v_pk_fma_f32 v[8:9], v[128:129], v[154:155], v[8:9] op_sel:[0,0,1] op_sel_hi:[1,1,0]
	v_pk_mul_f32 v[204:205], v[134:135], v[200:201]
	v_pk_mul_f32 v[216:217], v[132:133], v[206:207]
	v_mov_b32_e32 v159, v209
	v_pk_add_f32 v[2:3], v[2:3], v[8:9]
	v_pk_fma_f32 v[204:205], v[134:135], v[156:157], v[204:205] op_sel:[0,0,1] op_sel_hi:[1,1,0]
	v_pk_fma_f32 v[208:209], v[132:133], v[158:159], v[216:217] op_sel:[0,0,1] op_sel_hi:[1,1,0]
	v_pk_add_f32 v[0:1], v[0:1], v[2:3]
	v_pk_mul_f32 v[2:3], v[138:139], v[200:201]
	v_pk_mul_f32 v[8:9], v[136:137], v[206:207]
	v_pk_add_f32 v[204:205], v[204:205], v[208:209]
	v_pk_fma_f32 v[2:3], v[138:139], v[156:157], v[2:3] op_sel:[0,0,1] op_sel_hi:[1,1,0]
	v_pk_fma_f32 v[8:9], v[136:137], v[158:159], v[8:9] op_sel:[0,0,1] op_sel_hi:[1,1,0]
	v_pk_add_f32 v[14:15], v[14:15], v[204:205]
	s_waitcnt lgkmcnt(0)
	v_mov_b32_e32 v204, v210
	v_mov_b32_e32 v205, v161
	v_mov_b32_e32 v161, v211
	v_mov_b32_e32 v210, v212
	v_mov_b32_e32 v211, v163
	v_pk_add_f32 v[2:3], v[2:3], v[8:9]
	v_pk_mul_f32 v[208:209], v[6:7], v[204:205]
	v_pk_mul_f32 v[216:217], v[4:5], v[210:211]
	v_mov_b32_e32 v163, v213
	v_pk_add_f32 v[0:1], v[0:1], v[2:3]
	v_pk_mul_f32 v[2:3], v[12:13], v[204:205]
	v_pk_mul_f32 v[8:9], v[10:11], v[210:211]
	v_pk_fma_f32 v[208:209], v[6:7], v[160:161], v[208:209] op_sel:[0,0,1] op_sel_hi:[1,1,0]
	v_pk_fma_f32 v[212:213], v[4:5], v[162:163], v[216:217] op_sel:[0,0,1] op_sel_hi:[1,1,0]
	v_pk_fma_f32 v[2:3], v[12:13], v[160:161], v[2:3] op_sel:[0,0,1] op_sel_hi:[1,1,0]
	v_pk_fma_f32 v[8:9], v[10:11], v[162:163], v[8:9] op_sel:[0,0,1] op_sel_hi:[1,1,0]
	v_pk_add_f32 v[208:209], v[208:209], v[212:213]
	v_pk_add_f32 v[2:3], v[2:3], v[8:9]
	v_pk_add_f32 v[14:15], v[14:15], v[208:209]
	v_pk_add_f32 v[0:1], v[0:1], v[2:3]
	ds_read_b128 v[140:143], v25 offset:16384
	ds_read_b128 v[144:147], v25 offset:17408
	ds_read_b128 v[148:151], v25 offset:18432
	ds_read_b128 v[152:155], v25 offset:19456
	ds_read_b128 v[156:159], v25 offset:20480
	ds_read_b128 v[160:163], v25 offset:21504
	ds_read_b128 v[164:167], v25 offset:22528
	ds_read_b128 v[174:177], v25 offset:23552
	ds_read_b128 v[92:95], v25 offset:24576
	ds_read_b128 v[178:181], v25 offset:25600
	ds_read_b128 v[182:185], v25 offset:26624
	ds_read_b128 v[198:201], v25 offset:27648
	ds_read_b128 v[202:205], v25 offset:28672
	ds_read_b128 v[206:209], v25 offset:29696
	ds_read_b128 v[210:213], v25 offset:30720
	ds_read_b128 v[214:217], v25 offset:31744
	s_waitcnt lgkmcnt(7)
	v_mov_b32_e32 v2, v92
	v_mov_b32_e32 v3, v141
	v_mov_b32_e32 v218, v94
	v_mov_b32_e32 v219, v143
	v_pk_mul_f32 v[8:9], v[82:83], v[2:3]
	v_mov_b32_e32 v141, v93
	v_pk_mul_f32 v[92:93], v[80:81], v[218:219]
	v_mov_b32_e32 v143, v95
	v_pk_fma_f32 v[8:9], v[82:83], v[140:141], v[8:9] op_sel:[0,0,1] op_sel_hi:[1,1,0]
	v_pk_fma_f32 v[92:93], v[80:81], v[142:143], v[92:93] op_sel:[0,0,1] op_sel_hi:[1,1,0]
	s_waitcnt lgkmcnt(6)
	v_mov_b32_e32 v94, v178
	v_mov_b32_e32 v95, v145
	v_mov_b32_e32 v145, v179
	v_mov_b32_e32 v178, v180
	v_mov_b32_e32 v179, v147
	v_pk_add_f32 v[8:9], v[8:9], v[92:93]
	v_pk_mul_f32 v[92:93], v[90:91], v[94:95]
	v_pk_mul_f32 v[224:225], v[88:89], v[178:179]
	v_mov_b32_e32 v147, v181
	v_pk_fma_f32 v[92:93], v[90:91], v[144:145], v[92:93] op_sel:[0,0,1] op_sel_hi:[1,1,0]
	v_pk_fma_f32 v[180:181], v[88:89], v[146:147], v[224:225] op_sel:[0,0,1] op_sel_hi:[1,1,0]
	v_pk_add_f32 v[8:9], v[8:9], 0 op_sel_hi:[1,0]
	v_pk_add_f32 v[92:93], v[92:93], v[180:181]
	s_waitcnt lgkmcnt(5)
	v_mov_b32_e32 v180, v182
	v_mov_b32_e32 v181, v149
	v_mov_b32_e32 v149, v183
	v_mov_b32_e32 v182, v184
	v_mov_b32_e32 v183, v151
	v_pk_add_f32 v[8:9], v[8:9], v[92:93]
	v_pk_mul_f32 v[92:93], v[102:103], v[180:181]
	v_pk_mul_f32 v[224:225], v[100:101], v[182:183]
	v_mov_b32_e32 v151, v185
	v_pk_fma_f32 v[92:93], v[102:103], v[148:149], v[92:93] op_sel:[0,0,1] op_sel_hi:[1,1,0]
	v_pk_fma_f32 v[184:185], v[100:101], v[150:151], v[224:225] op_sel:[0,0,1] op_sel_hi:[1,1,0]
	v_pk_mul_f32 v[2:3], v[86:87], v[2:3]
	v_pk_add_f32 v[92:93], v[92:93], v[184:185]
	s_waitcnt lgkmcnt(4)
	v_mov_b32_e32 v184, v198
	v_mov_b32_e32 v185, v153
	v_mov_b32_e32 v153, v199
	v_mov_b32_e32 v198, v200
	v_mov_b32_e32 v199, v155
	v_pk_add_f32 v[8:9], v[8:9], v[92:93]
	v_pk_mul_f32 v[92:93], v[110:111], v[184:185]
	v_pk_mul_f32 v[224:225], v[108:109], v[198:199]
	v_mov_b32_e32 v155, v201
	v_pk_fma_f32 v[92:93], v[110:111], v[152:153], v[92:93] op_sel:[0,0,1] op_sel_hi:[1,1,0]
	v_pk_fma_f32 v[200:201], v[108:109], v[154:155], v[224:225] op_sel:[0,0,1] op_sel_hi:[1,1,0]
	v_pk_fma_f32 v[2:3], v[86:87], v[140:141], v[2:3] op_sel:[0,0,1] op_sel_hi:[1,1,0]
	v_pk_add_f32 v[92:93], v[92:93], v[200:201]
	s_waitcnt lgkmcnt(3)
	v_mov_b32_e32 v200, v202
	v_mov_b32_e32 v201, v157
	v_mov_b32_e32 v157, v203
	v_mov_b32_e32 v202, v204
	v_mov_b32_e32 v203, v159
	v_pk_add_f32 v[8:9], v[8:9], v[92:93]
	v_pk_mul_f32 v[92:93], v[118:119], v[200:201]
	v_pk_mul_f32 v[224:225], v[116:117], v[202:203]
	v_mov_b32_e32 v159, v205
	v_pk_fma_f32 v[92:93], v[118:119], v[156:157], v[92:93] op_sel:[0,0,1] op_sel_hi:[1,1,0]
	v_pk_fma_f32 v[204:205], v[116:117], v[158:159], v[224:225] op_sel:[0,0,1] op_sel_hi:[1,1,0]
	ds_bpermute_b32 v53, v41, v49
	v_pk_add_f32 v[92:93], v[92:93], v[204:205]
	s_waitcnt lgkmcnt(3)
	v_mov_b32_e32 v204, v206
	v_mov_b32_e32 v205, v161
	v_mov_b32_e32 v161, v207
	v_mov_b32_e32 v206, v208
	v_mov_b32_e32 v207, v163
	v_pk_add_f32 v[8:9], v[8:9], v[92:93]
	v_pk_mul_f32 v[92:93], v[126:127], v[204:205]
	v_pk_mul_f32 v[224:225], v[124:125], v[206:207]
	v_mov_b32_e32 v163, v209
	v_pk_fma_f32 v[92:93], v[126:127], v[160:161], v[92:93] op_sel:[0,0,1] op_sel_hi:[1,1,0]
	v_pk_fma_f32 v[208:209], v[124:125], v[162:163], v[224:225] op_sel:[0,0,1] op_sel_hi:[1,1,0]
	v_fmac_f32_e32 v45, v51, v29
	v_pk_add_f32 v[92:93], v[92:93], v[208:209]
	s_waitcnt lgkmcnt(2)
	v_mov_b32_e32 v208, v210
	v_mov_b32_e32 v209, v165
	v_mov_b32_e32 v165, v211
	v_mov_b32_e32 v210, v212
	v_mov_b32_e32 v211, v167
	v_pk_add_f32 v[8:9], v[8:9], v[92:93]
	v_pk_mul_f32 v[92:93], v[134:135], v[208:209]
	v_pk_mul_f32 v[224:225], v[132:133], v[210:211]
	v_mov_b32_e32 v167, v213
	v_pk_fma_f32 v[92:93], v[134:135], v[164:165], v[92:93] op_sel:[0,0,1] op_sel_hi:[1,1,0]
	v_pk_fma_f32 v[212:213], v[132:133], v[166:167], v[224:225] op_sel:[0,0,1] op_sel_hi:[1,1,0]
	s_nop 0
	v_pk_add_f32 v[92:93], v[92:93], v[212:213]
	s_waitcnt lgkmcnt(1)
	v_mov_b32_e32 v212, v214
	v_mov_b32_e32 v213, v175
	v_mov_b32_e32 v175, v215
	v_mov_b32_e32 v214, v216
	v_mov_b32_e32 v215, v177
	v_pk_add_f32 v[8:9], v[8:9], v[92:93]
	v_pk_mul_f32 v[92:93], v[6:7], v[212:213]
	v_pk_mul_f32 v[224:225], v[4:5], v[214:215]
	v_mov_b32_e32 v177, v217
	v_pk_fma_f32 v[92:93], v[6:7], v[174:175], v[92:93] op_sel:[0,0,1] op_sel_hi:[1,1,0]
	v_pk_fma_f32 v[216:217], v[4:5], v[176:177], v[224:225] op_sel:[0,0,1] op_sel_hi:[1,1,0]
	s_nop 0
	v_pk_add_f32 v[92:93], v[92:93], v[216:217]
	s_nop 0
	v_pk_add_f32 v[92:93], v[8:9], v[92:93]
	v_pk_mul_f32 v[8:9], v[84:85], v[218:219]
	s_nop 0
	v_pk_fma_f32 v[8:9], v[84:85], v[142:143], v[8:9] op_sel:[0,0,1] op_sel_hi:[1,1,0]
	s_nop 0
	v_pk_add_f32 v[2:3], v[2:3], v[8:9]
	v_pk_mul_f32 v[8:9], v[98:99], v[94:95]
	v_pk_mul_f32 v[94:95], v[96:97], v[178:179]
	v_pk_fma_f32 v[8:9], v[98:99], v[144:145], v[8:9] op_sel:[0,0,1] op_sel_hi:[1,1,0]
	v_pk_fma_f32 v[94:95], v[96:97], v[146:147], v[94:95] op_sel:[0,0,1] op_sel_hi:[1,1,0]
	v_pk_add_f32 v[2:3], v[2:3], 0 op_sel_hi:[1,0]
	v_pk_add_f32 v[8:9], v[8:9], v[94:95]
	v_pk_mul_f32 v[94:95], v[104:105], v[182:183]
	v_pk_add_f32 v[2:3], v[2:3], v[8:9]
	v_pk_mul_f32 v[8:9], v[106:107], v[180:181]
	v_pk_fma_f32 v[94:95], v[104:105], v[150:151], v[94:95] op_sel:[0,0,1] op_sel_hi:[1,1,0]
	v_pk_fma_f32 v[8:9], v[106:107], v[148:149], v[8:9] op_sel:[0,0,1] op_sel_hi:[1,1,0]
	s_nop 0
	v_pk_add_f32 v[8:9], v[8:9], v[94:95]
	v_pk_mul_f32 v[94:95], v[112:113], v[198:199]
	v_pk_add_f32 v[2:3], v[2:3], v[8:9]
	v_pk_mul_f32 v[8:9], v[114:115], v[184:185]
	v_pk_fma_f32 v[94:95], v[112:113], v[154:155], v[94:95] op_sel:[0,0,1] op_sel_hi:[1,1,0]
	v_pk_fma_f32 v[8:9], v[114:115], v[152:153], v[8:9] op_sel:[0,0,1] op_sel_hi:[1,1,0]
	s_nop 0
	v_pk_add_f32 v[8:9], v[8:9], v[94:95]
	v_pk_mul_f32 v[94:95], v[120:121], v[202:203]
	v_pk_add_f32 v[2:3], v[2:3], v[8:9]
	v_pk_mul_f32 v[8:9], v[122:123], v[200:201]
	v_pk_fma_f32 v[94:95], v[120:121], v[158:159], v[94:95] op_sel:[0,0,1] op_sel_hi:[1,1,0]
	v_pk_fma_f32 v[8:9], v[122:123], v[156:157], v[8:9] op_sel:[0,0,1] op_sel_hi:[1,1,0]
	s_nop 0
	v_pk_add_f32 v[8:9], v[8:9], v[94:95]
	v_pk_mul_f32 v[94:95], v[128:129], v[206:207]
	v_pk_add_f32 v[2:3], v[2:3], v[8:9]
	v_pk_mul_f32 v[8:9], v[130:131], v[204:205]
	v_pk_fma_f32 v[94:95], v[128:129], v[162:163], v[94:95] op_sel:[0,0,1] op_sel_hi:[1,1,0]
	v_pk_fma_f32 v[8:9], v[130:131], v[160:161], v[8:9] op_sel:[0,0,1] op_sel_hi:[1,1,0]
	s_nop 0
	v_pk_add_f32 v[8:9], v[8:9], v[94:95]
	v_pk_mul_f32 v[94:95], v[136:137], v[210:211]
	v_pk_add_f32 v[2:3], v[2:3], v[8:9]
	v_pk_mul_f32 v[8:9], v[138:139], v[208:209]
	v_pk_fma_f32 v[94:95], v[136:137], v[166:167], v[94:95] op_sel:[0,0,1] op_sel_hi:[1,1,0]
	v_pk_fma_f32 v[8:9], v[138:139], v[164:165], v[8:9] op_sel:[0,0,1] op_sel_hi:[1,1,0]
	s_nop 0
	v_pk_add_f32 v[8:9], v[8:9], v[94:95]
	v_pk_mul_f32 v[94:95], v[10:11], v[214:215]
	v_pk_add_f32 v[2:3], v[2:3], v[8:9]
	v_pk_mul_f32 v[8:9], v[12:13], v[212:213]
	v_pk_fma_f32 v[94:95], v[10:11], v[176:177], v[94:95] op_sel:[0,0,1] op_sel_hi:[1,1,0]
	v_pk_fma_f32 v[8:9], v[12:13], v[174:175], v[8:9] op_sel:[0,0,1] op_sel_hi:[1,1,0]
	ds_read_b128 v[140:143], v25 offset:32768
	ds_read_b128 v[144:147], v25 offset:33792
	ds_read_b128 v[148:151], v25 offset:34816
	ds_read_b128 v[152:155], v25 offset:35840
	ds_read_b128 v[156:159], v25 offset:36864
	ds_read_b128 v[160:163], v25 offset:37888
	ds_read_b128 v[164:167], v25 offset:38912
	ds_read_b128 v[174:177], v25 offset:39936
	ds_read_b128 v[178:181], v25 offset:40960
	ds_read_b128 v[182:185], v25 offset:41984
	ds_read_b128 v[198:201], v25 offset:43008
	ds_read_b128 v[202:205], v25 offset:44032
	ds_read_b128 v[206:209], v25 offset:45056
	ds_read_b128 v[210:213], v25 offset:46080
	ds_read_b128 v[214:217], v25 offset:47104
	ds_read_b128 v[224:227], v25 offset:48128
	v_pk_add_f32 v[8:9], v[8:9], v[94:95]
	s_nop 0
	v_pk_add_f32 v[2:3], v[2:3], v[8:9]
	s_waitcnt lgkmcnt(7)
	v_mov_b32_e32 v8, v178
	v_mov_b32_e32 v9, v141
	v_mov_b32_e32 v141, v179
	v_mov_b32_e32 v178, v180
	v_mov_b32_e32 v179, v143
	v_pk_mul_f32 v[94:95], v[82:83], v[8:9]
	v_pk_mul_f32 v[218:219], v[80:81], v[178:179]
	v_mov_b32_e32 v143, v181
	v_pk_fma_f32 v[94:95], v[82:83], v[140:141], v[94:95] op_sel:[0,0,1] op_sel_hi:[1,1,0]
	v_pk_fma_f32 v[180:181], v[80:81], v[142:143], v[218:219] op_sel:[0,0,1] op_sel_hi:[1,1,0]
	v_pk_mul_f32 v[8:9], v[86:87], v[8:9]
	v_pk_add_f32 v[94:95], v[94:95], v[180:181]
	s_waitcnt lgkmcnt(6)
	v_mov_b32_e32 v180, v182
	v_mov_b32_e32 v181, v145
	v_pk_mul_f32 v[218:219], v[90:91], v[180:181]
	v_mov_b32_e32 v145, v183
	v_pk_fma_f32 v[182:183], v[90:91], v[144:145], v[218:219] op_sel:[0,0,1] op_sel_hi:[1,1,0]
	v_mov_b32_e32 v218, v184
	v_mov_b32_e32 v219, v147
	v_pk_mul_f32 v[228:229], v[88:89], v[218:219]
	v_mov_b32_e32 v147, v185
	v_pk_fma_f32 v[184:185], v[88:89], v[146:147], v[228:229] op_sel:[0,0,1] op_sel_hi:[1,1,0]
	v_pk_add_f32 v[94:95], v[94:95], 0 op_sel_hi:[1,0]
	v_pk_add_f32 v[182:183], v[182:183], v[184:185]
	v_pk_fma_f32 v[8:9], v[86:87], v[140:141], v[8:9] op_sel:[0,0,1] op_sel_hi:[1,1,0]
	v_pk_add_f32 v[94:95], v[94:95], v[182:183]
	s_waitcnt lgkmcnt(5)
	v_mov_b32_e32 v182, v198
	v_mov_b32_e32 v183, v149
	v_mov_b32_e32 v149, v199
	v_mov_b32_e32 v198, v200
	v_mov_b32_e32 v199, v151
	v_pk_mul_f32 v[184:185], v[102:103], v[182:183]
	v_pk_mul_f32 v[228:229], v[100:101], v[198:199]
	v_mov_b32_e32 v151, v201
	v_pk_mul_f32 v[140:141], v[84:85], v[178:179]
	v_pk_fma_f32 v[184:185], v[102:103], v[148:149], v[184:185] op_sel:[0,0,1] op_sel_hi:[1,1,0]
	v_pk_fma_f32 v[200:201], v[100:101], v[150:151], v[228:229] op_sel:[0,0,1] op_sel_hi:[1,1,0]
	v_pk_fma_f32 v[140:141], v[84:85], v[142:143], v[140:141] op_sel:[0,0,1] op_sel_hi:[1,1,0]
	v_pk_add_f32 v[184:185], v[184:185], v[200:201]
	v_pk_add_f32 v[8:9], v[8:9], v[140:141]
	v_pk_mul_f32 v[140:141], v[98:99], v[180:181]
	v_pk_mul_f32 v[142:143], v[96:97], v[218:219]
	v_pk_add_f32 v[94:95], v[94:95], v[184:185]
	s_waitcnt lgkmcnt(4)
	v_mov_b32_e32 v184, v202
	v_mov_b32_e32 v185, v153
	v_mov_b32_e32 v153, v203
	v_mov_b32_e32 v202, v204
	v_mov_b32_e32 v203, v155
	v_pk_fma_f32 v[140:141], v[98:99], v[144:145], v[140:141] op_sel:[0,0,1] op_sel_hi:[1,1,0]
	v_pk_fma_f32 v[142:143], v[96:97], v[146:147], v[142:143] op_sel:[0,0,1] op_sel_hi:[1,1,0]
	v_pk_mul_f32 v[200:201], v[110:111], v[184:185]
	v_pk_mul_f32 v[228:229], v[108:109], v[202:203]
	v_mov_b32_e32 v155, v205
	v_pk_add_f32 v[8:9], v[8:9], 0 op_sel_hi:[1,0]
	v_pk_add_f32 v[140:141], v[140:141], v[142:143]
	v_pk_fma_f32 v[200:201], v[110:111], v[152:153], v[200:201] op_sel:[0,0,1] op_sel_hi:[1,1,0]
	v_pk_fma_f32 v[204:205], v[108:109], v[154:155], v[228:229] op_sel:[0,0,1] op_sel_hi:[1,1,0]
	v_pk_add_f32 v[8:9], v[8:9], v[140:141]
	v_pk_mul_f32 v[140:141], v[106:107], v[182:183]
	v_pk_mul_f32 v[142:143], v[104:105], v[198:199]
	v_pk_add_f32 v[200:201], v[200:201], v[204:205]
	v_pk_fma_f32 v[140:141], v[106:107], v[148:149], v[140:141] op_sel:[0,0,1] op_sel_hi:[1,1,0]
	v_pk_fma_f32 v[142:143], v[104:105], v[150:151], v[142:143] op_sel:[0,0,1] op_sel_hi:[1,1,0]
	v_pk_add_f32 v[94:95], v[94:95], v[200:201]
	s_waitcnt lgkmcnt(3)
	v_mov_b32_e32 v200, v206
	v_mov_b32_e32 v201, v157
	v_mov_b32_e32 v157, v207
	v_mov_b32_e32 v206, v208
	v_mov_b32_e32 v207, v159
	v_pk_add_f32 v[140:141], v[140:141], v[142:143]
	v_pk_mul_f32 v[204:205], v[118:119], v[200:201]
	v_pk_mul_f32 v[228:229], v[116:117], v[206:207]
	v_mov_b32_e32 v159, v209
	v_pk_add_f32 v[8:9], v[8:9], v[140:141]
	v_pk_mul_f32 v[140:141], v[114:115], v[184:185]
	v_pk_mul_f32 v[142:143], v[112:113], v[202:203]
	v_pk_fma_f32 v[204:205], v[118:119], v[156:157], v[204:205] op_sel:[0,0,1] op_sel_hi:[1,1,0]
	v_pk_fma_f32 v[208:209], v[116:117], v[158:159], v[228:229] op_sel:[0,0,1] op_sel_hi:[1,1,0]
	v_pk_fma_f32 v[140:141], v[114:115], v[152:153], v[140:141] op_sel:[0,0,1] op_sel_hi:[1,1,0]
	v_pk_fma_f32 v[142:143], v[112:113], v[154:155], v[142:143] op_sel:[0,0,1] op_sel_hi:[1,1,0]
	v_pk_add_f32 v[204:205], v[204:205], v[208:209]
	v_pk_add_f32 v[140:141], v[140:141], v[142:143]
	v_pk_add_f32 v[94:95], v[94:95], v[204:205]
	s_waitcnt lgkmcnt(2)
	v_mov_b32_e32 v204, v210
	v_mov_b32_e32 v205, v161
	v_mov_b32_e32 v161, v211
	v_mov_b32_e32 v210, v212
	v_mov_b32_e32 v211, v163
	v_pk_add_f32 v[8:9], v[8:9], v[140:141]
	v_pk_mul_f32 v[140:141], v[122:123], v[200:201]
	v_pk_mul_f32 v[142:143], v[120:121], v[206:207]
	v_pk_mul_f32 v[208:209], v[126:127], v[204:205]
	v_pk_mul_f32 v[228:229], v[124:125], v[210:211]
	v_mov_b32_e32 v163, v213
	v_pk_fma_f32 v[140:141], v[122:123], v[156:157], v[140:141] op_sel:[0,0,1] op_sel_hi:[1,1,0]
	v_pk_fma_f32 v[142:143], v[120:121], v[158:159], v[142:143] op_sel:[0,0,1] op_sel_hi:[1,1,0]
	v_pk_fma_f32 v[208:209], v[126:127], v[160:161], v[208:209] op_sel:[0,0,1] op_sel_hi:[1,1,0]
	v_pk_fma_f32 v[212:213], v[124:125], v[162:163], v[228:229] op_sel:[0,0,1] op_sel_hi:[1,1,0]
	v_pk_add_f32 v[140:141], v[140:141], v[142:143]
	v_pk_add_f32 v[208:209], v[208:209], v[212:213]
	v_pk_add_f32 v[8:9], v[8:9], v[140:141]
	v_pk_mul_f32 v[140:141], v[130:131], v[204:205]
	v_pk_mul_f32 v[142:143], v[128:129], v[210:211]
	v_pk_add_f32 v[94:95], v[94:95], v[208:209]
	s_waitcnt lgkmcnt(1)
	v_mov_b32_e32 v208, v214
	v_mov_b32_e32 v209, v165
	v_mov_b32_e32 v165, v215
	v_mov_b32_e32 v214, v216
	v_mov_b32_e32 v215, v167
	v_pk_fma_f32 v[140:141], v[130:131], v[160:161], v[140:141] op_sel:[0,0,1] op_sel_hi:[1,1,0]
	v_pk_fma_f32 v[142:143], v[128:129], v[162:163], v[142:143] op_sel:[0,0,1] op_sel_hi:[1,1,0]
	v_pk_mul_f32 v[212:213], v[134:135], v[208:209]
	v_pk_mul_f32 v[228:229], v[132:133], v[214:215]
	v_mov_b32_e32 v167, v217
	v_pk_add_f32 v[140:141], v[140:141], v[142:143]
	v_pk_fma_f32 v[212:213], v[134:135], v[164:165], v[212:213] op_sel:[0,0,1] op_sel_hi:[1,1,0]
	v_pk_fma_f32 v[216:217], v[132:133], v[166:167], v[228:229] op_sel:[0,0,1] op_sel_hi:[1,1,0]
	v_pk_add_f32 v[8:9], v[8:9], v[140:141]
	v_pk_mul_f32 v[140:141], v[138:139], v[208:209]
	v_pk_mul_f32 v[142:143], v[136:137], v[214:215]
	v_pk_add_f32 v[212:213], v[212:213], v[216:217]
	v_pk_fma_f32 v[140:141], v[138:139], v[164:165], v[140:141] op_sel:[0,0,1] op_sel_hi:[1,1,0]
	v_pk_fma_f32 v[142:143], v[136:137], v[166:167], v[142:143] op_sel:[0,0,1] op_sel_hi:[1,1,0]
	v_pk_add_f32 v[94:95], v[94:95], v[212:213]
	s_waitcnt lgkmcnt(0)
	v_mov_b32_e32 v212, v224
	v_mov_b32_e32 v213, v175
	v_mov_b32_e32 v175, v225
	v_mov_b32_e32 v224, v226
	v_mov_b32_e32 v225, v177
	v_pk_add_f32 v[140:141], v[140:141], v[142:143]
	v_pk_mul_f32 v[216:217], v[6:7], v[212:213]
	v_pk_mul_f32 v[228:229], v[4:5], v[224:225]
	v_mov_b32_e32 v177, v227
	v_pk_add_f32 v[8:9], v[8:9], v[140:141]
	v_pk_mul_f32 v[140:141], v[12:13], v[212:213]
	v_pk_mul_f32 v[142:143], v[10:11], v[224:225]
	v_pk_fma_f32 v[216:217], v[6:7], v[174:175], v[216:217] op_sel:[0,0,1] op_sel_hi:[1,1,0]
	v_pk_fma_f32 v[226:227], v[4:5], v[176:177], v[228:229] op_sel:[0,0,1] op_sel_hi:[1,1,0]
	v_pk_fma_f32 v[140:141], v[12:13], v[174:175], v[140:141] op_sel:[0,0,1] op_sel_hi:[1,1,0]
	v_pk_fma_f32 v[142:143], v[10:11], v[176:177], v[142:143] op_sel:[0,0,1] op_sel_hi:[1,1,0]
	v_pk_add_f32 v[216:217], v[216:217], v[226:227]
	v_pk_add_f32 v[140:141], v[140:141], v[142:143]
	v_pk_add_f32 v[94:95], v[94:95], v[216:217]
	v_pk_add_f32 v[8:9], v[8:9], v[140:141]
	ds_read_b128 v[140:143], v25 offset:49152
	ds_read_b128 v[144:147], v25 offset:50176
	ds_read_b128 v[148:151], v25 offset:51200
	ds_read_b128 v[152:155], v25 offset:52224
	ds_read_b128 v[156:159], v25 offset:53248
	ds_read_b128 v[160:163], v25 offset:54272
	ds_read_b128 v[164:167], v25 offset:55296
	ds_read_b128 v[174:177], v25 offset:56320
	ds_read_b128 v[178:181], v25 offset:57344
	ds_read_b128 v[182:185], v25 offset:58368
	ds_read_b128 v[198:201], v25 offset:59392
	ds_read_b128 v[202:205], v25 offset:60416
	ds_read_b128 v[206:209], v25 offset:61440
	ds_read_b128 v[210:213], v25 offset:62464
	ds_read_b128 v[214:217], v25 offset:63488
	ds_read_b128 v[224:227], v25 offset:64512
	s_waitcnt lgkmcnt(7)
	v_mov_b32_e32 v218, v178
	v_mov_b32_e32 v219, v141
	v_pk_mul_f32 v[228:229], v[82:83], v[218:219]
	v_mov_b32_e32 v141, v179
	v_mov_b32_e32 v178, v180
	v_mov_b32_e32 v179, v143
	v_pk_fma_f32 v[82:83], v[82:83], v[140:141], v[228:229] op_sel:[0,0,1] op_sel_hi:[1,1,0]
	v_pk_mul_f32 v[228:229], v[80:81], v[178:179]
	v_mov_b32_e32 v143, v181
	v_pk_fma_f32 v[80:81], v[80:81], v[142:143], v[228:229] op_sel:[0,0,1] op_sel_hi:[1,1,0]
	s_nop 0
	v_pk_add_f32 v[80:81], v[82:83], v[80:81]
	s_waitcnt lgkmcnt(6)
	v_mov_b32_e32 v82, v182
	v_mov_b32_e32 v83, v145
	v_pk_mul_f32 v[180:181], v[90:91], v[82:83]
	v_mov_b32_e32 v145, v183
	v_pk_fma_f32 v[90:91], v[90:91], v[144:145], v[180:181] op_sel:[0,0,1] op_sel_hi:[1,1,0]
	v_mov_b32_e32 v180, v184
	v_mov_b32_e32 v181, v147
	v_pk_mul_f32 v[182:183], v[88:89], v[180:181]
	v_mov_b32_e32 v147, v185
	v_pk_fma_f32 v[88:89], v[88:89], v[146:147], v[182:183] op_sel:[0,0,1] op_sel_hi:[1,1,0]
	v_pk_add_f32 v[80:81], v[80:81], 0 op_sel_hi:[1,0]
	v_pk_add_f32 v[88:89], v[90:91], v[88:89]
	s_nop 0
	v_pk_add_f32 v[80:81], v[80:81], v[88:89]
	s_waitcnt lgkmcnt(5)
	v_mov_b32_e32 v88, v198
	v_mov_b32_e32 v89, v149
	v_pk_mul_f32 v[90:91], v[102:103], v[88:89]
	v_mov_b32_e32 v149, v199
	v_pk_fma_f32 v[90:91], v[102:103], v[148:149], v[90:91] op_sel:[0,0,1] op_sel_hi:[1,1,0]
	v_mov_b32_e32 v102, v200
	v_mov_b32_e32 v103, v151
	v_pk_mul_f32 v[182:183], v[100:101], v[102:103]
	v_mov_b32_e32 v151, v201
	v_pk_fma_f32 v[100:101], v[100:101], v[150:151], v[182:183] op_sel:[0,0,1] op_sel_hi:[1,1,0]
	s_nop 0
	v_pk_add_f32 v[90:91], v[90:91], v[100:101]
	s_nop 0
	v_pk_add_f32 v[80:81], v[80:81], v[90:91]
	s_waitcnt lgkmcnt(4)
	v_mov_b32_e32 v90, v202
	v_mov_b32_e32 v91, v153
	v_pk_mul_f32 v[100:101], v[110:111], v[90:91]
	v_mov_b32_e32 v153, v203
	v_pk_fma_f32 v[100:101], v[110:111], v[152:153], v[100:101] op_sel:[0,0,1] op_sel_hi:[1,1,0]
	v_mov_b32_e32 v110, v204
	v_mov_b32_e32 v111, v155
	v_pk_mul_f32 v[182:183], v[108:109], v[110:111]
	v_mov_b32_e32 v155, v205
	v_pk_fma_f32 v[108:109], v[108:109], v[154:155], v[182:183] op_sel:[0,0,1] op_sel_hi:[1,1,0]
	s_nop 0
	v_pk_add_f32 v[100:101], v[100:101], v[108:109]
	s_nop 0
	v_pk_add_f32 v[80:81], v[80:81], v[100:101]
	s_waitcnt lgkmcnt(3)
	v_mov_b32_e32 v100, v206
	v_mov_b32_e32 v101, v157
	v_pk_mul_f32 v[108:109], v[118:119], v[100:101]
	v_mov_b32_e32 v157, v207
	v_pk_fma_f32 v[108:109], v[118:119], v[156:157], v[108:109] op_sel:[0,0,1] op_sel_hi:[1,1,0]
	v_mov_b32_e32 v118, v208
	v_mov_b32_e32 v119, v159
	v_pk_mul_f32 v[182:183], v[116:117], v[118:119]
	v_mov_b32_e32 v159, v209
	v_pk_fma_f32 v[116:117], v[116:117], v[158:159], v[182:183] op_sel:[0,0,1] op_sel_hi:[1,1,0]
	s_nop 0
	v_pk_add_f32 v[108:109], v[108:109], v[116:117]
	s_nop 0
	v_pk_add_f32 v[80:81], v[80:81], v[108:109]
	s_waitcnt lgkmcnt(2)
	v_mov_b32_e32 v108, v210
	v_mov_b32_e32 v109, v161
	v_pk_mul_f32 v[116:117], v[126:127], v[108:109]
	v_mov_b32_e32 v161, v211
	v_pk_fma_f32 v[116:117], v[126:127], v[160:161], v[116:117] op_sel:[0,0,1] op_sel_hi:[1,1,0]
	v_mov_b32_e32 v126, v212
	v_mov_b32_e32 v127, v163
	v_pk_mul_f32 v[182:183], v[124:125], v[126:127]
	v_mov_b32_e32 v163, v213
	v_pk_fma_f32 v[124:125], v[124:125], v[162:163], v[182:183] op_sel:[0,0,1] op_sel_hi:[1,1,0]
	s_nop 0
	v_pk_add_f32 v[116:117], v[116:117], v[124:125]
	s_nop 0
	v_pk_add_f32 v[80:81], v[80:81], v[116:117]
	s_waitcnt lgkmcnt(1)
	v_mov_b32_e32 v116, v214
	v_mov_b32_e32 v117, v165
	v_pk_mul_f32 v[124:125], v[134:135], v[116:117]
	v_mov_b32_e32 v165, v215
	v_pk_fma_f32 v[124:125], v[134:135], v[164:165], v[124:125] op_sel:[0,0,1] op_sel_hi:[1,1,0]
	v_mov_b32_e32 v134, v216
	v_mov_b32_e32 v135, v167
	v_pk_mul_f32 v[182:183], v[132:133], v[134:135]
	v_mov_b32_e32 v167, v217
	v_pk_fma_f32 v[132:133], v[132:133], v[166:167], v[182:183] op_sel:[0,0,1] op_sel_hi:[1,1,0]
	s_nop 0
	v_pk_add_f32 v[124:125], v[124:125], v[132:133]
	s_nop 0
	v_pk_add_f32 v[80:81], v[80:81], v[124:125]
	s_waitcnt lgkmcnt(0)
	v_mov_b32_e32 v124, v224
	v_mov_b32_e32 v125, v175
	v_pk_mul_f32 v[132:133], v[6:7], v[124:125]
	v_mov_b32_e32 v175, v225
	v_pk_fma_f32 v[6:7], v[6:7], v[174:175], v[132:133] op_sel:[0,0,1] op_sel_hi:[1,1,0]
	v_mov_b32_e32 v132, v226
	v_mov_b32_e32 v133, v177
	v_pk_mul_f32 v[182:183], v[4:5], v[132:133]
	v_mov_b32_e32 v177, v227
	v_pk_fma_f32 v[4:5], v[4:5], v[176:177], v[182:183] op_sel:[0,0,1] op_sel_hi:[1,1,0]
	s_nop 0
	v_pk_add_f32 v[4:5], v[6:7], v[4:5]
	s_nop 0
	v_pk_add_f32 v[6:7], v[80:81], v[4:5]
	v_pk_mul_f32 v[4:5], v[86:87], v[218:219]
	v_pk_mul_f32 v[80:81], v[84:85], v[178:179]
	v_pk_fma_f32 v[4:5], v[86:87], v[140:141], v[4:5] op_sel:[0,0,1] op_sel_hi:[1,1,0]
	v_pk_fma_f32 v[80:81], v[84:85], v[142:143], v[80:81] op_sel:[0,0,1] op_sel_hi:[1,1,0]
	s_nop 0
	v_pk_add_f32 v[4:5], v[4:5], v[80:81]
	v_pk_mul_f32 v[80:81], v[98:99], v[82:83]
	v_pk_mul_f32 v[82:83], v[96:97], v[180:181]
	v_pk_fma_f32 v[80:81], v[98:99], v[144:145], v[80:81] op_sel:[0,0,1] op_sel_hi:[1,1,0]
	v_pk_fma_f32 v[82:83], v[96:97], v[146:147], v[82:83] op_sel:[0,0,1] op_sel_hi:[1,1,0]
	v_pk_add_f32 v[4:5], v[4:5], 0 op_sel_hi:[1,0]
	v_pk_add_f32 v[80:81], v[80:81], v[82:83]
	v_pk_mul_f32 v[82:83], v[104:105], v[102:103]
	v_pk_add_f32 v[4:5], v[4:5], v[80:81]
	v_pk_mul_f32 v[80:81], v[106:107], v[88:89]
	v_pk_fma_f32 v[82:83], v[104:105], v[150:151], v[82:83] op_sel:[0,0,1] op_sel_hi:[1,1,0]
	v_pk_fma_f32 v[80:81], v[106:107], v[148:149], v[80:81] op_sel:[0,0,1] op_sel_hi:[1,1,0]
	s_nop 0
	v_pk_add_f32 v[80:81], v[80:81], v[82:83]
	v_pk_mul_f32 v[82:83], v[112:113], v[110:111]
	v_pk_add_f32 v[4:5], v[4:5], v[80:81]
	v_pk_mul_f32 v[80:81], v[114:115], v[90:91]
	v_pk_fma_f32 v[82:83], v[112:113], v[154:155], v[82:83] op_sel:[0,0,1] op_sel_hi:[1,1,0]
	v_pk_fma_f32 v[80:81], v[114:115], v[152:153], v[80:81] op_sel:[0,0,1] op_sel_hi:[1,1,0]
	s_nop 0
	v_pk_add_f32 v[80:81], v[80:81], v[82:83]
	v_pk_mul_f32 v[82:83], v[120:121], v[118:119]
	v_pk_add_f32 v[4:5], v[4:5], v[80:81]
	v_pk_mul_f32 v[80:81], v[122:123], v[100:101]
	v_pk_fma_f32 v[82:83], v[120:121], v[158:159], v[82:83] op_sel:[0,0,1] op_sel_hi:[1,1,0]
	v_pk_fma_f32 v[80:81], v[122:123], v[156:157], v[80:81] op_sel:[0,0,1] op_sel_hi:[1,1,0]
	s_nop 0
	v_pk_add_f32 v[80:81], v[80:81], v[82:83]
	v_pk_mul_f32 v[82:83], v[128:129], v[126:127]
	v_pk_add_f32 v[4:5], v[4:5], v[80:81]
	v_pk_mul_f32 v[80:81], v[130:131], v[108:109]
	v_pk_fma_f32 v[82:83], v[128:129], v[162:163], v[82:83] op_sel:[0,0,1] op_sel_hi:[1,1,0]
	v_pk_fma_f32 v[80:81], v[130:131], v[160:161], v[80:81] op_sel:[0,0,1] op_sel_hi:[1,1,0]
	s_nop 0
	v_pk_add_f32 v[80:81], v[80:81], v[82:83]
	v_pk_mul_f32 v[82:83], v[136:137], v[134:135]
	v_pk_add_f32 v[4:5], v[4:5], v[80:81]
	v_pk_mul_f32 v[80:81], v[138:139], v[116:117]
	v_pk_fma_f32 v[82:83], v[136:137], v[166:167], v[82:83] op_sel:[0,0,1] op_sel_hi:[1,1,0]
	v_pk_fma_f32 v[80:81], v[138:139], v[164:165], v[80:81] op_sel:[0,0,1] op_sel_hi:[1,1,0]
	s_nop 0
	v_pk_add_f32 v[80:81], v[80:81], v[82:83]
	s_nop 0
	v_pk_add_f32 v[4:5], v[4:5], v[80:81]
	v_pk_mul_f32 v[80:81], v[12:13], v[124:125]
	s_nop 0
	v_pk_fma_f32 v[12:13], v[12:13], v[174:175], v[80:81] op_sel:[0,0,1] op_sel_hi:[1,1,0]
	v_pk_mul_f32 v[80:81], v[10:11], v[132:133]
	s_nop 0
	v_pk_fma_f32 v[10:11], v[10:11], v[176:177], v[80:81] op_sel:[0,0,1] op_sel_hi:[1,1,0]
	s_nop 0
	v_pk_add_f32 v[10:11], v[12:13], v[10:11]
	s_nop 0
	v_pk_add_f32 v[4:5], v[4:5], v[10:11]
	v_cndmask_b32_e64 v10, v14, v15, s[46:47]
	v_cmp_eq_u32_e64 s[46:47], 2, v20
	s_nop 1
	v_cndmask_b32_e64 v10, v10, v92, s[46:47]
	v_cmp_eq_u32_e64 s[46:47], 3, v20
	s_nop 1
	v_cndmask_b32_e64 v10, v10, v93, s[46:47]
	v_cmp_eq_u32_e64 s[46:47], 4, v20
	s_nop 1
	v_cndmask_b32_e64 v10, v10, v94, s[46:47]
	v_cmp_eq_u32_e64 s[46:47], 5, v20
	s_nop 1
	v_cndmask_b32_e64 v10, v10, v95, s[46:47]
	v_cmp_eq_u32_e64 s[46:47], 6, v20
	s_nop 1
	v_cndmask_b32_e64 v10, v10, v6, s[46:47]
	v_cmp_eq_u32_e64 s[46:47], 7, v20
	s_nop 1
	v_cndmask_b32_e64 v10, v10, v7, s[46:47]
	v_cmp_eq_u32_e64 s[46:47], 8, v20
	s_nop 1
	v_cndmask_b32_e64 v10, v10, v0, s[46:47]
	v_cmp_eq_u32_e64 s[46:47], 9, v20
	s_nop 1
	v_cndmask_b32_e64 v10, v10, v1, s[46:47]
	v_cmp_eq_u32_e64 s[46:47], 10, v20
	s_nop 1
	v_cndmask_b32_e64 v10, v10, v2, s[46:47]
	v_cmp_eq_u32_e64 s[46:47], 11, v20
	s_nop 1
	v_cndmask_b32_e64 v10, v10, v3, s[46:47]
	v_cmp_eq_u32_e64 s[46:47], 12, v20
	s_nop 1
	v_cndmask_b32_e64 v10, v10, v8, s[46:47]
	v_cmp_eq_u32_e64 s[46:47], 13, v20
	s_nop 1
	v_cndmask_b32_e64 v10, v10, v9, s[46:47]
	v_cmp_eq_u32_e64 s[46:47], 14, v20
	s_nop 1
	v_cndmask_b32_e64 v10, v10, v4, s[46:47]
	v_cmp_eq_u32_e64 s[46:47], 15, v20
	s_nop 1
	v_cndmask_b32_e64 v10, v10, v5, s[46:47]
	v_cmp_eq_u32_e64 s[46:47], 1, v22
	ds_bpermute_b32 v10, v39, v10
	s_nop 0
	v_cndmask_b32_e64 v11, v14, v15, s[46:47]
	v_cmp_eq_u32_e64 s[46:47], 2, v22
	s_nop 1
	v_cndmask_b32_e64 v11, v11, v92, s[46:47]
	v_cmp_eq_u32_e64 s[46:47], 3, v22
	s_nop 1
	v_cndmask_b32_e64 v11, v11, v93, s[46:47]
	v_cmp_eq_u32_e64 s[46:47], 4, v22
	s_nop 1
	v_cndmask_b32_e64 v11, v11, v94, s[46:47]
	v_cmp_eq_u32_e64 s[46:47], 5, v22
	s_nop 1
	v_cndmask_b32_e64 v11, v11, v95, s[46:47]
	v_cmp_eq_u32_e64 s[46:47], 6, v22
	s_nop 1
	v_cndmask_b32_e64 v11, v11, v6, s[46:47]
	v_cmp_eq_u32_e64 s[46:47], 7, v22
	s_nop 1
	v_cndmask_b32_e64 v11, v11, v7, s[46:47]
	v_cmp_eq_u32_e64 s[46:47], 8, v22
	s_nop 1
	v_cndmask_b32_e64 v11, v11, v0, s[46:47]
	v_cmp_eq_u32_e64 s[46:47], 9, v22
	s_nop 1
	v_cndmask_b32_e64 v11, v11, v1, s[46:47]
	v_cmp_eq_u32_e64 s[46:47], 10, v22
	s_nop 1
	v_cndmask_b32_e64 v11, v11, v2, s[46:47]
	v_cmp_eq_u32_e64 s[46:47], 11, v22
	s_nop 1
	v_cndmask_b32_e64 v11, v11, v3, s[46:47]
	v_cmp_eq_u32_e64 s[46:47], 12, v22
	s_nop 1
	v_cndmask_b32_e64 v11, v11, v8, s[46:47]
	v_cmp_eq_u32_e64 s[46:47], 13, v22
	s_nop 1
	v_cndmask_b32_e64 v11, v11, v9, s[46:47]
	v_cmp_eq_u32_e64 s[46:47], 14, v22
	s_nop 1
	v_cndmask_b32_e64 v11, v11, v4, s[46:47]
	v_cmp_eq_u32_e64 s[46:47], 15, v22
	s_nop 1
	v_cndmask_b32_e64 v11, v11, v5, s[46:47]
	s_waitcnt lgkmcnt(0)
	v_add_f32_e32 v12, v11, v10
	v_cmp_eq_u32_e64 s[46:47], 1, v24
	s_nop 1
	v_cndmask_b32_e64 v10, v12, v15, s[46:47]
	v_cmp_eq_u32_e64 s[46:47], 2, v24
	s_nop 1
	v_cndmask_b32_e64 v10, v10, v92, s[46:47]
	v_cmp_eq_u32_e64 s[46:47], 3, v24
	s_nop 1
	v_cndmask_b32_e64 v10, v10, v93, s[46:47]
	v_cmp_eq_u32_e64 s[46:47], 4, v24
	s_nop 1
	v_cndmask_b32_e64 v10, v10, v94, s[46:47]
	v_cmp_eq_u32_e64 s[46:47], 5, v24
	s_nop 1
	v_cndmask_b32_e64 v10, v10, v95, s[46:47]
	v_cmp_eq_u32_e64 s[46:47], 6, v24
	s_nop 1
	v_cndmask_b32_e64 v10, v10, v6, s[46:47]
	v_cmp_eq_u32_e64 s[46:47], 7, v24
	s_nop 1
	v_cndmask_b32_e64 v10, v10, v7, s[46:47]
	v_cmp_eq_u32_e64 s[46:47], 8, v24
	s_nop 1
	v_cndmask_b32_e64 v10, v10, v0, s[46:47]
	v_cmp_eq_u32_e64 s[46:47], 9, v24
	s_nop 1
	v_cndmask_b32_e64 v10, v10, v1, s[46:47]
	v_cmp_eq_u32_e64 s[46:47], 10, v24
	s_nop 1
	v_cndmask_b32_e64 v10, v10, v2, s[46:47]
	v_cmp_eq_u32_e64 s[46:47], 11, v24
	s_nop 1
	v_cndmask_b32_e64 v10, v10, v3, s[46:47]
	v_cmp_eq_u32_e64 s[46:47], 12, v24
	s_nop 1
	v_cndmask_b32_e64 v10, v10, v8, s[46:47]
	v_cmp_eq_u32_e64 s[46:47], 13, v24
	s_nop 1
	v_cndmask_b32_e64 v10, v10, v9, s[46:47]
	v_cmp_eq_u32_e64 s[46:47], 14, v24
	s_nop 1
	v_cndmask_b32_e64 v10, v10, v4, s[46:47]
	v_cmp_eq_u32_e64 s[46:47], 15, v24
	s_nop 1
	v_cndmask_b32_e64 v10, v10, v5, s[46:47]
	v_cmp_eq_u32_e64 s[46:47], 1, v26
	ds_bpermute_b32 v10, v39, v10
	s_nop 0
	v_cndmask_b32_e64 v11, v12, v15, s[46:47]
	v_cmp_eq_u32_e64 s[46:47], 2, v26
	s_nop 1
	v_cndmask_b32_e64 v11, v11, v92, s[46:47]
	v_cmp_eq_u32_e64 s[46:47], 3, v26
	s_nop 1
	v_cndmask_b32_e64 v11, v11, v93, s[46:47]
	v_cmp_eq_u32_e64 s[46:47], 4, v26
	s_nop 1
	v_cndmask_b32_e64 v11, v11, v94, s[46:47]
	v_cmp_eq_u32_e64 s[46:47], 5, v26
	s_nop 1
	v_cndmask_b32_e64 v11, v11, v95, s[46:47]
	v_cmp_eq_u32_e64 s[46:47], 6, v26
	s_nop 1
	v_cndmask_b32_e64 v11, v11, v6, s[46:47]
	v_cmp_eq_u32_e64 s[46:47], 7, v26
	s_nop 1
	v_cndmask_b32_e64 v11, v11, v7, s[46:47]
	v_cmp_eq_u32_e64 s[46:47], 8, v26
	s_nop 1
	v_cndmask_b32_e64 v11, v11, v0, s[46:47]
	v_cmp_eq_u32_e64 s[46:47], 9, v26
	s_nop 1
	v_cndmask_b32_e64 v11, v11, v1, s[46:47]
	v_cmp_eq_u32_e64 s[46:47], 10, v26
	s_nop 1
	v_cndmask_b32_e64 v11, v11, v2, s[46:47]
	v_cmp_eq_u32_e64 s[46:47], 11, v26
	s_nop 1
	v_cndmask_b32_e64 v11, v11, v3, s[46:47]
	v_cmp_eq_u32_e64 s[46:47], 12, v26
	s_nop 1
	v_cndmask_b32_e64 v11, v11, v8, s[46:47]
	v_cmp_eq_u32_e64 s[46:47], 13, v26
	s_nop 1
	v_cndmask_b32_e64 v11, v11, v9, s[46:47]
	v_cmp_eq_u32_e64 s[46:47], 14, v26
	s_nop 1
	v_cndmask_b32_e64 v11, v11, v4, s[46:47]
	v_cmp_eq_u32_e64 s[46:47], 15, v26
	s_nop 1
	v_cndmask_b32_e64 v11, v11, v5, s[46:47]
	s_waitcnt lgkmcnt(0)
	v_add_f32_e32 v13, v11, v10
	v_cmp_eq_u32_e64 s[46:47], 1, v28
	s_nop 1
	v_cndmask_b32_e64 v10, v12, v13, s[46:47]
	v_cmp_eq_u32_e64 s[46:47], 2, v28
	s_nop 1
	v_cndmask_b32_e64 v10, v10, v92, s[46:47]
	v_cmp_eq_u32_e64 s[46:47], 3, v28
	s_nop 1
	v_cndmask_b32_e64 v10, v10, v93, s[46:47]
	v_cmp_eq_u32_e64 s[46:47], 4, v28
	s_nop 1
	v_cndmask_b32_e64 v10, v10, v94, s[46:47]
	v_cmp_eq_u32_e64 s[46:47], 5, v28
	s_nop 1
	v_cndmask_b32_e64 v10, v10, v95, s[46:47]
	v_cmp_eq_u32_e64 s[46:47], 6, v28
	s_nop 1
	v_cndmask_b32_e64 v10, v10, v6, s[46:47]
	v_cmp_eq_u32_e64 s[46:47], 7, v28
	s_nop 1
	v_cndmask_b32_e64 v10, v10, v7, s[46:47]
	v_cmp_eq_u32_e64 s[46:47], 8, v28
	s_nop 1
	v_cndmask_b32_e64 v10, v10, v0, s[46:47]
	v_cmp_eq_u32_e64 s[46:47], 9, v28
	s_nop 1
	v_cndmask_b32_e64 v10, v10, v1, s[46:47]
	v_cmp_eq_u32_e64 s[46:47], 10, v28
	s_nop 1
	v_cndmask_b32_e64 v10, v10, v2, s[46:47]
	v_cmp_eq_u32_e64 s[46:47], 11, v28
	s_nop 1
	v_cndmask_b32_e64 v10, v10, v3, s[46:47]
	v_cmp_eq_u32_e64 s[46:47], 12, v28
	s_nop 1
	v_cndmask_b32_e64 v10, v10, v8, s[46:47]
	v_cmp_eq_u32_e64 s[46:47], 13, v28
	s_nop 1
	v_cndmask_b32_e64 v10, v10, v9, s[46:47]
	v_cmp_eq_u32_e64 s[46:47], 14, v28
	s_nop 1
	v_cndmask_b32_e64 v10, v10, v4, s[46:47]
	v_cmp_eq_u32_e64 s[46:47], 15, v28
	s_nop 1
	v_cndmask_b32_e64 v10, v10, v5, s[46:47]
	v_cmp_eq_u32_e64 s[46:47], 1, v30
	ds_bpermute_b32 v10, v39, v10
	s_nop 0
	v_cndmask_b32_e64 v11, v12, v13, s[46:47]
	v_cmp_eq_u32_e64 s[46:47], 2, v30
	s_nop 1
	v_cndmask_b32_e64 v11, v11, v92, s[46:47]
	v_cmp_eq_u32_e64 s[46:47], 3, v30
	s_nop 1
	v_cndmask_b32_e64 v11, v11, v93, s[46:47]
	v_cmp_eq_u32_e64 s[46:47], 4, v30
	s_nop 1
	v_cndmask_b32_e64 v11, v11, v94, s[46:47]
	v_cmp_eq_u32_e64 s[46:47], 5, v30
	s_nop 1
	v_cndmask_b32_e64 v11, v11, v95, s[46:47]
	v_cmp_eq_u32_e64 s[46:47], 6, v30
	s_nop 1
	v_cndmask_b32_e64 v11, v11, v6, s[46:47]
	v_cmp_eq_u32_e64 s[46:47], 7, v30
	s_nop 1
	v_cndmask_b32_e64 v11, v11, v7, s[46:47]
	v_cmp_eq_u32_e64 s[46:47], 8, v30
	s_nop 1
	v_cndmask_b32_e64 v11, v11, v0, s[46:47]
	v_cmp_eq_u32_e64 s[46:47], 9, v30
	s_nop 1
	v_cndmask_b32_e64 v11, v11, v1, s[46:47]
	v_cmp_eq_u32_e64 s[46:47], 10, v30
	s_nop 1
	v_cndmask_b32_e64 v11, v11, v2, s[46:47]
	v_cmp_eq_u32_e64 s[46:47], 11, v30
	s_nop 1
	v_cndmask_b32_e64 v11, v11, v3, s[46:47]
	v_cmp_eq_u32_e64 s[46:47], 12, v30
	s_nop 1
	v_cndmask_b32_e64 v11, v11, v8, s[46:47]
	v_cmp_eq_u32_e64 s[46:47], 13, v30
	s_nop 1
	v_cndmask_b32_e64 v11, v11, v9, s[46:47]
	v_cmp_eq_u32_e64 s[46:47], 14, v30
	s_nop 1
	v_cndmask_b32_e64 v11, v11, v4, s[46:47]
	v_cmp_eq_u32_e64 s[46:47], 15, v30
	s_nop 1
	v_cndmask_b32_e64 v11, v11, v5, s[46:47]
	v_cmp_eq_u32_e64 s[46:47], 1, v32
	s_waitcnt lgkmcnt(0)
	v_add_f32_e32 v14, v11, v10
	v_cndmask_b32_e64 v10, v12, v13, s[46:47]
	v_cmp_eq_u32_e64 s[46:47], 2, v32
	s_nop 1
	v_cndmask_b32_e64 v10, v10, v14, s[46:47]
	v_cmp_eq_u32_e64 s[46:47], 3, v32
	s_nop 1
	v_cndmask_b32_e64 v10, v10, v93, s[46:47]
	v_cmp_eq_u32_e64 s[46:47], 4, v32
	s_nop 1
	v_cndmask_b32_e64 v10, v10, v94, s[46:47]
	v_cmp_eq_u32_e64 s[46:47], 5, v32
	s_nop 1
	v_cndmask_b32_e64 v10, v10, v95, s[46:47]
	v_cmp_eq_u32_e64 s[46:47], 6, v32
	s_nop 1
	v_cndmask_b32_e64 v10, v10, v6, s[46:47]
	v_cmp_eq_u32_e64 s[46:47], 7, v32
	s_nop 1
	v_cndmask_b32_e64 v10, v10, v7, s[46:47]
	v_cmp_eq_u32_e64 s[46:47], 8, v32
	s_nop 1
	v_cndmask_b32_e64 v10, v10, v0, s[46:47]
	v_cmp_eq_u32_e64 s[46:47], 9, v32
	s_nop 1
	v_cndmask_b32_e64 v10, v10, v1, s[46:47]
	v_cmp_eq_u32_e64 s[46:47], 10, v32
	s_nop 1
	v_cndmask_b32_e64 v10, v10, v2, s[46:47]
	v_cmp_eq_u32_e64 s[46:47], 11, v32
	s_nop 1
	v_cndmask_b32_e64 v10, v10, v3, s[46:47]
	v_cmp_eq_u32_e64 s[46:47], 12, v32
	s_nop 1
	v_cndmask_b32_e64 v10, v10, v8, s[46:47]
	v_cmp_eq_u32_e64 s[46:47], 13, v32
	s_nop 1
	v_cndmask_b32_e64 v10, v10, v9, s[46:47]
	v_cmp_eq_u32_e64 s[46:47], 14, v32
	s_nop 1
	v_cndmask_b32_e64 v10, v10, v4, s[46:47]
	v_cmp_eq_u32_e64 s[46:47], 15, v32
	s_nop 1
	v_cndmask_b32_e64 v10, v10, v5, s[46:47]
	v_cmp_eq_u32_e64 s[46:47], 1, v34
	ds_bpermute_b32 v10, v39, v10
	s_nop 0
	v_cndmask_b32_e64 v11, v12, v13, s[46:47]
	v_cmp_eq_u32_e64 s[46:47], 2, v34
	s_nop 1
	v_cndmask_b32_e64 v11, v11, v14, s[46:47]
	v_cmp_eq_u32_e64 s[46:47], 3, v34
	s_nop 1
	v_cndmask_b32_e64 v11, v11, v93, s[46:47]
	v_cmp_eq_u32_e64 s[46:47], 4, v34
	s_nop 1
	v_cndmask_b32_e64 v11, v11, v94, s[46:47]
	v_cmp_eq_u32_e64 s[46:47], 5, v34
	s_nop 1
	v_cndmask_b32_e64 v11, v11, v95, s[46:47]
	v_cmp_eq_u32_e64 s[46:47], 6, v34
	s_nop 1
	v_cndmask_b32_e64 v11, v11, v6, s[46:47]
	v_cmp_eq_u32_e64 s[46:47], 7, v34
	s_nop 1
	v_cndmask_b32_e64 v11, v11, v7, s[46:47]
	v_cmp_eq_u32_e64 s[46:47], 8, v34
	s_nop 1
	v_cndmask_b32_e64 v11, v11, v0, s[46:47]
	v_cmp_eq_u32_e64 s[46:47], 9, v34
	s_nop 1
	v_cndmask_b32_e64 v11, v11, v1, s[46:47]
	v_cmp_eq_u32_e64 s[46:47], 10, v34
	s_nop 1
	v_cndmask_b32_e64 v11, v11, v2, s[46:47]
	v_cmp_eq_u32_e64 s[46:47], 11, v34
	s_nop 1
	v_cndmask_b32_e64 v11, v11, v3, s[46:47]
	v_cmp_eq_u32_e64 s[46:47], 12, v34
	s_nop 1
	v_cndmask_b32_e64 v11, v11, v8, s[46:47]
	v_cmp_eq_u32_e64 s[46:47], 13, v34
	s_nop 1
	v_cndmask_b32_e64 v11, v11, v9, s[46:47]
	v_cmp_eq_u32_e64 s[46:47], 14, v34
	s_nop 1
	v_cndmask_b32_e64 v11, v11, v4, s[46:47]
	v_cmp_eq_u32_e64 s[46:47], 15, v34
	s_nop 1
	v_cndmask_b32_e64 v11, v11, v5, s[46:47]
	v_cmp_eq_u32_e64 s[46:47], 1, v36
	s_waitcnt lgkmcnt(0)
	v_add_f32_e32 v15, v11, v10
	v_cndmask_b32_e64 v10, v12, v13, s[46:47]
	v_cmp_eq_u32_e64 s[46:47], 2, v36
	s_nop 1
	v_cndmask_b32_e64 v10, v10, v14, s[46:47]
	v_cmp_eq_u32_e64 s[46:47], 3, v36
	s_nop 1
	v_cndmask_b32_e64 v10, v10, v15, s[46:47]
	v_cmp_eq_u32_e64 s[46:47], 4, v36
	s_nop 1
	v_cndmask_b32_e64 v10, v10, v94, s[46:47]
	v_cmp_eq_u32_e64 s[46:47], 5, v36
	s_nop 1
	v_cndmask_b32_e64 v10, v10, v95, s[46:47]
	v_cmp_eq_u32_e64 s[46:47], 6, v36
	s_nop 1
	v_cndmask_b32_e64 v10, v10, v6, s[46:47]
	v_cmp_eq_u32_e64 s[46:47], 7, v36
	s_nop 1
	v_cndmask_b32_e64 v10, v10, v7, s[46:47]
	v_cmp_eq_u32_e64 s[46:47], 8, v36
	s_nop 1
	v_cndmask_b32_e64 v10, v10, v0, s[46:47]
	v_cmp_eq_u32_e64 s[46:47], 9, v36
	s_nop 1
	v_cndmask_b32_e64 v10, v10, v1, s[46:47]
	v_cmp_eq_u32_e64 s[46:47], 10, v36
	s_nop 1
	v_cndmask_b32_e64 v10, v10, v2, s[46:47]
	v_cmp_eq_u32_e64 s[46:47], 11, v36
	s_nop 1
	v_cndmask_b32_e64 v10, v10, v3, s[46:47]
	v_cmp_eq_u32_e64 s[46:47], 12, v36
	s_nop 1
	v_cndmask_b32_e64 v10, v10, v8, s[46:47]
	v_cmp_eq_u32_e64 s[46:47], 13, v36
	s_nop 1
	v_cndmask_b32_e64 v10, v10, v9, s[46:47]
	v_cmp_eq_u32_e64 s[46:47], 14, v36
	s_nop 1
	v_cndmask_b32_e64 v10, v10, v4, s[46:47]
	v_cmp_eq_u32_e64 s[46:47], 15, v36
	s_nop 1
	v_cndmask_b32_e64 v10, v10, v5, s[46:47]
	v_cmp_eq_u32_e64 s[46:47], 1, v38
	ds_bpermute_b32 v10, v39, v10
	s_nop 0
	v_cndmask_b32_e64 v11, v12, v13, s[46:47]
	v_cmp_eq_u32_e64 s[46:47], 2, v38
	s_nop 1
	v_cndmask_b32_e64 v11, v11, v14, s[46:47]
	v_cmp_eq_u32_e64 s[46:47], 3, v38
	s_nop 1
	v_cndmask_b32_e64 v11, v11, v15, s[46:47]
	v_cmp_eq_u32_e64 s[46:47], 4, v38
	s_nop 1
	v_cndmask_b32_e64 v11, v11, v94, s[46:47]
	v_cmp_eq_u32_e64 s[46:47], 5, v38
	s_nop 1
	v_cndmask_b32_e64 v11, v11, v95, s[46:47]
	v_cmp_eq_u32_e64 s[46:47], 6, v38
	s_nop 1
	v_cndmask_b32_e64 v11, v11, v6, s[46:47]
	v_cmp_eq_u32_e64 s[46:47], 7, v38
	s_nop 1
	v_cndmask_b32_e64 v11, v11, v7, s[46:47]
	v_cmp_eq_u32_e64 s[46:47], 8, v38
	s_nop 1
	v_cndmask_b32_e64 v11, v11, v0, s[46:47]
	v_cmp_eq_u32_e64 s[46:47], 9, v38
	s_nop 1
	v_cndmask_b32_e64 v11, v11, v1, s[46:47]
	v_cmp_eq_u32_e64 s[46:47], 10, v38
	s_nop 1
	v_cndmask_b32_e64 v11, v11, v2, s[46:47]
	v_cmp_eq_u32_e64 s[46:47], 11, v38
	s_nop 1
	v_cndmask_b32_e64 v11, v11, v3, s[46:47]
	v_cmp_eq_u32_e64 s[46:47], 12, v38
	s_nop 1
	v_cndmask_b32_e64 v11, v11, v8, s[46:47]
	v_cmp_eq_u32_e64 s[46:47], 13, v38
	s_nop 1
	v_cndmask_b32_e64 v11, v11, v9, s[46:47]
	v_cmp_eq_u32_e64 s[46:47], 14, v38
	s_nop 1
	v_cndmask_b32_e64 v11, v11, v4, s[46:47]
	v_cmp_eq_u32_e64 s[46:47], 15, v38
	s_nop 1
	v_cndmask_b32_e64 v11, v11, v5, s[46:47]
	v_cmp_eq_u32_e64 s[46:47], 1, v40
	s_waitcnt lgkmcnt(0)
	v_add_f32_e32 v10, v11, v10
	v_cndmask_b32_e64 v11, v12, v13, s[46:47]
	v_cmp_eq_u32_e64 s[46:47], 2, v40
	s_nop 1
	v_cndmask_b32_e64 v11, v11, v14, s[46:47]
	v_cmp_eq_u32_e64 s[46:47], 3, v40
	s_nop 1
	v_cndmask_b32_e64 v11, v11, v15, s[46:47]
	v_cmp_eq_u32_e64 s[46:47], 4, v40
	s_nop 1
	v_cndmask_b32_e64 v11, v11, v10, s[46:47]
	v_cmp_eq_u32_e64 s[46:47], 5, v40
	s_nop 1
	v_cndmask_b32_e64 v11, v11, v95, s[46:47]
	v_cmp_eq_u32_e64 s[46:47], 6, v40
	s_nop 1
	v_cndmask_b32_e64 v11, v11, v6, s[46:47]
	v_cmp_eq_u32_e64 s[46:47], 7, v40
	s_nop 1
	v_cndmask_b32_e64 v11, v11, v7, s[46:47]
	v_cmp_eq_u32_e64 s[46:47], 8, v40
	s_nop 1
	v_cndmask_b32_e64 v11, v11, v0, s[46:47]
	v_cmp_eq_u32_e64 s[46:47], 9, v40
	s_nop 1
	v_cndmask_b32_e64 v11, v11, v1, s[46:47]
	v_cmp_eq_u32_e64 s[46:47], 10, v40
	s_nop 1
	v_cndmask_b32_e64 v11, v11, v2, s[46:47]
	v_cmp_eq_u32_e64 s[46:47], 11, v40
	s_nop 1
	v_cndmask_b32_e64 v11, v11, v3, s[46:47]
	v_cmp_eq_u32_e64 s[46:47], 12, v40
	s_nop 1
	v_cndmask_b32_e64 v11, v11, v8, s[46:47]
	v_cmp_eq_u32_e64 s[46:47], 13, v40
	s_nop 1
	v_cndmask_b32_e64 v11, v11, v9, s[46:47]
	v_cmp_eq_u32_e64 s[46:47], 14, v40
	s_nop 1
	v_cndmask_b32_e64 v11, v11, v4, s[46:47]
	v_cmp_eq_u32_e64 s[46:47], 15, v40
	s_nop 1
	v_cndmask_b32_e64 v11, v11, v5, s[46:47]
	v_cmp_eq_u32_e64 s[46:47], 1, v42
	ds_bpermute_b32 v11, v39, v11
	s_nop 0
	v_cndmask_b32_e64 v55, v12, v13, s[46:47]
	v_cmp_eq_u32_e64 s[46:47], 2, v42
	s_nop 1
	v_cndmask_b32_e64 v55, v55, v14, s[46:47]
	v_cmp_eq_u32_e64 s[46:47], 3, v42
	s_nop 1
	v_cndmask_b32_e64 v55, v55, v15, s[46:47]
	v_cmp_eq_u32_e64 s[46:47], 4, v42
	s_nop 1
	v_cndmask_b32_e64 v55, v55, v10, s[46:47]
	v_cmp_eq_u32_e64 s[46:47], 5, v42
	s_nop 1
	v_cndmask_b32_e64 v55, v55, v95, s[46:47]
	v_cmp_eq_u32_e64 s[46:47], 6, v42
	s_nop 1
	v_cndmask_b32_e64 v55, v55, v6, s[46:47]
	v_cmp_eq_u32_e64 s[46:47], 7, v42
	s_nop 1
	v_cndmask_b32_e64 v55, v55, v7, s[46:47]
	v_cmp_eq_u32_e64 s[46:47], 8, v42
	s_nop 1
	v_cndmask_b32_e64 v55, v55, v0, s[46:47]
	v_cmp_eq_u32_e64 s[46:47], 9, v42
	s_nop 1
	v_cndmask_b32_e64 v55, v55, v1, s[46:47]
	v_cmp_eq_u32_e64 s[46:47], 10, v42
	s_nop 1
	v_cndmask_b32_e64 v55, v55, v2, s[46:47]
	v_cmp_eq_u32_e64 s[46:47], 11, v42
	s_nop 1
	v_cndmask_b32_e64 v55, v55, v3, s[46:47]
	v_cmp_eq_u32_e64 s[46:47], 12, v42
	s_nop 1
	v_cndmask_b32_e64 v55, v55, v8, s[46:47]
	v_cmp_eq_u32_e64 s[46:47], 13, v42
	s_nop 1
	v_cndmask_b32_e64 v55, v55, v9, s[46:47]
	v_cmp_eq_u32_e64 s[46:47], 14, v42
	s_nop 1
	v_cndmask_b32_e64 v55, v55, v4, s[46:47]
	v_cmp_eq_u32_e64 s[46:47], 15, v42
	s_nop 1
	v_cndmask_b32_e64 v55, v55, v5, s[46:47]
	v_cmp_eq_u32_e64 s[46:47], 1, v44
	s_waitcnt lgkmcnt(0)
	v_add_f32_e32 v11, v55, v11
	v_cndmask_b32_e64 v55, v12, v13, s[46:47]
	v_cmp_eq_u32_e64 s[46:47], 2, v44
	s_nop 1
	v_cndmask_b32_e64 v55, v55, v14, s[46:47]
	v_cmp_eq_u32_e64 s[46:47], 3, v44
	s_nop 1
	v_cndmask_b32_e64 v55, v55, v15, s[46:47]
	v_cmp_eq_u32_e64 s[46:47], 4, v44
	s_nop 1
	v_cndmask_b32_e64 v55, v55, v10, s[46:47]
	v_cmp_eq_u32_e64 s[46:47], 5, v44
	s_nop 1
	v_cndmask_b32_e64 v55, v55, v11, s[46:47]
	v_cmp_eq_u32_e64 s[46:47], 6, v44
	s_nop 1
	v_cndmask_b32_e64 v55, v55, v6, s[46:47]
	v_cmp_eq_u32_e64 s[46:47], 7, v44
	s_nop 1
	v_cndmask_b32_e64 v55, v55, v7, s[46:47]
	v_cmp_eq_u32_e64 s[46:47], 8, v44
	s_nop 1
	v_cndmask_b32_e64 v55, v55, v0, s[46:47]
	v_cmp_eq_u32_e64 s[46:47], 9, v44
	s_nop 1
	v_cndmask_b32_e64 v55, v55, v1, s[46:47]
	v_cmp_eq_u32_e64 s[46:47], 10, v44
	s_nop 1
	v_cndmask_b32_e64 v55, v55, v2, s[46:47]
	v_cmp_eq_u32_e64 s[46:47], 11, v44
	s_nop 1
	v_cndmask_b32_e64 v55, v55, v3, s[46:47]
	v_cmp_eq_u32_e64 s[46:47], 12, v44
	s_nop 1
	v_cndmask_b32_e64 v55, v55, v8, s[46:47]
	v_cmp_eq_u32_e64 s[46:47], 13, v44
	s_nop 1
	v_cndmask_b32_e64 v55, v55, v9, s[46:47]
	v_cmp_eq_u32_e64 s[46:47], 14, v44
	s_nop 1
	v_cndmask_b32_e64 v55, v55, v4, s[46:47]
	v_cmp_eq_u32_e64 s[46:47], 15, v44
	s_nop 1
	v_cndmask_b32_e64 v55, v55, v5, s[46:47]
	v_cmp_eq_u32_e64 s[46:47], 1, v46
	ds_bpermute_b32 v55, v39, v55
	s_nop 0
	v_cndmask_b32_e64 v57, v12, v13, s[46:47]
	v_cmp_eq_u32_e64 s[46:47], 2, v46
	s_nop 1
	v_cndmask_b32_e64 v57, v57, v14, s[46:47]
	v_cmp_eq_u32_e64 s[46:47], 3, v46
	s_nop 1
	v_cndmask_b32_e64 v57, v57, v15, s[46:47]
	v_cmp_eq_u32_e64 s[46:47], 4, v46
	s_nop 1
	v_cndmask_b32_e64 v57, v57, v10, s[46:47]
	v_cmp_eq_u32_e64 s[46:47], 5, v46
	s_nop 1
	v_cndmask_b32_e64 v57, v57, v11, s[46:47]
	v_cmp_eq_u32_e64 s[46:47], 6, v46
	s_nop 1
	v_cndmask_b32_e64 v6, v57, v6, s[46:47]
	v_cmp_eq_u32_e64 s[46:47], 7, v46
	s_nop 1
	v_cndmask_b32_e64 v6, v6, v7, s[46:47]
	v_cmp_eq_u32_e64 s[46:47], 8, v46
	s_nop 1
	v_cndmask_b32_e64 v6, v6, v0, s[46:47]
	v_cmp_eq_u32_e64 s[46:47], 9, v46
	s_nop 1
	v_cndmask_b32_e64 v6, v6, v1, s[46:47]
	v_cmp_eq_u32_e64 s[46:47], 10, v46
	s_nop 1
	v_cndmask_b32_e64 v6, v6, v2, s[46:47]
	v_cmp_eq_u32_e64 s[46:47], 11, v46
	s_nop 1
	v_cndmask_b32_e64 v6, v6, v3, s[46:47]
	v_cmp_eq_u32_e64 s[46:47], 12, v46
	s_nop 1
	v_cndmask_b32_e64 v6, v6, v8, s[46:47]
	v_cmp_eq_u32_e64 s[46:47], 13, v46
	s_nop 1
	v_cndmask_b32_e64 v6, v6, v9, s[46:47]
	v_cmp_eq_u32_e64 s[46:47], 14, v46
	s_nop 1
	v_cndmask_b32_e64 v6, v6, v4, s[46:47]
	v_cmp_eq_u32_e64 s[46:47], 15, v46
	s_nop 1
	v_cndmask_b32_e64 v6, v6, v5, s[46:47]
	v_cmp_eq_u32_e64 s[46:47], 1, v48
	s_waitcnt lgkmcnt(0)
	v_add_f32_e32 v6, v6, v55
	v_cndmask_b32_e64 v55, v12, v13, s[46:47]
	v_cmp_eq_u32_e64 s[46:47], 2, v48
	s_nop 1
	v_cndmask_b32_e64 v55, v55, v14, s[46:47]
	v_cmp_eq_u32_e64 s[46:47], 3, v48
	s_nop 1
	v_cndmask_b32_e64 v55, v55, v15, s[46:47]
	v_cmp_eq_u32_e64 s[46:47], 4, v48
	s_nop 1
	v_cndmask_b32_e64 v55, v55, v10, s[46:47]
	v_cmp_eq_u32_e64 s[46:47], 5, v48
	s_nop 1
	v_cndmask_b32_e64 v55, v55, v11, s[46:47]
	v_cmp_eq_u32_e64 s[46:47], 6, v48
	s_nop 1
	v_cndmask_b32_e64 v55, v55, v6, s[46:47]
	v_cmp_eq_u32_e64 s[46:47], 7, v48
	s_nop 1
	v_cndmask_b32_e64 v55, v55, v7, s[46:47]
	v_cmp_eq_u32_e64 s[46:47], 8, v48
	s_nop 1
	v_cndmask_b32_e64 v55, v55, v0, s[46:47]
	v_cmp_eq_u32_e64 s[46:47], 9, v48
	s_nop 1
	v_cndmask_b32_e64 v55, v55, v1, s[46:47]
	v_cmp_eq_u32_e64 s[46:47], 10, v48
	s_nop 1
	v_cndmask_b32_e64 v55, v55, v2, s[46:47]
	v_cmp_eq_u32_e64 s[46:47], 11, v48
	s_nop 1
	v_cndmask_b32_e64 v55, v55, v3, s[46:47]
	v_cmp_eq_u32_e64 s[46:47], 12, v48
	s_nop 1
	v_cndmask_b32_e64 v55, v55, v8, s[46:47]
	v_cmp_eq_u32_e64 s[46:47], 13, v48
	s_nop 1
	v_cndmask_b32_e64 v55, v55, v9, s[46:47]
	v_cmp_eq_u32_e64 s[46:47], 14, v48
	s_nop 1
	v_cndmask_b32_e64 v55, v55, v4, s[46:47]
	v_cmp_eq_u32_e64 s[46:47], 15, v48
	s_nop 1
	v_cndmask_b32_e64 v55, v55, v5, s[46:47]
	v_cmp_eq_u32_e64 s[46:47], 1, v50
	ds_bpermute_b32 v55, v39, v55
	s_nop 0
	v_cndmask_b32_e64 v57, v12, v13, s[46:47]
	v_cmp_eq_u32_e64 s[46:47], 2, v50
	s_nop 1
	v_cndmask_b32_e64 v57, v57, v14, s[46:47]
	v_cmp_eq_u32_e64 s[46:47], 3, v50
	s_nop 1
	v_cndmask_b32_e64 v57, v57, v15, s[46:47]
	v_cmp_eq_u32_e64 s[46:47], 4, v50
	s_nop 1
	v_cndmask_b32_e64 v57, v57, v10, s[46:47]
	v_cmp_eq_u32_e64 s[46:47], 5, v50
	s_nop 1
	v_cndmask_b32_e64 v57, v57, v11, s[46:47]
	v_cmp_eq_u32_e64 s[46:47], 6, v50
	s_nop 1
	v_cndmask_b32_e64 v57, v57, v6, s[46:47]
	v_cmp_eq_u32_e64 s[46:47], 7, v50
	s_nop 1
	v_cndmask_b32_e64 v7, v57, v7, s[46:47]
	v_cmp_eq_u32_e64 s[46:47], 8, v50
	s_nop 1
	v_cndmask_b32_e64 v7, v7, v0, s[46:47]
	v_cmp_eq_u32_e64 s[46:47], 9, v50
	s_nop 1
	v_cndmask_b32_e64 v7, v7, v1, s[46:47]
	v_cmp_eq_u32_e64 s[46:47], 10, v50
	s_nop 1
	v_cndmask_b32_e64 v7, v7, v2, s[46:47]
	v_cmp_eq_u32_e64 s[46:47], 11, v50
	s_nop 1
	v_cndmask_b32_e64 v7, v7, v3, s[46:47]
	v_cmp_eq_u32_e64 s[46:47], 12, v50
	s_nop 1
	v_cndmask_b32_e64 v7, v7, v8, s[46:47]
	v_cmp_eq_u32_e64 s[46:47], 13, v50
	s_nop 1
	v_cndmask_b32_e64 v7, v7, v9, s[46:47]
	v_cmp_eq_u32_e64 s[46:47], 14, v50
	s_nop 1
	v_cndmask_b32_e64 v7, v7, v4, s[46:47]
	v_cmp_eq_u32_e64 s[46:47], 15, v50
	s_nop 1
	v_cndmask_b32_e64 v7, v7, v5, s[46:47]
	v_cmp_eq_u32_e64 s[46:47], 1, v52
	s_waitcnt lgkmcnt(0)
	v_add_f32_e32 v7, v7, v55
	v_cndmask_b32_e64 v55, v12, v13, s[46:47]
	v_cmp_eq_u32_e64 s[46:47], 2, v52
	s_nop 1
	v_cndmask_b32_e64 v55, v55, v14, s[46:47]
	v_cmp_eq_u32_e64 s[46:47], 3, v52
	s_nop 1
	v_cndmask_b32_e64 v55, v55, v15, s[46:47]
	v_cmp_eq_u32_e64 s[46:47], 4, v52
	s_nop 1
	v_cndmask_b32_e64 v55, v55, v10, s[46:47]
	v_cmp_eq_u32_e64 s[46:47], 5, v52
	s_nop 1
	v_cndmask_b32_e64 v55, v55, v11, s[46:47]
	v_cmp_eq_u32_e64 s[46:47], 6, v52
	s_nop 1
	v_cndmask_b32_e64 v55, v55, v6, s[46:47]
	v_cmp_eq_u32_e64 s[46:47], 7, v52
	s_nop 1
	v_cndmask_b32_e64 v55, v55, v7, s[46:47]
	v_cmp_eq_u32_e64 s[46:47], 8, v52
	s_nop 1
	v_cndmask_b32_e64 v55, v55, v0, s[46:47]
	v_cmp_eq_u32_e64 s[46:47], 9, v52
	s_nop 1
	v_cndmask_b32_e64 v55, v55, v1, s[46:47]
	v_cmp_eq_u32_e64 s[46:47], 10, v52
	s_nop 1
	v_cndmask_b32_e64 v55, v55, v2, s[46:47]
	v_cmp_eq_u32_e64 s[46:47], 11, v52
	s_nop 1
	v_cndmask_b32_e64 v55, v55, v3, s[46:47]
	v_cmp_eq_u32_e64 s[46:47], 12, v52
	s_nop 1
	v_cndmask_b32_e64 v55, v55, v8, s[46:47]
	v_cmp_eq_u32_e64 s[46:47], 13, v52
	s_nop 1
	v_cndmask_b32_e64 v55, v55, v9, s[46:47]
	v_cmp_eq_u32_e64 s[46:47], 14, v52
	s_nop 1
	v_cndmask_b32_e64 v55, v55, v4, s[46:47]
	v_cmp_eq_u32_e64 s[46:47], 15, v52
	s_nop 1
	v_cndmask_b32_e64 v55, v55, v5, s[46:47]
	v_cmp_eq_u32_e64 s[46:47], 1, v54
	ds_bpermute_b32 v55, v37, v55
	s_nop 0
	v_cndmask_b32_e64 v12, v12, v13, s[46:47]
	v_cmp_eq_u32_e64 s[46:47], 2, v54
	s_nop 1
	v_cndmask_b32_e64 v12, v12, v14, s[46:47]
	v_cmp_eq_u32_e64 s[46:47], 3, v54
	s_nop 1
	v_cndmask_b32_e64 v12, v12, v15, s[46:47]
	v_cmp_eq_u32_e64 s[46:47], 4, v54
	s_nop 1
	v_cndmask_b32_e64 v12, v12, v10, s[46:47]
	v_cmp_eq_u32_e64 s[46:47], 5, v54
	s_nop 1
	v_cndmask_b32_e64 v12, v12, v11, s[46:47]
	v_cmp_eq_u32_e64 s[46:47], 6, v54
	s_nop 1
	v_cndmask_b32_e64 v12, v12, v6, s[46:47]
	v_cmp_eq_u32_e64 s[46:47], 7, v54
	s_nop 1
	v_cndmask_b32_e64 v12, v12, v7, s[46:47]
	v_cmp_eq_u32_e64 s[46:47], 8, v54
	s_nop 1
	v_cndmask_b32_e64 v12, v12, v0, s[46:47]
	v_cmp_eq_u32_e64 s[46:47], 9, v54
	s_nop 1
	v_cndmask_b32_e64 v12, v12, v1, s[46:47]
	v_cmp_eq_u32_e64 s[46:47], 10, v54
	s_nop 1
	v_cndmask_b32_e64 v12, v12, v2, s[46:47]
	v_cmp_eq_u32_e64 s[46:47], 11, v54
	s_nop 1
	v_cndmask_b32_e64 v12, v12, v3, s[46:47]
	v_cmp_eq_u32_e64 s[46:47], 12, v54
	s_nop 1
	v_cndmask_b32_e64 v12, v12, v8, s[46:47]
	v_cmp_eq_u32_e64 s[46:47], 13, v54
	s_nop 1
	v_cndmask_b32_e64 v12, v12, v9, s[46:47]
	v_cmp_eq_u32_e64 s[46:47], 14, v54
	s_nop 1
	v_cndmask_b32_e64 v12, v12, v4, s[46:47]
	v_cmp_eq_u32_e64 s[46:47], 15, v54
	s_nop 1
	v_cndmask_b32_e64 v12, v12, v5, s[46:47]
	s_waitcnt lgkmcnt(0)
	v_add_f32_e32 v12, v12, v55
	v_cmp_eq_u32_e64 s[46:47], 1, v56
	s_nop 1
	v_cndmask_b32_e64 v55, v12, v13, s[46:47]
	v_cmp_eq_u32_e64 s[46:47], 2, v56
	s_nop 1
	v_cndmask_b32_e64 v55, v55, v14, s[46:47]
	v_cmp_eq_u32_e64 s[46:47], 3, v56
	s_nop 1
	v_cndmask_b32_e64 v55, v55, v15, s[46:47]
	v_cmp_eq_u32_e64 s[46:47], 4, v56
	s_nop 1
	v_cndmask_b32_e64 v55, v55, v10, s[46:47]
	v_cmp_eq_u32_e64 s[46:47], 5, v56
	s_nop 1
	v_cndmask_b32_e64 v55, v55, v11, s[46:47]
	v_cmp_eq_u32_e64 s[46:47], 6, v56
	s_nop 1
	v_cndmask_b32_e64 v55, v55, v6, s[46:47]
	v_cmp_eq_u32_e64 s[46:47], 7, v56
	s_nop 1
	v_cndmask_b32_e64 v55, v55, v7, s[46:47]
	v_cmp_eq_u32_e64 s[46:47], 8, v56
	s_nop 1
	v_cndmask_b32_e64 v55, v55, v0, s[46:47]
	v_cmp_eq_u32_e64 s[46:47], 9, v56
	s_nop 1
	v_cndmask_b32_e64 v55, v55, v1, s[46:47]
	v_cmp_eq_u32_e64 s[46:47], 10, v56
	s_nop 1
	v_cndmask_b32_e64 v55, v55, v2, s[46:47]
	v_cmp_eq_u32_e64 s[46:47], 11, v56
	s_nop 1
	v_cndmask_b32_e64 v55, v55, v3, s[46:47]
	v_cmp_eq_u32_e64 s[46:47], 12, v56
	s_nop 1
	v_cndmask_b32_e64 v55, v55, v8, s[46:47]
	v_cmp_eq_u32_e64 s[46:47], 13, v56
	s_nop 1
	v_cndmask_b32_e64 v55, v55, v9, s[46:47]
	v_cmp_eq_u32_e64 s[46:47], 14, v56
	s_nop 1
	v_cndmask_b32_e64 v55, v55, v4, s[46:47]
	v_cmp_eq_u32_e64 s[46:47], 15, v56
	s_nop 1
	v_cndmask_b32_e64 v55, v55, v5, s[46:47]
	v_cmp_eq_u32_e64 s[46:47], 1, v58
	ds_bpermute_b32 v55, v37, v55
	s_nop 0
	v_cndmask_b32_e64 v13, v12, v13, s[46:47]
	v_cmp_eq_u32_e64 s[46:47], 2, v58
	s_nop 1
	v_cndmask_b32_e64 v13, v13, v14, s[46:47]
	v_cmp_eq_u32_e64 s[46:47], 3, v58
	s_nop 1
	v_cndmask_b32_e64 v13, v13, v15, s[46:47]
	v_cmp_eq_u32_e64 s[46:47], 4, v58
	s_nop 1
	v_cndmask_b32_e64 v13, v13, v10, s[46:47]
	v_cmp_eq_u32_e64 s[46:47], 5, v58
	s_nop 1
	v_cndmask_b32_e64 v13, v13, v11, s[46:47]
	v_cmp_eq_u32_e64 s[46:47], 6, v58
	s_nop 1
	v_cndmask_b32_e64 v13, v13, v6, s[46:47]
	v_cmp_eq_u32_e64 s[46:47], 7, v58
	s_nop 1
	v_cndmask_b32_e64 v13, v13, v7, s[46:47]
	v_cmp_eq_u32_e64 s[46:47], 8, v58
	s_nop 1
	v_cndmask_b32_e64 v13, v13, v0, s[46:47]
	v_cmp_eq_u32_e64 s[46:47], 9, v58
	s_nop 1
	v_cndmask_b32_e64 v13, v13, v1, s[46:47]
	v_cmp_eq_u32_e64 s[46:47], 10, v58
	s_nop 1
	v_cndmask_b32_e64 v13, v13, v2, s[46:47]
	v_cmp_eq_u32_e64 s[46:47], 11, v58
	s_nop 1
	v_cndmask_b32_e64 v13, v13, v3, s[46:47]
	v_cmp_eq_u32_e64 s[46:47], 12, v58
	s_nop 1
	v_cndmask_b32_e64 v13, v13, v8, s[46:47]
	v_cmp_eq_u32_e64 s[46:47], 13, v58
	s_nop 1
	v_cndmask_b32_e64 v13, v13, v9, s[46:47]
	v_cmp_eq_u32_e64 s[46:47], 14, v58
	s_nop 1
	v_cndmask_b32_e64 v13, v13, v4, s[46:47]
	v_cmp_eq_u32_e64 s[46:47], 15, v58
	s_nop 1
	v_cndmask_b32_e64 v13, v13, v5, s[46:47]
	s_waitcnt lgkmcnt(0)
	v_add_f32_e32 v13, v13, v55
	v_cmp_eq_u32_e64 s[46:47], 1, v60
	s_nop 1
	v_cndmask_b32_e64 v55, v12, v13, s[46:47]
	v_cmp_eq_u32_e64 s[46:47], 2, v60
	s_nop 1
	v_cndmask_b32_e64 v55, v55, v14, s[46:47]
	v_cmp_eq_u32_e64 s[46:47], 3, v60
	s_nop 1
	v_cndmask_b32_e64 v55, v55, v15, s[46:47]
	v_cmp_eq_u32_e64 s[46:47], 4, v60
	s_nop 1
	v_cndmask_b32_e64 v55, v55, v10, s[46:47]
	v_cmp_eq_u32_e64 s[46:47], 5, v60
	s_nop 1
	v_cndmask_b32_e64 v55, v55, v11, s[46:47]
	v_cmp_eq_u32_e64 s[46:47], 6, v60
	s_nop 1
	v_cndmask_b32_e64 v55, v55, v6, s[46:47]
	v_cmp_eq_u32_e64 s[46:47], 7, v60
	s_nop 1
	v_cndmask_b32_e64 v55, v55, v7, s[46:47]
	v_cmp_eq_u32_e64 s[46:47], 8, v60
	s_nop 1
	v_cndmask_b32_e64 v55, v55, v0, s[46:47]
	v_cmp_eq_u32_e64 s[46:47], 9, v60
	s_nop 1
	v_cndmask_b32_e64 v55, v55, v1, s[46:47]
	v_cmp_eq_u32_e64 s[46:47], 10, v60
	s_nop 1
	v_cndmask_b32_e64 v55, v55, v2, s[46:47]
	v_cmp_eq_u32_e64 s[46:47], 11, v60
	s_nop 1
	v_cndmask_b32_e64 v55, v55, v3, s[46:47]
	v_cmp_eq_u32_e64 s[46:47], 12, v60
	s_nop 1
	v_cndmask_b32_e64 v55, v55, v8, s[46:47]
	v_cmp_eq_u32_e64 s[46:47], 13, v60
	s_nop 1
	v_cndmask_b32_e64 v55, v55, v9, s[46:47]
	v_cmp_eq_u32_e64 s[46:47], 14, v60
	s_nop 1
	v_cndmask_b32_e64 v55, v55, v4, s[46:47]
	v_cmp_eq_u32_e64 s[46:47], 15, v60
	s_nop 1
	v_cndmask_b32_e64 v55, v55, v5, s[46:47]
	v_cmp_eq_u32_e64 s[46:47], 1, v62
	ds_bpermute_b32 v55, v37, v55
	s_nop 0
	v_cndmask_b32_e64 v57, v12, v13, s[46:47]
	v_cmp_eq_u32_e64 s[46:47], 2, v62
	s_nop 1
	v_cndmask_b32_e64 v14, v57, v14, s[46:47]
	v_cmp_eq_u32_e64 s[46:47], 3, v62
	s_nop 1
	v_cndmask_b32_e64 v14, v14, v15, s[46:47]
	v_cmp_eq_u32_e64 s[46:47], 4, v62
	s_nop 1
	v_cndmask_b32_e64 v14, v14, v10, s[46:47]
	v_cmp_eq_u32_e64 s[46:47], 5, v62
	s_nop 1
	v_cndmask_b32_e64 v14, v14, v11, s[46:47]
	v_cmp_eq_u32_e64 s[46:47], 6, v62
	s_nop 1
	v_cndmask_b32_e64 v14, v14, v6, s[46:47]
	v_cmp_eq_u32_e64 s[46:47], 7, v62
	s_nop 1
	v_cndmask_b32_e64 v14, v14, v7, s[46:47]
	v_cmp_eq_u32_e64 s[46:47], 8, v62
	s_nop 1
	v_cndmask_b32_e64 v14, v14, v0, s[46:47]
	v_cmp_eq_u32_e64 s[46:47], 9, v62
	s_nop 1
	v_cndmask_b32_e64 v14, v14, v1, s[46:47]
	v_cmp_eq_u32_e64 s[46:47], 10, v62
	s_nop 1
	v_cndmask_b32_e64 v14, v14, v2, s[46:47]
	v_cmp_eq_u32_e64 s[46:47], 11, v62
	s_nop 1
	v_cndmask_b32_e64 v14, v14, v3, s[46:47]
	v_cmp_eq_u32_e64 s[46:47], 12, v62
	s_nop 1
	v_cndmask_b32_e64 v14, v14, v8, s[46:47]
	v_cmp_eq_u32_e64 s[46:47], 13, v62
	s_nop 1
	v_cndmask_b32_e64 v14, v14, v9, s[46:47]
	v_cmp_eq_u32_e64 s[46:47], 14, v62
	s_nop 1
	v_cndmask_b32_e64 v14, v14, v4, s[46:47]
	v_cmp_eq_u32_e64 s[46:47], 15, v62
	s_nop 1
	v_cndmask_b32_e64 v14, v14, v5, s[46:47]
	v_cmp_eq_u32_e64 s[46:47], 1, v64
	s_waitcnt lgkmcnt(0)
	v_add_f32_e32 v14, v14, v55
	v_cndmask_b32_e64 v55, v12, v13, s[46:47]
	v_cmp_eq_u32_e64 s[46:47], 2, v64
	s_nop 1
	v_cndmask_b32_e64 v55, v55, v14, s[46:47]
	v_cmp_eq_u32_e64 s[46:47], 3, v64
	s_nop 1
	v_cndmask_b32_e64 v55, v55, v15, s[46:47]
	v_cmp_eq_u32_e64 s[46:47], 4, v64
	s_nop 1
	v_cndmask_b32_e64 v55, v55, v10, s[46:47]
	v_cmp_eq_u32_e64 s[46:47], 5, v64
	s_nop 1
	v_cndmask_b32_e64 v55, v55, v11, s[46:47]
	v_cmp_eq_u32_e64 s[46:47], 6, v64
	s_nop 1
	v_cndmask_b32_e64 v55, v55, v6, s[46:47]
	v_cmp_eq_u32_e64 s[46:47], 7, v64
	s_nop 1
	v_cndmask_b32_e64 v55, v55, v7, s[46:47]
	v_cmp_eq_u32_e64 s[46:47], 8, v64
	s_nop 1
	v_cndmask_b32_e64 v55, v55, v0, s[46:47]
	v_cmp_eq_u32_e64 s[46:47], 9, v64
	s_nop 1
	v_cndmask_b32_e64 v55, v55, v1, s[46:47]
	v_cmp_eq_u32_e64 s[46:47], 10, v64
	s_nop 1
	v_cndmask_b32_e64 v55, v55, v2, s[46:47]
	v_cmp_eq_u32_e64 s[46:47], 11, v64
	s_nop 1
	v_cndmask_b32_e64 v55, v55, v3, s[46:47]
	v_cmp_eq_u32_e64 s[46:47], 12, v64
	s_nop 1
	v_cndmask_b32_e64 v55, v55, v8, s[46:47]
	v_cmp_eq_u32_e64 s[46:47], 13, v64
	s_nop 1
	v_cndmask_b32_e64 v55, v55, v9, s[46:47]
	v_cmp_eq_u32_e64 s[46:47], 14, v64
	s_nop 1
	v_cndmask_b32_e64 v55, v55, v4, s[46:47]
	v_cmp_eq_u32_e64 s[46:47], 15, v64
	s_nop 1
	v_cndmask_b32_e64 v55, v55, v5, s[46:47]
	v_cmp_eq_u32_e64 s[46:47], 1, v66
	ds_bpermute_b32 v55, v37, v55
	s_nop 0
	v_cndmask_b32_e64 v57, v12, v13, s[46:47]
	v_cmp_eq_u32_e64 s[46:47], 2, v66
	s_nop 1
	v_cndmask_b32_e64 v57, v57, v14, s[46:47]
	v_cmp_eq_u32_e64 s[46:47], 3, v66
	s_nop 1
	v_cndmask_b32_e64 v15, v57, v15, s[46:47]
	v_cmp_eq_u32_e64 s[46:47], 4, v66
	s_nop 1
	v_cndmask_b32_e64 v15, v15, v10, s[46:47]
	v_cmp_eq_u32_e64 s[46:47], 5, v66
	s_nop 1
	v_cndmask_b32_e64 v15, v15, v11, s[46:47]
	v_cmp_eq_u32_e64 s[46:47], 6, v66
	s_nop 1
	v_cndmask_b32_e64 v15, v15, v6, s[46:47]
	v_cmp_eq_u32_e64 s[46:47], 7, v66
	s_nop 1
	v_cndmask_b32_e64 v15, v15, v7, s[46:47]
	v_cmp_eq_u32_e64 s[46:47], 8, v66
	s_nop 1
	v_cndmask_b32_e64 v15, v15, v0, s[46:47]
	v_cmp_eq_u32_e64 s[46:47], 9, v66
	s_nop 1
	v_cndmask_b32_e64 v15, v15, v1, s[46:47]
	v_cmp_eq_u32_e64 s[46:47], 10, v66
	s_nop 1
	v_cndmask_b32_e64 v15, v15, v2, s[46:47]
	v_cmp_eq_u32_e64 s[46:47], 11, v66
	s_nop 1
	v_cndmask_b32_e64 v15, v15, v3, s[46:47]
	v_cmp_eq_u32_e64 s[46:47], 12, v66
	s_nop 1
	v_cndmask_b32_e64 v15, v15, v8, s[46:47]
	v_cmp_eq_u32_e64 s[46:47], 13, v66
	s_nop 1
	v_cndmask_b32_e64 v15, v15, v9, s[46:47]
	v_cmp_eq_u32_e64 s[46:47], 14, v66
	s_nop 1
	v_cndmask_b32_e64 v15, v15, v4, s[46:47]
	v_cmp_eq_u32_e64 s[46:47], 15, v66
	s_nop 1
	v_cndmask_b32_e64 v15, v15, v5, s[46:47]
	v_cmp_eq_u32_e64 s[46:47], 1, v68
	s_waitcnt lgkmcnt(0)
	v_add_f32_e32 v15, v15, v55
	v_cndmask_b32_e64 v55, v12, v13, s[46:47]
	v_cmp_eq_u32_e64 s[46:47], 2, v68
	s_nop 1
	v_cndmask_b32_e64 v55, v55, v14, s[46:47]
	v_cmp_eq_u32_e64 s[46:47], 3, v68
	s_nop 1
	v_cndmask_b32_e64 v55, v55, v15, s[46:47]
	v_cmp_eq_u32_e64 s[46:47], 4, v68
	s_nop 1
	v_cndmask_b32_e64 v55, v55, v10, s[46:47]
	v_cmp_eq_u32_e64 s[46:47], 5, v68
	s_nop 1
	v_cndmask_b32_e64 v55, v55, v11, s[46:47]
	v_cmp_eq_u32_e64 s[46:47], 6, v68
	s_nop 1
	v_cndmask_b32_e64 v55, v55, v6, s[46:47]
	v_cmp_eq_u32_e64 s[46:47], 7, v68
	s_nop 1
	v_cndmask_b32_e64 v55, v55, v7, s[46:47]
	v_cmp_eq_u32_e64 s[46:47], 8, v68
	s_nop 1
	v_cndmask_b32_e64 v55, v55, v0, s[46:47]
	v_cmp_eq_u32_e64 s[46:47], 9, v68
	s_nop 1
	v_cndmask_b32_e64 v55, v55, v1, s[46:47]
	v_cmp_eq_u32_e64 s[46:47], 10, v68
	s_nop 1
	v_cndmask_b32_e64 v55, v55, v2, s[46:47]
	v_cmp_eq_u32_e64 s[46:47], 11, v68
	s_nop 1
	v_cndmask_b32_e64 v55, v55, v3, s[46:47]
	v_cmp_eq_u32_e64 s[46:47], 12, v68
	s_nop 1
	v_cndmask_b32_e64 v55, v55, v8, s[46:47]
	v_cmp_eq_u32_e64 s[46:47], 13, v68
	s_nop 1
	v_cndmask_b32_e64 v55, v55, v9, s[46:47]
	v_cmp_eq_u32_e64 s[46:47], 14, v68
	s_nop 1
	v_cndmask_b32_e64 v55, v55, v4, s[46:47]
	v_cmp_eq_u32_e64 s[46:47], 15, v68
	s_nop 1
	v_cndmask_b32_e64 v55, v55, v5, s[46:47]
	v_cmp_eq_u32_e64 s[46:47], 1, v70
	ds_bpermute_b32 v55, v41, v55
	s_nop 0
	v_cndmask_b32_e64 v12, v12, v13, s[46:47]
	v_cmp_eq_u32_e64 s[46:47], 2, v70
	s_nop 1
	v_cndmask_b32_e64 v12, v12, v14, s[46:47]
	v_cmp_eq_u32_e64 s[46:47], 3, v70
	s_nop 1
	v_cndmask_b32_e64 v12, v12, v15, s[46:47]
	v_cmp_eq_u32_e64 s[46:47], 4, v70
	s_nop 1
	v_cndmask_b32_e64 v12, v12, v10, s[46:47]
	v_cmp_eq_u32_e64 s[46:47], 5, v70
	s_nop 1
	v_cndmask_b32_e64 v12, v12, v11, s[46:47]
	v_cmp_eq_u32_e64 s[46:47], 6, v70
	s_nop 1
	v_cndmask_b32_e64 v12, v12, v6, s[46:47]
	v_cmp_eq_u32_e64 s[46:47], 7, v70
	s_nop 1
	v_cndmask_b32_e64 v12, v12, v7, s[46:47]
	v_cmp_eq_u32_e64 s[46:47], 8, v70
	s_nop 1
	v_cndmask_b32_e64 v12, v12, v0, s[46:47]
	v_cmp_eq_u32_e64 s[46:47], 9, v70
	s_nop 1
	v_cndmask_b32_e64 v12, v12, v1, s[46:47]
	v_cmp_eq_u32_e64 s[46:47], 10, v70
	s_nop 1
	v_cndmask_b32_e64 v12, v12, v2, s[46:47]
	v_cmp_eq_u32_e64 s[46:47], 11, v70
	s_nop 1
	v_cndmask_b32_e64 v12, v12, v3, s[46:47]
	v_cmp_eq_u32_e64 s[46:47], 12, v70
	s_nop 1
	v_cndmask_b32_e64 v12, v12, v8, s[46:47]
	v_cmp_eq_u32_e64 s[46:47], 13, v70
	s_nop 1
	v_cndmask_b32_e64 v12, v12, v9, s[46:47]
	v_cmp_eq_u32_e64 s[46:47], 14, v70
	s_nop 1
	v_cndmask_b32_e64 v12, v12, v4, s[46:47]
	v_cmp_eq_u32_e64 s[46:47], 15, v70
	s_nop 1
	v_cndmask_b32_e64 v12, v12, v5, s[46:47]
	s_waitcnt lgkmcnt(0)
	v_add_f32_e32 v12, v12, v55
	v_cmp_eq_u32_e64 s[46:47], 1, v72
	s_nop 1
	v_cndmask_b32_e64 v55, v12, v13, s[46:47]
	v_cmp_eq_u32_e64 s[46:47], 2, v72
	s_nop 1
	v_cndmask_b32_e64 v55, v55, v14, s[46:47]
	v_cmp_eq_u32_e64 s[46:47], 3, v72
	s_nop 1
	v_cndmask_b32_e64 v55, v55, v15, s[46:47]
	v_cmp_eq_u32_e64 s[46:47], 4, v72
	s_nop 1
	v_cndmask_b32_e64 v55, v55, v10, s[46:47]
	v_cmp_eq_u32_e64 s[46:47], 5, v72
	s_nop 1
	v_cndmask_b32_e64 v55, v55, v11, s[46:47]
	v_cmp_eq_u32_e64 s[46:47], 6, v72
	s_nop 1
	v_cndmask_b32_e64 v55, v55, v6, s[46:47]
	v_cmp_eq_u32_e64 s[46:47], 7, v72
	s_nop 1
	v_cndmask_b32_e64 v55, v55, v7, s[46:47]
	v_cmp_eq_u32_e64 s[46:47], 8, v72
	s_nop 1
	v_cndmask_b32_e64 v55, v55, v0, s[46:47]
	v_cmp_eq_u32_e64 s[46:47], 9, v72
	s_nop 1
	v_cndmask_b32_e64 v55, v55, v1, s[46:47]
	v_cmp_eq_u32_e64 s[46:47], 10, v72
	s_nop 1
	v_cndmask_b32_e64 v55, v55, v2, s[46:47]
	v_cmp_eq_u32_e64 s[46:47], 11, v72
	s_nop 1
	v_cndmask_b32_e64 v55, v55, v3, s[46:47]
	v_cmp_eq_u32_e64 s[46:47], 12, v72
	s_nop 1
	v_cndmask_b32_e64 v55, v55, v8, s[46:47]
	v_cmp_eq_u32_e64 s[46:47], 13, v72
	s_nop 1
	v_cndmask_b32_e64 v55, v55, v9, s[46:47]
	v_cmp_eq_u32_e64 s[46:47], 14, v72
	s_nop 1
	v_cndmask_b32_e64 v55, v55, v4, s[46:47]
	v_cmp_eq_u32_e64 s[46:47], 15, v72
	s_nop 1
	v_cndmask_b32_e64 v55, v55, v5, s[46:47]
	v_cmp_eq_u32_e64 s[46:47], 1, v74
	ds_bpermute_b32 v55, v41, v55
	s_nop 0
	v_cndmask_b32_e64 v13, v12, v13, s[46:47]
	v_cmp_eq_u32_e64 s[46:47], 2, v74
	s_nop 1
	v_cndmask_b32_e64 v13, v13, v14, s[46:47]
	v_cmp_eq_u32_e64 s[46:47], 3, v74
	s_nop 1
	v_cndmask_b32_e64 v13, v13, v15, s[46:47]
	v_cmp_eq_u32_e64 s[46:47], 4, v74
	s_nop 1
	v_cndmask_b32_e64 v13, v13, v10, s[46:47]
	v_cmp_eq_u32_e64 s[46:47], 5, v74
	s_nop 1
	v_cndmask_b32_e64 v13, v13, v11, s[46:47]
	v_cmp_eq_u32_e64 s[46:47], 6, v74
	s_nop 1
	v_cndmask_b32_e64 v13, v13, v6, s[46:47]
	v_cmp_eq_u32_e64 s[46:47], 7, v74
	s_nop 1
	v_cndmask_b32_e64 v13, v13, v7, s[46:47]
	v_cmp_eq_u32_e64 s[46:47], 8, v74
	s_nop 1
	v_cndmask_b32_e64 v13, v13, v0, s[46:47]
	v_cmp_eq_u32_e64 s[46:47], 9, v74
	s_nop 1
	v_cndmask_b32_e64 v13, v13, v1, s[46:47]
	v_cmp_eq_u32_e64 s[46:47], 10, v74
	s_nop 1
	v_cndmask_b32_e64 v13, v13, v2, s[46:47]
	v_cmp_eq_u32_e64 s[46:47], 11, v74
	s_nop 1
	v_cndmask_b32_e64 v13, v13, v3, s[46:47]
	v_cmp_eq_u32_e64 s[46:47], 12, v74
	s_nop 1
	v_cndmask_b32_e64 v13, v13, v8, s[46:47]
	v_cmp_eq_u32_e64 s[46:47], 13, v74
	s_nop 1
	v_cndmask_b32_e64 v13, v13, v9, s[46:47]
	v_cmp_eq_u32_e64 s[46:47], 14, v74
	s_nop 1
	v_cndmask_b32_e64 v13, v13, v4, s[46:47]
	v_cmp_eq_u32_e64 s[46:47], 15, v74
	s_nop 1
	v_cndmask_b32_e64 v13, v13, v5, s[46:47]
	s_waitcnt lgkmcnt(0)
	v_add_f32_e32 v13, v13, v55
	v_cmp_ne_u64_e64 s[46:47], 0, v[76:77]
	s_nop 1
	v_cndmask_b32_e64 v55, v12, v13, s[46:47]
	v_cmp_eq_u32_e64 s[46:47], 2, v76
	s_nop 1
	v_cndmask_b32_e64 v55, v55, v14, s[46:47]
	v_cmp_eq_u32_e64 s[46:47], 3, v76
	s_nop 1
	v_cndmask_b32_e64 v55, v55, v15, s[46:47]
	v_cmp_eq_u32_e64 s[46:47], 4, v76
	s_nop 1
	v_cndmask_b32_e64 v55, v55, v10, s[46:47]
	v_cmp_eq_u32_e64 s[46:47], 5, v76
	s_nop 1
	v_cndmask_b32_e64 v55, v55, v11, s[46:47]
	v_cmp_eq_u32_e64 s[46:47], 6, v76
	s_nop 1
	v_cndmask_b32_e64 v55, v55, v6, s[46:47]
	v_cmp_eq_u32_e64 s[46:47], 7, v76
	s_nop 1
	v_cndmask_b32_e64 v55, v55, v7, s[46:47]
	v_cmp_eq_u32_e64 s[46:47], 8, v76
	s_nop 1
	v_cndmask_b32_e64 v55, v55, v0, s[46:47]
	v_cmp_eq_u32_e64 s[46:47], 9, v76
	s_nop 1
	v_cndmask_b32_e64 v55, v55, v1, s[46:47]
	v_cmp_eq_u32_e64 s[46:47], 10, v76
	s_nop 1
	v_cndmask_b32_e64 v55, v55, v2, s[46:47]
	v_cmp_eq_u32_e64 s[46:47], 11, v76
	s_nop 1
	v_cndmask_b32_e64 v55, v55, v3, s[46:47]
	v_cmp_eq_u32_e64 s[46:47], 12, v76
	s_nop 1
	v_cndmask_b32_e64 v55, v55, v8, s[46:47]
	v_cmp_eq_u32_e64 s[46:47], 13, v76
	s_nop 1
	v_cndmask_b32_e64 v55, v55, v9, s[46:47]
	v_cmp_ne_u64_e64 s[46:47], 0, v[78:79]
	s_nop 1
	v_cndmask_b32_e64 v12, v12, v13, s[46:47]
	v_cmp_eq_u32_e64 s[46:47], 2, v78
	s_nop 1
	v_cndmask_b32_e64 v12, v12, v14, s[46:47]
	v_cmp_eq_u32_e64 s[46:47], 3, v78
	s_nop 1
	v_cndmask_b32_e64 v12, v12, v15, s[46:47]
	v_cmp_eq_u32_e64 s[46:47], 4, v78
	s_nop 1
	v_cndmask_b32_e64 v10, v12, v10, s[46:47]
	v_cmp_eq_u32_e64 s[46:47], 5, v78
	s_nop 1
	v_cndmask_b32_e64 v10, v10, v11, s[46:47]
	v_cmp_eq_u32_e64 s[46:47], 6, v78
	s_nop 1
	v_cndmask_b32_e64 v6, v10, v6, s[46:47]
	v_cmp_eq_u32_e64 s[46:47], 7, v78
	s_nop 1
	v_cndmask_b32_e64 v6, v6, v7, s[46:47]
	v_cmp_eq_u32_e64 s[46:47], 8, v78
	s_nop 1
	v_cndmask_b32_e64 v0, v6, v0, s[46:47]
	v_cmp_eq_u32_e64 s[46:47], 9, v78
	s_nop 1
	v_cndmask_b32_e64 v0, v0, v1, s[46:47]
	v_cmp_eq_u32_e64 s[46:47], 10, v78
	s_nop 1
	v_cndmask_b32_e64 v0, v0, v2, s[46:47]
	v_cmp_eq_u32_e64 s[46:47], 11, v78
	v_fma_f32 v2, -v43, v45, v47
	s_nop 0
	v_cndmask_b32_e64 v0, v0, v3, s[46:47]
	v_cmp_eq_u32_e64 s[46:47], 12, v78
	v_add_f32_e32 v3, v49, v53
	s_nop 0
	v_cndmask_b32_e64 v0, v0, v8, s[46:47]
	v_cmp_eq_u32_e64 s[46:47], 13, v78
	s_nop 1
	v_cndmask_b32_e64 v0, v0, v9, s[46:47]
	v_cmp_eq_u32_e64 s[46:47], 14, v78
	s_nop 1
	v_cndmask_b32_e64 v0, v0, v4, s[46:47]
	v_cmp_eq_u32_e64 s[46:47], 15, v78
	s_nop 1
	v_cndmask_b32_e64 v0, v0, v5, s[46:47]
	ds_bpermute_b32 v0, v35, v0
	v_cmp_eq_u32_e64 s[46:47], 14, v76
	s_nop 1
	v_cndmask_b32_e64 v1, v55, v4, s[46:47]
	v_cmp_eq_u32_e64 s[46:47], 15, v76
	ds_bpermute_b32 v4, v37, v3
	s_nop 0
	v_cndmask_b32_e64 v1, v1, v5, s[46:47]
	s_waitcnt lgkmcnt(1)
	v_add_f32_e32 v0, v1, v0
	ds_bpermute_b32 v1, v33, v0
	s_waitcnt lgkmcnt(0)
	v_add_f32_e32 v5, v0, v1
	ds_bpermute_b32 v6, v31, v5
	v_div_fmas_f32 v0, v2, v29, v45
	v_div_fixup_f32 v8, v0, v27, 1.0
	v_add_f32_e32 v0, v3, v4
	ds_bpermute_b32 v1, v39, v0
	s_waitcnt lgkmcnt(1)
	v_add_f32_e32 v2, v5, v6
	s_nop 0
	v_readlane_b32 s1, v2, 0
	v_readlane_b32 s0, v2, 4
	v_readlane_b32 s8, v2, 32
	v_readlane_b32 s9, v2, 36
	v_pk_mul_f32 v[6:7], v[8:9], s[0:1] op_sel_hi:[0,1]
	v_readlane_b32 s0, v2, 8
	v_cmp_gt_f32_e32 vcc, v6, v7
	v_readlane_b32 s10, v2, 40
	v_mul_f32_e32 v3, s0, v8
	v_readlane_b32 s0, v2, 12
	v_readlane_b32 s11, v2, 44
	v_readlane_b32 s12, v2, 48
	v_mul_f32_e32 v4, s0, v8
	v_readlane_b32 s0, v2, 16
	v_readlane_b32 s13, v2, 52
	v_readlane_b32 s14, v2, 56
	v_mul_f32_e32 v9, s0, v8
	v_readlane_b32 s0, v2, 20
	v_readlane_b32 s15, v2, 60
	v_cndmask_b32_e64 v12, 0, 1, vcc
	v_mul_f32_e32 v10, s0, v8
	v_readlane_b32 s0, v2, 24
	v_cmp_lt_f32_e64 s[52:53], s33, v7
	s_nop 0
	v_mul_f32_e32 v11, s0, v8
	v_readlane_b32 s0, v2, 28
	v_cndmask_b32_e32 v2, v7, v6, vcc
	v_cmp_gt_f32_e32 vcc, v3, v2
	v_mul_f32_e32 v5, s0, v8
	s_nop 0
	v_cndmask_b32_e32 v2, v2, v3, vcc
	v_cndmask_b32_e64 v12, v12, 2, vcc
	v_cmp_gt_f32_e32 vcc, v4, v2
	s_nop 1
	v_cndmask_b32_e32 v2, v2, v4, vcc
	v_cndmask_b32_e64 v12, v12, 3, vcc
	v_cmp_gt_f32_e32 vcc, v9, v2
	s_nop 1
	v_cndmask_b32_e32 v2, v2, v9, vcc
	v_cndmask_b32_e64 v12, v12, 4, vcc
	v_cmp_gt_f32_e32 vcc, v10, v2
	s_nop 1
	v_cndmask_b32_e32 v2, v2, v10, vcc
	v_cndmask_b32_e64 v12, v12, 5, vcc
	v_cmp_ngt_f32_e32 vcc, v11, v2
	s_nop 1
	v_cndmask_b32_e32 v2, v11, v2, vcc
	v_cndmask_b32_e32 v12, 6, v12, vcc
	v_cmp_gt_f32_e64 s[48:49], v5, v2
	s_or_b64 s[0:1], vcc, s[48:49]
	v_cmp_ngt_f32_e64 s[46:47], v5, v2
	v_cndmask_b32_e64 v172, v12, 7, s[48:49]
	v_cmp_ne_u32_e64 s[50:51], 0, v172
	s_and_b64 s[50:51], s[50:51], s[52:53]
	s_nop 0
	v_cndmask_b32_e64 v7, v196, v7, s[50:51]
	v_cmp_ne_u32_e64 s[50:51], 1, v172
	v_cmp_gt_f32_e64 s[52:53], v6, v7
	s_and_b64 s[50:51], s[50:51], s[52:53]
	v_cndmask_b32_e64 v6, v7, v6, s[50:51]
	v_cndmask_b32_e64 v7, 0, 1, s[50:51]
	v_cmp_ne_u32_e64 s[50:51], 2, v172
	v_cmp_gt_f32_e64 s[52:53], v3, v6
	s_and_b64 s[50:51], s[50:51], s[52:53]
	v_cndmask_b32_e64 v3, v6, v3, s[50:51]
	v_cndmask_b32_e64 v6, v7, 2, s[50:51]
	v_cmp_ne_u32_e64 s[50:51], 3, v172
	v_cmp_gt_f32_e64 s[52:53], v4, v3
	s_and_b64 s[50:51], s[50:51], s[52:53]
	v_cndmask_b32_e64 v3, v3, v4, s[50:51]
	v_cndmask_b32_e64 v4, v6, 3, s[50:51]
	v_cmp_ne_u32_e64 s[50:51], 4, v172
	v_cmp_gt_f32_e64 s[52:53], v9, v3
	s_and_b64 s[50:51], s[50:51], s[52:53]
	v_cndmask_b32_e64 v3, v3, v9, s[50:51]
	v_cndmask_b32_e64 v4, v4, 4, s[50:51]
	v_cmp_ne_u32_e64 s[50:51], 5, v172
	v_cmp_gt_f32_e64 s[52:53], v10, v3
	s_and_b64 s[50:51], s[50:51], s[52:53]
	v_cndmask_b32_e64 v3, v3, v10, s[50:51]
	v_cmp_gt_f32_e32 vcc, v11, v3
	v_cndmask_b32_e64 v4, v4, 5, s[50:51]
	s_and_b64 vcc, s[0:1], vcc
	v_cndmask_b32_e32 v43, v3, v11, vcc
	v_cndmask_b32_e64 v9, v4, 6, vcc
	s_and_saveexec_b64 s[0:1], s[46:47]
	s_cbranch_execz .LBB0_1340
	v_cmp_gt_f32_e32 vcc, v5, v43
	s_and_saveexec_b64 s[2:3], vcc
	v_mov_b32_e32 v9, 7
	v_mov_b32_e32 v43, v5
	s_or_b64 exec, exec, s[2:3]
	v_mov_b32_e32 v5, v2
